# v15 + 40 exact-duplicate s_waitcnt lgkmcnt(0) removed from the GEMM K-loop MFMA heads
# baseline (speedup 1.0000x reference)
; #define PG8_STAGE(bufoff, gbase, v0, v1) do { \
;         __builtin_amdgcn_global_load_lds((const unsigned*)((const char*)(gbase) + (v0)), (LAS unsigned*)(lds + (bufoff) + ldsw), 16, 0, 0); \
;         __builtin_amdgcn_global_load_lds((const unsigned*)((const char*)(gbase) + (v1)), (LAS unsigned*)(lds + (bufoff) + ldsw + 8192), 16, 0, 0); } while (0)
; #define PG8_LDA(dst, b, h) do { _Pragma("unroll") for (int m = 0; m < 4; ++m) _Pragma("unroll") for (int k = 0; k < 2; ++k) dst[m][k] = *(const LAS bf16x8*)(lds + PG8_SA(b, h) + aoff + m * 2048 + k * 1024); } while (0)
; #define PG8_LDB(dst, b, h) do { _Pragma("unroll") for (int n = 0; n < 2; ++n) _Pragma("unroll") for (int k = 0; k < 2; ++k) dst[n][k] = *(const LAS bf16x8*)(lds + PG8_SB(b, h) + boff + n * 2048 + k * 1024); } while (0)
; #define PG8_MMA(ai, bj, At, Bt) do { __builtin_amdgcn_s_setprio(1); _Pragma("unroll") for (int m = 0; m < 4; ++m) _Pragma("unroll") for (int n = 0; n < 2; ++n) _Pragma("unroll") for (int k = 0; k < 2; ++k) \
;         acc[ai][bj][m][n] = __builtin_amdgcn_mfma_f32_16x16x32_bf16(Bt[n][k], At[m][k], acc[ai][bj][m][n], 0, 0, 0); __builtin_amdgcn_s_setprio(0); } while (0)
; #define PG8_WAIT_V(n) asm volatile("s_waitcnt vmcnt(" #n ")" ::: "memory")
; #define PG8_WAIT_L(n) asm volatile("s_waitcnt lgkmcnt(" #n ")" ::: "memory")
; #define PG8_BAR __builtin_amdgcn_s_barrier()
; template <class Epi, class Sched>
; __device__ __forceinline__ void gemm_phase(LAS unsigned char* lds, const int K, const Sched& S, const Epi& E) {
;     ...
;             PG8_LDB(B0, 0, 0); PG8_SCHED; PG8_LDA(At, 0, 0); PG8_STAGE(PG8_SA(1, 1), a1, c10, c11);
;             PG8_WAIT_L(8); PG8_BAR; PG8_WAIT_L(0); PG8_MMA(0, 0, At, B0); PG8_BAR; PG8_SCHED;
;             PG8_LDB(B1, 0, 1); PG8_STAGE(PG8_SB(0, 0), b2, voffB0, voffB1);
;             PG8_BAR; PG8_WAIT_L(0); PG8_MMA(0, 1, At, B1); PG8_BAR;
;             PG8_LDA(At, 0, 1); PG8_STAGE(PG8_SA(0, 0), a2, x00, x01);
;             PG8_BAR; PG8_WAIT_L(0); PG8_MMA(1, 0, At, B0); PG8_BAR; PG8_SCHED;
;             PG8_STAGE(PG8_SB(0, 1), b2 + hstep, voffB0, voffB1);
;             PG8_WAIT_V(6); PG8_BAR; PG8_MMA(1, 1, At, B1); PG8_BAR;
;             PG8_LDB(B0, 1, 0); PG8_SCHED; PG8_LDA(At, 1, 0); PG8_STAGE(PG8_SA(0, 1), a2, x10, x11);
;             PG8_WAIT_L(8); PG8_BAR; PG8_WAIT_L(0); PG8_MMA(0, 0, At, B0); PG8_BAR; PG8_SCHED;
.LBB0_246:
	s_add_u32 s22, s4, s20
	s_addc_u32 s23, s5, s21
	s_add_u32 s24, s22, 0x34c30100
	ds_read_b128 v[166:169], v158
	ds_read_b128 v[170:173], v158 offset:1024
	ds_read_b128 v[174:177], v158 offset:2048
	ds_read_b128 v[178:181], v158 offset:3072
	s_addc_u32 s25, s23, 0
	s_add_u32 s47, s19, s20
	s_addc_u32 s48, s45, s21
	s_cmpk_eq_i32 s20, 0xf00
	s_cselect_b64 vcc, -1, 0
	s_and_b64 s[22:23], vcc, exec
	v_cndmask_b32_e32 v134, v141, v161, vcc
	s_cselect_b32 s25, s7, s25
	s_cselect_b32 s24, s6, s24
	v_cndmask_b32_e32 v143, v142, v163, vcc
	s_cselect_b32 s23, s3, s48
	s_cselect_b32 s22, s2, s47
	v_cndmask_b32_e32 v206, v140, v162, vcc
	s_mov_b32 m0, s40
	v_lshl_add_u64 v[216:217], v[148:149], 0, s[20:21]
	ds_read_b128 v[182:185], v159
	ds_read_b128 v[186:189], v159 offset:1024
	ds_read_b128 v[190:193], v159 offset:2048
	ds_read_b128 v[194:197], v159 offset:3072
	ds_read_b128 v[198:201], v159 offset:4096
	ds_read_b128 v[202:205], v159 offset:5120
	ds_read_b128 v[208:211], v159 offset:6144
	ds_read_b128 v[212:215], v159 offset:7168
	global_load_lds_dwordx4 v[216:217], off
	v_lshl_add_u64 v[216:217], v[146:147], 0, s[20:21]
	s_add_i32 m0, s29, 0xe000
	s_nop 0
	global_load_lds_dwordx4 v[216:217], off
	s_waitcnt lgkmcnt(8)
	s_barrier
	s_waitcnt lgkmcnt(0)
	s_setprio 1
	v_mfma_f32_16x16x32_bf16 v[126:129], v[166:169], v[182:185], v[126:129]
	v_mfma_f32_16x16x32_bf16 v[122:125], v[174:177], v[182:185], v[122:125]
	v_mfma_f32_16x16x32_bf16 v[118:121], v[166:169], v[190:193], v[118:121]
	v_mfma_f32_16x16x32_bf16 v[110:113], v[174:177], v[190:193], v[110:113]
	v_mfma_f32_16x16x32_bf16 v[102:105], v[166:169], v[198:201], v[102:105]
	v_mfma_f32_16x16x32_bf16 v[94:97], v[174:177], v[198:201], v[94:97]
	v_mfma_f32_16x16x32_bf16 v[86:89], v[166:169], v[208:211], v[86:89]
	v_mfma_f32_16x16x32_bf16 v[78:81], v[174:177], v[208:211], v[78:81]
	v_mfma_f32_16x16x32_bf16 v[126:129], v[170:173], v[186:189], v[126:129]
	v_mfma_f32_16x16x32_bf16 v[122:125], v[178:181], v[186:189], v[122:125]
	v_mfma_f32_16x16x32_bf16 v[118:121], v[170:173], v[194:197], v[118:121]
	v_mfma_f32_16x16x32_bf16 v[110:113], v[178:181], v[194:197], v[110:113]
	v_mfma_f32_16x16x32_bf16 v[102:105], v[170:173], v[202:205], v[102:105]
	v_mfma_f32_16x16x32_bf16 v[94:97], v[178:181], v[202:205], v[94:97]
	v_mfma_f32_16x16x32_bf16 v[86:89], v[170:173], v[212:215], v[86:89]
	v_mfma_f32_16x16x32_bf16 v[78:81], v[178:181], v[212:215], v[78:81]
	s_setprio 0
	s_barrier
	s_add_i32 s47, s37, s27
	v_lshl_add_u64 v[232:233], s[22:23], 0, v[132:133]
	s_mov_b32 m0, s47
	ds_read_b128 v[216:219], v160
	ds_read_b128 v[220:223], v160 offset:1024
	ds_read_b128 v[224:227], v160 offset:2048
	ds_read_b128 v[228:231], v160 offset:3072
	global_load_lds_dwordx4 v[232:233], off
	v_lshl_add_u64 v[234:235], s[22:23], 0, v[130:131]
	s_add_i32 m0, s47, 0x2000
	s_nop 0
	global_load_lds_dwordx4 v[234:235], off
	s_barrier
	s_waitcnt lgkmcnt(0)
	s_setprio 1
	v_mfma_f32_16x16x32_bf16 v[114:117], v[216:219], v[182:185], v[114:117]
	v_mfma_f32_16x16x32_bf16 v[106:109], v[224:227], v[182:185], v[106:109]
	v_mfma_f32_16x16x32_bf16 v[98:101], v[216:219], v[190:193], v[98:101]
	v_mfma_f32_16x16x32_bf16 v[90:93], v[224:227], v[190:193], v[90:93]
	v_mfma_f32_16x16x32_bf16 v[82:85], v[216:219], v[198:201], v[82:85]
	v_mfma_f32_16x16x32_bf16 v[74:77], v[224:227], v[198:201], v[74:77]
	v_mfma_f32_16x16x32_bf16 v[70:73], v[216:219], v[208:211], v[70:73]
	v_mfma_f32_16x16x32_bf16 v[66:69], v[224:227], v[208:211], v[66:69]
	v_mfma_f32_16x16x32_bf16 v[114:117], v[220:223], v[186:189], v[114:117]
	v_mfma_f32_16x16x32_bf16 v[106:109], v[228:231], v[186:189], v[106:109]
	v_mfma_f32_16x16x32_bf16 v[98:101], v[220:223], v[194:197], v[98:101]
	v_mfma_f32_16x16x32_bf16 v[90:93], v[228:231], v[194:197], v[90:93]
	v_mfma_f32_16x16x32_bf16 v[82:85], v[220:223], v[202:205], v[82:85]
	v_mfma_f32_16x16x32_bf16 v[74:77], v[228:231], v[202:205], v[74:77]
	v_mfma_f32_16x16x32_bf16 v[70:73], v[220:223], v[212:215], v[70:73]
	v_mfma_f32_16x16x32_bf16 v[66:69], v[228:231], v[212:215], v[66:69]
	s_setprio 0
	s_mov_b32 m0, s29
	s_barrier
	ds_read_b128 v[182:185], v159 offset:16384
	ds_read_b128 v[186:189], v159 offset:17408
	ds_read_b128 v[190:193], v159 offset:18432
	ds_read_b128 v[194:197], v159 offset:19456
	ds_read_b128 v[198:201], v159 offset:20480
	ds_read_b128 v[202:205], v159 offset:21504
	ds_read_b128 v[208:211], v159 offset:22528
	ds_read_b128 v[212:215], v159 offset:23552
	global_load_lds_dwordx4 v134, s[24:25]
	s_mov_b32 m0, s30
	v_mov_b32_e32 v207, v135
	global_load_lds_dwordx4 v206, s[24:25]
	s_barrier
	s_waitcnt lgkmcnt(0)
	v_lshl_add_u64 v[236:237], s[24:25], 0, v[134:135]
	v_lshl_add_u64 v[206:207], s[24:25], 0, v[206:207]
	s_setprio 1
	s_waitcnt lgkmcnt(0)
	v_mfma_f32_16x16x32_bf16 v[62:65], v[166:169], v[182:185], v[62:65]
	v_mfma_f32_16x16x32_bf16 v[58:61], v[174:177], v[182:185], v[58:61]
	v_mfma_f32_16x16x32_bf16 v[54:57], v[166:169], v[190:193], v[54:57]
	v_mfma_f32_16x16x32_bf16 v[46:49], v[174:177], v[190:193], v[46:49]
	v_mfma_f32_16x16x32_bf16 v[38:41], v[166:169], v[198:201], v[38:41]
	v_mfma_f32_16x16x32_bf16 v[30:33], v[174:177], v[198:201], v[30:33]
	v_mfma_f32_16x16x32_bf16 v[22:25], v[166:169], v[208:211], v[22:25]
	v_mfma_f32_16x16x32_bf16 v[14:17], v[174:177], v[208:211], v[14:17]
	v_mfma_f32_16x16x32_bf16 v[62:65], v[170:173], v[186:189], v[62:65]
	v_mfma_f32_16x16x32_bf16 v[58:61], v[178:181], v[186:189], v[58:61]
	v_mfma_f32_16x16x32_bf16 v[54:57], v[170:173], v[194:197], v[54:57]
	v_mfma_f32_16x16x32_bf16 v[46:49], v[178:181], v[194:197], v[46:49]
	v_mfma_f32_16x16x32_bf16 v[38:41], v[170:173], v[202:205], v[38:41]
	v_mfma_f32_16x16x32_bf16 v[30:33], v[178:181], v[202:205], v[30:33]
	v_mfma_f32_16x16x32_bf16 v[22:25], v[170:173], v[212:215], v[22:25]
	v_mfma_f32_16x16x32_bf16 v[14:17], v[178:181], v[212:215], v[14:17]
	s_setprio 0
	s_barrier
; #define PG8_STAGE(bufoff, gbase, v0, v1) do { \
;         __builtin_amdgcn_global_load_lds((const unsigned*)((const char*)(gbase) + (v0)), (LAS unsigned*)(lds + (bufoff) + ldsw), 16, 0, 0); \
;         __builtin_amdgcn_global_load_lds((const unsigned*)((const char*)(gbase) + (v1)), (LAS unsigned*)(lds + (bufoff) + ldsw + 8192), 16, 0, 0); } while (0)
; #define PG8_LDA(dst, b, h) do { _Pragma("unroll") for (int m = 0; m < 4; ++m) _Pragma("unroll") for (int k = 0; k < 2; ++k) dst[m][k] = *(const LAS bf16x8*)(lds + PG8_SA(b, h) + aoff + m * 2048 + k * 1024); } while (0)
; #define PG8_LDB(dst, b, h) do { _Pragma("unroll") for (int n = 0; n < 2; ++n) _Pragma("unroll") for (int k = 0; k < 2; ++k) dst[n][k] = *(const LAS bf16x8*)(lds + PG8_SB(b, h) + boff + n * 2048 + k * 1024); } while (0)
; #define PG8_MMA(ai, bj, At, Bt) do { __builtin_amdgcn_s_setprio(1); _Pragma("unroll") for (int m = 0; m < 4; ++m) _Pragma("unroll") for (int n = 0; n < 2; ++n) _Pragma("unroll") for (int k = 0; k < 2; ++k) \
;         acc[ai][bj][m][n] = __builtin_amdgcn_mfma_f32_16x16x32_bf16(Bt[n][k], At[m][k], acc[ai][bj][m][n], 0, 0, 0); __builtin_amdgcn_s_setprio(0); } while (0)
; #define PG8_WAIT_V(n) asm volatile("s_waitcnt vmcnt(" #n ")" ::: "memory")
; #define PG8_WAIT_L(n) asm volatile("s_waitcnt lgkmcnt(" #n ")" ::: "memory")
; #define PG8_BAR __builtin_amdgcn_s_barrier()
; #define PG8_SCHED __builtin_amdgcn_sched_barrier(0)
; template <class Epi, class Sched>
; __device__ __forceinline__ void gemm_phase(LAS unsigned char* lds, const int K, const Sched& S, const Epi& E) {
;     ...
;             PG8_BAR; PG8_WAIT_L(0); PG8_MMA(0, 1, At, B1); PG8_BAR;
;             PG8_LDA(At, 0, 1); PG8_STAGE(PG8_SA(0, 0), a2, x00, x01);
;             PG8_BAR; PG8_WAIT_L(0); PG8_MMA(1, 0, At, B0); PG8_BAR; PG8_SCHED;
;             PG8_STAGE(PG8_SB(0, 1), b2 + hstep, voffB0, voffB1);
;             PG8_WAIT_V(6); PG8_BAR; PG8_MMA(1, 1, At, B1); PG8_BAR;
;             PG8_LDB(B0, 1, 0); PG8_SCHED; PG8_LDA(At, 1, 0); PG8_STAGE(PG8_SA(0, 1), a2, x10, x11);
;             PG8_WAIT_L(8); PG8_BAR; PG8_WAIT_L(0); PG8_MMA(0, 0, At, B0); PG8_BAR; PG8_SCHED;
;             PG8_LDB(B1, 1, 1); PG8_STAGE(PG8_SB(1, 0), b3, voffB0, voffB1);
;             PG8_BAR; PG8_WAIT_L(0); PG8_MMA(0, 1, At, B1); PG8_BAR;
;             PG8_LDA(At, 1, 1); PG8_STAGE(PG8_SA(1, 0), a3, x00, x01);
	s_add_u32 s48, s22, 0x80000
	s_addc_u32 s49, s23, 0
	s_add_i32 s47, s38, s27
	v_lshl_add_u64 v[166:167], s[48:49], 0, v[132:133]
	s_mov_b32 m0, s47
	s_nop 0
	global_load_lds_dwordx4 v[166:167], off
	v_lshl_add_u64 v[166:167], s[48:49], 0, v[130:131]
	s_add_i32 m0, s47, 0x2000
	s_nop 0
	global_load_lds_dwordx4 v[166:167], off
	s_waitcnt vmcnt(6)
	s_barrier
	s_setprio 1
	v_mfma_f32_16x16x32_bf16 v[50:53], v[216:219], v[182:185], v[50:53]
	v_mfma_f32_16x16x32_bf16 v[42:45], v[224:227], v[182:185], v[42:45]
	v_mfma_f32_16x16x32_bf16 v[34:37], v[216:219], v[190:193], v[34:37]
	v_mfma_f32_16x16x32_bf16 v[26:29], v[224:227], v[190:193], v[26:29]
	v_mfma_f32_16x16x32_bf16 v[18:21], v[216:219], v[198:201], v[18:21]
	v_mfma_f32_16x16x32_bf16 v[10:13], v[224:227], v[198:201], v[10:13]
	v_mfma_f32_16x16x32_bf16 v[6:9], v[216:219], v[208:211], v[6:9]
	v_mfma_f32_16x16x32_bf16 v[2:5], v[224:227], v[208:211], v[2:5]
	v_mfma_f32_16x16x32_bf16 v[50:53], v[220:223], v[186:189], v[50:53]
	v_mfma_f32_16x16x32_bf16 v[42:45], v[228:231], v[186:189], v[42:45]
	v_mfma_f32_16x16x32_bf16 v[34:37], v[220:223], v[194:197], v[34:37]
	v_mfma_f32_16x16x32_bf16 v[26:29], v[228:231], v[194:197], v[26:29]
	v_mfma_f32_16x16x32_bf16 v[18:21], v[220:223], v[202:205], v[18:21]
	v_mfma_f32_16x16x32_bf16 v[10:13], v[228:231], v[202:205], v[10:13]
	v_mfma_f32_16x16x32_bf16 v[6:9], v[220:223], v[212:215], v[6:9]
	v_mfma_f32_16x16x32_bf16 v[2:5], v[228:231], v[212:215], v[2:5]
	s_setprio 0
	s_add_i32 s47, 0, 0x18000
	v_add_u32_e32 v134, s47, v156
	s_barrier
	ds_read_b128 v[166:169], v134
	ds_read_b128 v[170:173], v134 offset:1024
	ds_read_b128 v[174:177], v134 offset:2048
	ds_read_b128 v[178:181], v134 offset:3072
	s_mov_b32 m0, s31
	ds_read_b128 v[182:185], v159 offset:32768
	ds_read_b128 v[186:189], v159 offset:33792
	ds_read_b128 v[190:193], v159 offset:34816
	ds_read_b128 v[194:197], v159 offset:35840
	ds_read_b128 v[198:201], v159 offset:36864
	ds_read_b128 v[202:205], v159 offset:37888
	ds_read_b128 v[208:211], v159 offset:38912
	ds_read_b128 v[212:215], v159 offset:39936
	v_cndmask_b32_e32 v134, v144, v164, vcc
	global_load_lds_dwordx4 v143, s[24:25]
	s_mov_b32 m0, s33
	s_nop 0
	global_load_lds_dwordx4 v134, s[24:25]
	s_waitcnt lgkmcnt(8)
	s_barrier
	s_waitcnt lgkmcnt(0)
	s_setprio 1
	v_mfma_f32_16x16x32_bf16 v[126:129], v[166:169], v[182:185], v[126:129]
	v_mfma_f32_16x16x32_bf16 v[122:125], v[174:177], v[182:185], v[122:125]
	v_mfma_f32_16x16x32_bf16 v[118:121], v[166:169], v[190:193], v[118:121]
	v_mfma_f32_16x16x32_bf16 v[110:113], v[174:177], v[190:193], v[110:113]
	v_mfma_f32_16x16x32_bf16 v[102:105], v[166:169], v[198:201], v[102:105]
	v_mfma_f32_16x16x32_bf16 v[94:97], v[174:177], v[198:201], v[94:97]
	v_mfma_f32_16x16x32_bf16 v[86:89], v[166:169], v[208:211], v[86:89]
	v_mfma_f32_16x16x32_bf16 v[78:81], v[174:177], v[208:211], v[78:81]
	v_mfma_f32_16x16x32_bf16 v[126:129], v[170:173], v[186:189], v[126:129]
	v_mfma_f32_16x16x32_bf16 v[122:125], v[178:181], v[186:189], v[122:125]
	v_mfma_f32_16x16x32_bf16 v[118:121], v[170:173], v[194:197], v[118:121]
	v_mfma_f32_16x16x32_bf16 v[110:113], v[178:181], v[194:197], v[110:113]
	v_mfma_f32_16x16x32_bf16 v[102:105], v[170:173], v[202:205], v[102:105]
	v_mfma_f32_16x16x32_bf16 v[94:97], v[178:181], v[202:205], v[94:97]
	v_mfma_f32_16x16x32_bf16 v[86:89], v[170:173], v[212:215], v[86:89]
	v_mfma_f32_16x16x32_bf16 v[78:81], v[178:181], v[212:215], v[78:81]
	s_setprio 0
	s_barrier
	s_add_i32 s24, 0, 0x1c000
	s_add_i32 s25, s47, s27
	v_add_u32_e32 v134, s24, v156
	v_lshl_add_u64 v[232:233], v[232:233], 0, s[14:15]
	s_mov_b32 m0, s25
	ds_read_b128 v[216:219], v134
	ds_read_b128 v[220:223], v134 offset:1024
	ds_read_b128 v[224:227], v134 offset:2048
	ds_read_b128 v[228:231], v134 offset:3072
	global_load_lds_dwordx4 v[232:233], off
	v_lshl_add_u64 v[232:233], v[234:235], 0, s[14:15]
	s_add_i32 m0, s25, 0x2000
	s_nop 0
	global_load_lds_dwordx4 v[232:233], off
	s_barrier
	s_waitcnt lgkmcnt(0)
	s_setprio 1
	v_mfma_f32_16x16x32_bf16 v[114:117], v[216:219], v[182:185], v[114:117]
	v_mfma_f32_16x16x32_bf16 v[106:109], v[224:227], v[182:185], v[106:109]
	v_mfma_f32_16x16x32_bf16 v[98:101], v[216:219], v[190:193], v[98:101]
	v_mfma_f32_16x16x32_bf16 v[90:93], v[224:227], v[190:193], v[90:93]
	v_mfma_f32_16x16x32_bf16 v[82:85], v[216:219], v[198:201], v[82:85]
	v_mfma_f32_16x16x32_bf16 v[74:77], v[224:227], v[198:201], v[74:77]
	v_mfma_f32_16x16x32_bf16 v[70:73], v[216:219], v[208:211], v[70:73]
	v_mfma_f32_16x16x32_bf16 v[66:69], v[224:227], v[208:211], v[66:69]
	v_mfma_f32_16x16x32_bf16 v[114:117], v[220:223], v[186:189], v[114:117]
	v_mfma_f32_16x16x32_bf16 v[106:109], v[228:231], v[186:189], v[106:109]
	v_mfma_f32_16x16x32_bf16 v[98:101], v[220:223], v[194:197], v[98:101]
	v_mfma_f32_16x16x32_bf16 v[90:93], v[228:231], v[194:197], v[90:93]
	v_mfma_f32_16x16x32_bf16 v[82:85], v[220:223], v[202:205], v[82:85]
	v_mfma_f32_16x16x32_bf16 v[74:77], v[228:231], v[202:205], v[74:77]
	v_mfma_f32_16x16x32_bf16 v[70:73], v[220:223], v[212:215], v[70:73]
	v_mfma_f32_16x16x32_bf16 v[66:69], v[228:231], v[212:215], v[66:69]
	s_setprio 0
	s_mov_b32 m0, s35
	v_lshl_add_u64 v[232:233], v[236:237], 0, s[14:15]
	s_barrier
	ds_read_b128 v[182:185], v159 offset:49152
	ds_read_b128 v[186:189], v159 offset:50176
	ds_read_b128 v[190:193], v159 offset:51200
	ds_read_b128 v[194:197], v159 offset:52224
	ds_read_b128 v[198:201], v159 offset:53248
	ds_read_b128 v[202:205], v159 offset:54272
	ds_read_b128 v[208:211], v159 offset:55296
	ds_read_b128 v[212:215], v159 offset:56320
	global_load_lds_dwordx4 v[232:233], off
	v_lshl_add_u64 v[206:207], v[206:207], 0, s[14:15]
	s_mov_b32 m0, s36
	s_nop 0
	global_load_lds_dwordx4 v[206:207], off
	s_barrier
; #define PG8_STAGE(bufoff, gbase, v0, v1) do { \
;         __builtin_amdgcn_global_load_lds((const unsigned*)((const char*)(gbase) + (v0)), (LAS unsigned*)(lds + (bufoff) + ldsw), 16, 0, 0); \
;         __builtin_amdgcn_global_load_lds((const unsigned*)((const char*)(gbase) + (v1)), (LAS unsigned*)(lds + (bufoff) + ldsw + 8192), 16, 0, 0); } while (0)
; #define PG8_MMA(ai, bj, At, Bt) do { __builtin_amdgcn_s_setprio(1); _Pragma("unroll") for (int m = 0; m < 4; ++m) _Pragma("unroll") for (int n = 0; n < 2; ++n) _Pragma("unroll") for (int k = 0; k < 2; ++k) \
;         acc[ai][bj][m][n] = __builtin_amdgcn_mfma_f32_16x16x32_bf16(Bt[n][k], At[m][k], acc[ai][bj][m][n], 0, 0, 0); __builtin_amdgcn_s_setprio(0); } while (0)
; #define PG8_WAIT_V(n) asm volatile("s_waitcnt vmcnt(" #n ")" ::: "memory")
; #define PG8_WAIT_L(n) asm volatile("s_waitcnt lgkmcnt(" #n ")" ::: "memory")
; #define PG8_BAR __builtin_amdgcn_s_barrier()
; #define PG8_SCHED __builtin_amdgcn_sched_barrier(0)
; template <class Epi, class Sched>
; __device__ __forceinline__ void gemm_phase(LAS unsigned char* lds, const int K, const Sched& S, const Epi& E) {
;     ...
;             PG8_BAR; PG8_WAIT_L(0); PG8_MMA(1, 0, At, B0); PG8_BAR; PG8_SCHED;
;             PG8_STAGE(PG8_SB(1, 1), b3 + hstep, voffB0, voffB1);
;             PG8_WAIT_V(6); PG8_BAR; PG8_MMA(1, 1, At, B1); PG8_BAR;
	s_waitcnt lgkmcnt(0)
	s_setprio 1
	v_mfma_f32_16x16x32_bf16 v[62:65], v[166:169], v[182:185], v[62:65]
	v_mfma_f32_16x16x32_bf16 v[58:61], v[174:177], v[182:185], v[58:61]
	v_mfma_f32_16x16x32_bf16 v[54:57], v[166:169], v[190:193], v[54:57]
	v_mfma_f32_16x16x32_bf16 v[46:49], v[174:177], v[190:193], v[46:49]
	v_mfma_f32_16x16x32_bf16 v[38:41], v[166:169], v[198:201], v[38:41]
	v_mfma_f32_16x16x32_bf16 v[30:33], v[174:177], v[198:201], v[30:33]
	v_mfma_f32_16x16x32_bf16 v[22:25], v[166:169], v[208:211], v[22:25]
	v_mfma_f32_16x16x32_bf16 v[14:17], v[174:177], v[208:211], v[14:17]
	v_mfma_f32_16x16x32_bf16 v[62:65], v[170:173], v[186:189], v[62:65]
	v_mfma_f32_16x16x32_bf16 v[58:61], v[178:181], v[186:189], v[58:61]
	v_mfma_f32_16x16x32_bf16 v[54:57], v[170:173], v[194:197], v[54:57]
	v_mfma_f32_16x16x32_bf16 v[46:49], v[178:181], v[194:197], v[46:49]
	v_mfma_f32_16x16x32_bf16 v[38:41], v[170:173], v[202:205], v[38:41]
	v_mfma_f32_16x16x32_bf16 v[30:33], v[178:181], v[202:205], v[30:33]
	v_mfma_f32_16x16x32_bf16 v[22:25], v[170:173], v[212:215], v[22:25]
	v_mfma_f32_16x16x32_bf16 v[14:17], v[178:181], v[212:215], v[14:17]
	s_setprio 0
	s_barrier
	s_add_u32 s22, s22, 0x80080
	s_addc_u32 s23, s23, 0
	s_add_i32 s24, s24, s27
	v_lshl_add_u64 v[166:167], s[22:23], 0, v[132:133]
	s_mov_b32 m0, s24
	s_nop 0
	global_load_lds_dwordx4 v[166:167], off
	v_lshl_add_u64 v[166:167], s[22:23], 0, v[130:131]
	s_add_i32 m0, s24, 0x2000
	s_nop 0
	global_load_lds_dwordx4 v[166:167], off
	s_waitcnt vmcnt(6)
	s_barrier
	s_setprio 1
	v_mfma_f32_16x16x32_bf16 v[50:53], v[216:219], v[182:185], v[50:53]
	v_mfma_f32_16x16x32_bf16 v[42:45], v[224:227], v[182:185], v[42:45]
	v_mfma_f32_16x16x32_bf16 v[34:37], v[216:219], v[190:193], v[34:37]
	v_mfma_f32_16x16x32_bf16 v[26:29], v[224:227], v[190:193], v[26:29]
	v_mfma_f32_16x16x32_bf16 v[18:21], v[216:219], v[198:201], v[18:21]
	v_mfma_f32_16x16x32_bf16 v[10:13], v[224:227], v[198:201], v[10:13]
	v_mfma_f32_16x16x32_bf16 v[6:9], v[216:219], v[208:211], v[6:9]
	v_mfma_f32_16x16x32_bf16 v[2:5], v[224:227], v[208:211], v[2:5]
	v_mfma_f32_16x16x32_bf16 v[50:53], v[220:223], v[186:189], v[50:53]
	v_mfma_f32_16x16x32_bf16 v[42:45], v[228:231], v[186:189], v[42:45]
	v_mfma_f32_16x16x32_bf16 v[34:37], v[220:223], v[194:197], v[34:37]
	v_mfma_f32_16x16x32_bf16 v[26:29], v[228:231], v[194:197], v[26:29]
	v_mfma_f32_16x16x32_bf16 v[18:21], v[220:223], v[202:205], v[18:21]
	v_mfma_f32_16x16x32_bf16 v[10:13], v[228:231], v[202:205], v[10:13]
	v_mfma_f32_16x16x32_bf16 v[6:9], v[220:223], v[212:215], v[6:9]
	v_mfma_f32_16x16x32_bf16 v[2:5], v[228:231], v[212:215], v[2:5]
	s_setprio 0
	s_add_i32 s46, s46, 2
	s_add_u32 s20, s20, 0x100
	s_addc_u32 s21, s21, 0
	s_cmp_gt_u32 s46, 29
	s_barrier
	s_cbranch_scc0 .LBB0_246
; __device__ __forceinline__ unsigned cvt_pk_bf16(float lo, float hi) { unsigned r; asm volatile("v_cvt_pk_bf16_f32 %0, %1, %2" : "=v"(r) : "v"(lo), "v"(hi)); return r; }
; template <class Epi, class Sched>
; __device__ __forceinline__ void gemm_phase(LAS unsigned char* lds, const int K, const Sched& S, const Epi& E) {
;     ...
;         E(acc, cur, wr, wc, fr, fq);
;         if (!has_next) break;
;     __device__ __forceinline__ void operator()(const f32x4 (&acc)[2][2][4][2], const Unit& u, int wr, int wc, int fr, int fq) const {
;         const int row0 = u.rbase + wr * 64 + fr, col0 = u.pn * BM + wc * 32 + 8 * fq;
; #pragma unroll
;         for (int ai = 0; ai < 2; ++ai)
; #pragma unroll
;             for (int m = 0; m < 4; ++m) { bf16_t* rowp = O + (size_t)(row0 + ai * HALF + m * 16) * ldc + col0;
; #pragma unroll
;                 for (int bj = 0; bj < 2; ++bj) { const f32x4 v0 = acc[ai][bj][m][0], v1 = acc[ai][bj][m][1];
;                     u32x4 w; w.x = cvt_pk_bf16(v0[0], v0[1]); w.y = cvt_pk_bf16(v0[2], v0[3]); w.z = cvt_pk_bf16(v1[0], v1[1]); w.w = cvt_pk_bf16(v1[2], v1[3]);
;                     *(u32x4*)(rowp + bj * HALF) = w; } }
	v_lshl_or_b32 v142, s44, 8, v157
	v_add_u32_e32 v134, s43, v155
	v_ashrrev_i32_e32 v143, 31, v142
	v_mov_b64_e32 v[140:141], s[8:9]
	v_mad_i64_i32 v[144:145], s[20:21], v134, s39, v[140:141]
	v_lshlrev_b64 v[142:143], 1, v[142:143]
	v_lshl_add_u64 v[144:145], v[144:145], 0, v[142:143]
	v_cvt_pk_bf16_f32 v126, v126, v127
	v_cvt_pk_bf16_f32 v127, v128, v129
	v_cvt_pk_bf16_f32 v128, v122, v123
	v_cvt_pk_bf16_f32 v129, v124, v125
	global_store_dwordx4 v[144:145], v[126:129], off
	v_cvt_pk_bf16_f32 v114, v114, v115
	v_cvt_pk_bf16_f32 v115, v116, v117
	v_cvt_pk_bf16_f32 v116, v106, v107
	v_add_u32_e32 v106, 16, v134
	v_mad_i64_i32 v[106:107], s[20:21], v106, s39, v[140:141]
	v_cvt_pk_bf16_f32 v117, v108, v109
	global_store_dwordx4 v[144:145], v[114:117], off offset:256
	s_and_b64 vcc, exec, s[0:1]
	s_mov_b32 s44, s18
	v_lshl_add_u64 v[114:115], v[106:107], 0, v[142:143]
	v_cvt_pk_bf16_f32 v106, v118, v119
	v_cvt_pk_bf16_f32 v107, v120, v121
	v_cvt_pk_bf16_f32 v108, v110, v111
	v_cvt_pk_bf16_f32 v109, v112, v113
	global_store_dwordx4 v[114:115], v[106:109], off
	v_cvt_pk_bf16_f32 v98, v98, v99
	v_cvt_pk_bf16_f32 v99, v100, v101
	v_cvt_pk_bf16_f32 v100, v90, v91
	v_add_u32_e32 v90, 32, v134
	v_mad_i64_i32 v[90:91], s[20:21], v90, s39, v[140:141]
	v_cvt_pk_bf16_f32 v101, v92, v93
	global_store_dwordx4 v[114:115], v[98:101], off offset:256
	s_mov_b32 s43, s41
	v_mov_b32_e32 v144, v164
	v_lshl_add_u64 v[98:99], v[90:91], 0, v[142:143]
	v_cvt_pk_bf16_f32 v90, v102, v103
	v_cvt_pk_bf16_f32 v91, v104, v105
	v_cvt_pk_bf16_f32 v92, v94, v95
	v_cvt_pk_bf16_f32 v93, v96, v97
	global_store_dwordx4 v[98:99], v[90:93], off
	v_cvt_pk_bf16_f32 v82, v82, v83
	v_cvt_pk_bf16_f32 v83, v84, v85
	v_cvt_pk_bf16_f32 v84, v74, v75
	v_add_u32_e32 v74, 48, v134
	v_mad_i64_i32 v[74:75], s[20:21], v74, s39, v[140:141]
	v_cvt_pk_bf16_f32 v85, v76, v77
	global_store_dwordx4 v[98:99], v[82:85], off offset:256
	s_nop 1
	v_lshl_add_u64 v[82:83], v[74:75], 0, v[142:143]
	v_cvt_pk_bf16_f32 v74, v86, v87
	v_cvt_pk_bf16_f32 v75, v88, v89
	v_cvt_pk_bf16_f32 v76, v78, v79
	v_cvt_pk_bf16_f32 v77, v80, v81
	global_store_dwordx4 v[82:83], v[74:77], off
	v_cvt_pk_bf16_f32 v70, v70, v71
	v_cvt_pk_bf16_f32 v71, v72, v73
	v_cvt_pk_bf16_f32 v72, v66, v67
	v_add_u32_e32 v66, 0x80, v134
	v_mad_i64_i32 v[66:67], s[20:21], v66, s39, v[140:141]
	v_lshl_add_u64 v[66:67], v[66:67], 0, v[142:143]
	v_cvt_pk_bf16_f32 v73, v68, v69
	global_store_dwordx4 v[82:83], v[70:73], off offset:256
	v_cvt_pk_bf16_f32 v62, v62, v63
	v_cvt_pk_bf16_f32 v63, v64, v65
	v_cvt_pk_bf16_f32 v64, v58, v59
	v_cvt_pk_bf16_f32 v65, v60, v61
	global_store_dwordx4 v[66:67], v[62:65], off
	v_cvt_pk_bf16_f32 v50, v50, v51
	v_cvt_pk_bf16_f32 v51, v52, v53
	v_cvt_pk_bf16_f32 v52, v42, v43
	v_add_u32_e32 v42, 0x90, v134
	v_mad_i64_i32 v[42:43], s[20:21], v42, s39, v[140:141]
	v_cvt_pk_bf16_f32 v53, v44, v45
	global_store_dwordx4 v[66:67], v[50:53], off offset:256
	s_nop 1
	v_lshl_add_u64 v[50:51], v[42:43], 0, v[142:143]
	v_cvt_pk_bf16_f32 v42, v54, v55
	v_cvt_pk_bf16_f32 v43, v56, v57
	v_cvt_pk_bf16_f32 v44, v46, v47
	v_cvt_pk_bf16_f32 v45, v48, v49
	global_store_dwordx4 v[50:51], v[42:45], off
	v_cvt_pk_bf16_f32 v34, v34, v35
	v_cvt_pk_bf16_f32 v35, v36, v37
	v_cvt_pk_bf16_f32 v36, v26, v27
	v_add_u32_e32 v26, 0xa0, v134
	v_mad_i64_i32 v[26:27], s[20:21], v26, s39, v[140:141]
	v_cvt_pk_bf16_f32 v37, v28, v29
	global_store_dwordx4 v[50:51], v[34:37], off offset:256
	s_nop 1
	v_lshl_add_u64 v[34:35], v[26:27], 0, v[142:143]
	v_cvt_pk_bf16_f32 v26, v38, v39
	v_cvt_pk_bf16_f32 v27, v40, v41
	v_cvt_pk_bf16_f32 v28, v30, v31
	v_cvt_pk_bf16_f32 v29, v32, v33
	global_store_dwordx4 v[34:35], v[26:29], off
	v_cvt_pk_bf16_f32 v18, v18, v19
	v_cvt_pk_bf16_f32 v19, v20, v21
	v_cvt_pk_bf16_f32 v20, v10, v11
	v_add_u32_e32 v10, 0xb0, v134
	v_mad_i64_i32 v[10:11], s[20:21], v10, s39, v[140:141]
	v_cvt_pk_bf16_f32 v21, v12, v13
	global_store_dwordx4 v[34:35], v[18:21], off offset:256
	v_mov_b32_e32 v141, v161
	v_mov_b32_e32 v140, v162
	v_lshl_add_u64 v[18:19], v[10:11], 0, v[142:143]
	v_mov_b32_e32 v142, v163
	s_mov_b64 s[20:21], s[2:3]
	v_cvt_pk_bf16_f32 v10, v22, v23
	v_cvt_pk_bf16_f32 v11, v24, v25
	v_cvt_pk_bf16_f32 v12, v14, v15
	v_cvt_pk_bf16_f32 v13, v16, v17
	global_store_dwordx4 v[18:19], v[10:13], off
	v_cvt_pk_bf16_f32 v6, v6, v7
	v_cvt_pk_bf16_f32 v7, v8, v9
	v_cvt_pk_bf16_f32 v8, v2, v3
	v_cvt_pk_bf16_f32 v9, v4, v5
	global_store_dwordx4 v[18:19], v[6:9], off offset:256
	s_cbranch_vccz .LBB0_241
	s_waitcnt vmcnt(0)
	s_cmpk_gt_u32 s13, 0xff
	s_cbranch_scc1 .LBB0_250
	s_barrier

; #define PG8_STAGE(bufoff, gbase, v0, v1) do { \
;         __builtin_amdgcn_global_load_lds((const unsigned*)((const char*)(gbase) + (v0)), (LAS unsigned*)(lds + (bufoff) + ldsw), 16, 0, 0); \
;         __builtin_amdgcn_global_load_lds((const unsigned*)((const char*)(gbase) + (v1)), (LAS unsigned*)(lds + (bufoff) + ldsw + 8192), 16, 0, 0); } while (0)
; #define PG8_LDA(dst, b, h) do { _Pragma("unroll") for (int m = 0; m < 4; ++m) _Pragma("unroll") for (int k = 0; k < 2; ++k) dst[m][k] = *(const LAS bf16x8*)(lds + PG8_SA(b, h) + aoff + m * 2048 + k * 1024); } while (0)
; #define PG8_LDB(dst, b, h) do { _Pragma("unroll") for (int n = 0; n < 2; ++n) _Pragma("unroll") for (int k = 0; k < 2; ++k) dst[n][k] = *(const LAS bf16x8*)(lds + PG8_SB(b, h) + boff + n * 2048 + k * 1024); } while (0)
; #define PG8_MMA(ai, bj, At, Bt) do { __builtin_amdgcn_s_setprio(1); _Pragma("unroll") for (int m = 0; m < 4; ++m) _Pragma("unroll") for (int n = 0; n < 2; ++n) _Pragma("unroll") for (int k = 0; k < 2; ++k) \
;         acc[ai][bj][m][n] = __builtin_amdgcn_mfma_f32_16x16x32_bf16(Bt[n][k], At[m][k], acc[ai][bj][m][n], 0, 0, 0); __builtin_amdgcn_s_setprio(0); } while (0)
; #define PG8_WAIT_L(n) asm volatile("s_waitcnt lgkmcnt(" #n ")" ::: "memory")
; template <class Epi, class Sched>
; __device__ __forceinline__ void gemm_phase(LAS unsigned char* lds, const int K, const Sched& S, const Epi& E) {
;     ...
;         for (int t = 0; t < nt; t += 2) {
;             const bool last = (t == nt - 2);
;             const char* a1 = gA + (size_t)(t + 1) * kstep;
;             const char* a2 = last ? gA : gA + (size_t)(t + 2) * kstep; const char* b2 = last ? nB : cB + (size_t)(t + 2) * kstepB;
;             const char* a3 = a2 + kstep; const char* b3 = b2 + kstepB;
;             const unsigned x00 = last ? n00 : c00, x01 = last ? n01 : c01, x10 = last ? n10 : c10, x11 = last ? n11 : c11;
;             PG8_LDB(B0, 0, 0); PG8_SCHED; PG8_LDA(At, 0, 0); PG8_STAGE(PG8_SA(1, 1), a1, c10, c11);
;             PG8_WAIT_L(8); PG8_BAR; PG8_WAIT_L(0); PG8_MMA(0, 0, At, B0); PG8_BAR; PG8_SCHED;
;             PG8_LDB(B1, 0, 1); PG8_STAGE(PG8_SB(0, 0), b2, voffB0, voffB1);
;             PG8_BAR; PG8_WAIT_L(0); PG8_MMA(0, 1, At, B1); PG8_BAR;
;             PG8_LDA(At, 0, 1); PG8_STAGE(PG8_SA(0, 0), a2, x00, x01);
;             PG8_BAR; PG8_WAIT_L(0); PG8_MMA(1, 0, At, B0); PG8_BAR; PG8_SCHED;
.LBB0_942:
	s_add_u32 s38, s4, s36
	s_addc_u32 s39, s5, s37
	s_add_u32 s40, s38, 0x34c30100
	ds_read_b128 v[140:143], v170
	ds_read_b128 v[156:159], v170 offset:1024
	ds_read_b128 v[178:181], v170 offset:2048
	ds_read_b128 v[182:185], v170 offset:3072
	s_addc_u32 s41, s39, 0
	s_add_u32 s60, s35, s36
	s_addc_u32 s61, s58, s37
	s_cmpk_eq_i32 s36, 0xf00
	s_cselect_b64 vcc, -1, 0
	s_and_b64 s[38:39], vcc, exec
	v_cndmask_b32_e32 v150, v131, v173, vcc
	s_cselect_b32 s41, s9, s41
	s_cselect_b32 s40, s8, s40
	v_cndmask_b32_e32 v133, v132, v175, vcc
	s_cselect_b32 s39, s3, s61
	s_cselect_b32 s38, s2, s60
	v_cndmask_b32_e32 v144, v130, v174, vcc
	v_lshl_add_u64 v[160:161], v[138:139], 0, s[36:37]
	s_add_i32 m0, s45, 0xc000
	ds_read_b128 v[186:189], v171
	ds_read_b128 v[190:193], v171 offset:1024
	ds_read_b128 v[194:197], v171 offset:2048
	ds_read_b128 v[198:201], v171 offset:3072
	ds_read_b128 v[202:205], v171 offset:4096
	ds_read_b128 v[208:211], v171 offset:5120
	ds_read_b128 v[212:215], v171 offset:6144
	ds_read_b128 v[216:219], v171 offset:7168
	global_load_lds_dwordx4 v[160:161], off
	v_lshl_add_u64 v[160:161], v[136:137], 0, s[36:37]
	s_add_i32 m0, s45, 0xe000
	s_nop 0
	global_load_lds_dwordx4 v[160:161], off
	s_waitcnt lgkmcnt(8)
	s_barrier
	s_waitcnt lgkmcnt(0)
	s_setprio 1
	v_mfma_f32_16x16x32_bf16 v[126:129], v[140:143], v[186:189], v[126:129]
	v_mfma_f32_16x16x32_bf16 v[122:125], v[178:181], v[186:189], v[122:125]
	v_mfma_f32_16x16x32_bf16 v[118:121], v[140:143], v[194:197], v[118:121]
	v_mfma_f32_16x16x32_bf16 v[114:117], v[178:181], v[194:197], v[114:117]
	v_mfma_f32_16x16x32_bf16 v[110:113], v[140:143], v[202:205], v[110:113]
	v_mfma_f32_16x16x32_bf16 v[102:105], v[178:181], v[202:205], v[102:105]
	v_mfma_f32_16x16x32_bf16 v[94:97], v[140:143], v[212:215], v[94:97]
	v_mfma_f32_16x16x32_bf16 v[82:85], v[178:181], v[212:215], v[82:85]
	v_mfma_f32_16x16x32_bf16 v[126:129], v[156:159], v[190:193], v[126:129]
	v_mfma_f32_16x16x32_bf16 v[122:125], v[182:185], v[190:193], v[122:125]
	v_mfma_f32_16x16x32_bf16 v[118:121], v[156:159], v[198:201], v[118:121]
	v_mfma_f32_16x16x32_bf16 v[114:117], v[182:185], v[198:201], v[114:117]
	v_mfma_f32_16x16x32_bf16 v[110:113], v[156:159], v[208:211], v[110:113]
	v_mfma_f32_16x16x32_bf16 v[102:105], v[182:185], v[208:211], v[102:105]
	v_mfma_f32_16x16x32_bf16 v[94:97], v[156:159], v[216:219], v[94:97]
	v_mfma_f32_16x16x32_bf16 v[82:85], v[182:185], v[216:219], v[82:85]
	s_setprio 0
	s_barrier
	s_add_i32 s60, s52, s44
	v_lshl_add_u64 v[160:161], s[38:39], 0, v[148:149]
	s_mov_b32 m0, s60
	ds_read_b128 v[220:223], v172
	ds_read_b128 v[224:227], v172 offset:1024
	ds_read_b128 v[228:231], v172 offset:2048
	ds_read_b128 v[232:235], v172 offset:3072
	global_load_lds_dwordx4 v[160:161], off
	v_lshl_add_u64 v[206:207], s[38:39], 0, v[146:147]
	s_add_i32 m0, s60, 0x2000
	s_nop 0
	global_load_lds_dwordx4 v[206:207], off
	s_barrier
	s_waitcnt lgkmcnt(0)
	s_setprio 1
	v_mfma_f32_16x16x32_bf16 v[106:109], v[220:223], v[186:189], v[106:109]
	v_mfma_f32_16x16x32_bf16 v[98:101], v[228:231], v[186:189], v[98:101]
	v_mfma_f32_16x16x32_bf16 v[90:93], v[220:223], v[194:197], v[90:93]
	v_mfma_f32_16x16x32_bf16 v[86:89], v[228:231], v[194:197], v[86:89]
	v_mfma_f32_16x16x32_bf16 v[78:81], v[220:223], v[202:205], v[78:81]
	v_mfma_f32_16x16x32_bf16 v[74:77], v[228:231], v[202:205], v[74:77]
	v_mfma_f32_16x16x32_bf16 v[70:73], v[220:223], v[212:215], v[70:73]
	v_mfma_f32_16x16x32_bf16 v[66:69], v[228:231], v[212:215], v[66:69]
	v_mfma_f32_16x16x32_bf16 v[106:109], v[224:227], v[190:193], v[106:109]
	v_mfma_f32_16x16x32_bf16 v[98:101], v[232:235], v[190:193], v[98:101]
	v_mfma_f32_16x16x32_bf16 v[90:93], v[224:227], v[198:201], v[90:93]
	v_mfma_f32_16x16x32_bf16 v[86:89], v[232:235], v[198:201], v[86:89]
	v_mfma_f32_16x16x32_bf16 v[78:81], v[224:227], v[208:211], v[78:81]
	v_mfma_f32_16x16x32_bf16 v[74:77], v[232:235], v[208:211], v[74:77]
	v_mfma_f32_16x16x32_bf16 v[70:73], v[224:227], v[216:219], v[70:73]
	v_mfma_f32_16x16x32_bf16 v[66:69], v[232:235], v[216:219], v[66:69]
	s_setprio 0
	s_mov_b32 m0, s45
	s_barrier
	ds_read_b128 v[186:189], v171 offset:16384
	ds_read_b128 v[190:193], v171 offset:17408
	ds_read_b128 v[194:197], v171 offset:18432
	ds_read_b128 v[198:201], v171 offset:19456
	ds_read_b128 v[202:205], v171 offset:20480
	ds_read_b128 v[208:211], v171 offset:21504
	ds_read_b128 v[212:215], v171 offset:22528
	ds_read_b128 v[216:219], v171 offset:23552
	global_load_lds_dwordx4 v150, s[40:41]
	s_mov_b32 m0, s46
	v_mov_b32_e32 v145, v151
	global_load_lds_dwordx4 v144, s[40:41]
	s_barrier
	s_waitcnt lgkmcnt(0)
	v_lshl_add_u64 v[236:237], s[40:41], 0, v[150:151]
	v_lshl_add_u64 v[144:145], s[40:41], 0, v[144:145]
	s_setprio 1
	s_waitcnt lgkmcnt(0)
	v_mfma_f32_16x16x32_bf16 v[62:65], v[140:143], v[186:189], v[62:65]
	v_mfma_f32_16x16x32_bf16 v[58:61], v[178:181], v[186:189], v[58:61]
	v_mfma_f32_16x16x32_bf16 v[54:57], v[140:143], v[194:197], v[54:57]
	v_mfma_f32_16x16x32_bf16 v[50:53], v[178:181], v[194:197], v[50:53]
	v_mfma_f32_16x16x32_bf16 v[46:49], v[140:143], v[202:205], v[46:49]
	v_mfma_f32_16x16x32_bf16 v[38:41], v[178:181], v[202:205], v[38:41]
	v_mfma_f32_16x16x32_bf16 v[30:33], v[140:143], v[212:215], v[30:33]
	v_mfma_f32_16x16x32_bf16 v[18:21], v[178:181], v[212:215], v[18:21]
	v_mfma_f32_16x16x32_bf16 v[62:65], v[156:159], v[190:193], v[62:65]
	v_mfma_f32_16x16x32_bf16 v[58:61], v[182:185], v[190:193], v[58:61]
	v_mfma_f32_16x16x32_bf16 v[54:57], v[156:159], v[198:201], v[54:57]
	v_mfma_f32_16x16x32_bf16 v[50:53], v[182:185], v[198:201], v[50:53]
	v_mfma_f32_16x16x32_bf16 v[46:49], v[156:159], v[208:211], v[46:49]
	v_mfma_f32_16x16x32_bf16 v[38:41], v[182:185], v[208:211], v[38:41]
	v_mfma_f32_16x16x32_bf16 v[30:33], v[156:159], v[216:219], v[30:33]
	v_mfma_f32_16x16x32_bf16 v[18:21], v[182:185], v[216:219], v[18:21]
	s_setprio 0
	s_barrier
; #define PG8_STAGE(bufoff, gbase, v0, v1) do { \
;         __builtin_amdgcn_global_load_lds((const unsigned*)((const char*)(gbase) + (v0)), (LAS unsigned*)(lds + (bufoff) + ldsw), 16, 0, 0); \
;         __builtin_amdgcn_global_load_lds((const unsigned*)((const char*)(gbase) + (v1)), (LAS unsigned*)(lds + (bufoff) + ldsw + 8192), 16, 0, 0); } while (0)
; #define PG8_LDA(dst, b, h) do { _Pragma("unroll") for (int m = 0; m < 4; ++m) _Pragma("unroll") for (int k = 0; k < 2; ++k) dst[m][k] = *(const LAS bf16x8*)(lds + PG8_SA(b, h) + aoff + m * 2048 + k * 1024); } while (0)
; #define PG8_LDB(dst, b, h) do { _Pragma("unroll") for (int n = 0; n < 2; ++n) _Pragma("unroll") for (int k = 0; k < 2; ++k) dst[n][k] = *(const LAS bf16x8*)(lds + PG8_SB(b, h) + boff + n * 2048 + k * 1024); } while (0)
; #define PG8_MMA(ai, bj, At, Bt) do { __builtin_amdgcn_s_setprio(1); _Pragma("unroll") for (int m = 0; m < 4; ++m) _Pragma("unroll") for (int n = 0; n < 2; ++n) _Pragma("unroll") for (int k = 0; k < 2; ++k) \
;         acc[ai][bj][m][n] = __builtin_amdgcn_mfma_f32_16x16x32_bf16(Bt[n][k], At[m][k], acc[ai][bj][m][n], 0, 0, 0); __builtin_amdgcn_s_setprio(0); } while (0)
; #define PG8_WAIT_V(n) asm volatile("s_waitcnt vmcnt(" #n ")" ::: "memory")
; #define PG8_WAIT_L(n) asm volatile("s_waitcnt lgkmcnt(" #n ")" ::: "memory")
; #define PG8_BAR __builtin_amdgcn_s_barrier()
; #define PG8_SCHED __builtin_amdgcn_sched_barrier(0)
; template <class Epi, class Sched>
; __device__ __forceinline__ void gemm_phase(LAS unsigned char* lds, const int K, const Sched& S, const Epi& E) {
;     ...
;             PG8_STAGE(PG8_SB(0, 1), b2 + hstep, voffB0, voffB1);
;             PG8_WAIT_V(6); PG8_BAR; PG8_MMA(1, 1, At, B1); PG8_BAR;
;             PG8_LDB(B0, 1, 0); PG8_SCHED; PG8_LDA(At, 1, 0); PG8_STAGE(PG8_SA(0, 1), a2, x10, x11);
;             PG8_WAIT_L(8); PG8_BAR; PG8_WAIT_L(0); PG8_MMA(0, 0, At, B0); PG8_BAR; PG8_SCHED;
;             PG8_LDB(B1, 1, 1); PG8_STAGE(PG8_SB(1, 0), b3, voffB0, voffB1);
;             PG8_BAR; PG8_WAIT_L(0); PG8_MMA(0, 1, At, B1); PG8_BAR;
;             PG8_LDA(At, 1, 1); PG8_STAGE(PG8_SA(1, 0), a3, x00, x01);
	s_add_u32 s60, s38, 0x80000
	s_addc_u32 s61, s39, 0
	s_add_i32 s62, s53, s44
	v_lshl_add_u64 v[140:141], s[60:61], 0, v[148:149]
	s_mov_b32 m0, s62
	s_nop 0
	global_load_lds_dwordx4 v[140:141], off
	v_lshl_add_u64 v[140:141], s[60:61], 0, v[146:147]
	s_add_i32 m0, s62, 0x2000
	s_nop 0
	global_load_lds_dwordx4 v[140:141], off
	s_waitcnt vmcnt(6)
	s_barrier
	s_setprio 1
	v_mfma_f32_16x16x32_bf16 v[42:45], v[220:223], v[186:189], v[42:45]
	v_mfma_f32_16x16x32_bf16 v[34:37], v[228:231], v[186:189], v[34:37]
	v_mfma_f32_16x16x32_bf16 v[26:29], v[220:223], v[194:197], v[26:29]
	v_mfma_f32_16x16x32_bf16 v[22:25], v[228:231], v[194:197], v[22:25]
	v_mfma_f32_16x16x32_bf16 v[14:17], v[220:223], v[202:205], v[14:17]
	v_mfma_f32_16x16x32_bf16 v[10:13], v[228:231], v[202:205], v[10:13]
	v_mfma_f32_16x16x32_bf16 v[6:9], v[220:223], v[212:215], v[6:9]
	v_mfma_f32_16x16x32_bf16 v[2:5], v[228:231], v[212:215], v[2:5]
	v_mfma_f32_16x16x32_bf16 v[42:45], v[224:227], v[190:193], v[42:45]
	v_mfma_f32_16x16x32_bf16 v[34:37], v[232:235], v[190:193], v[34:37]
	v_mfma_f32_16x16x32_bf16 v[26:29], v[224:227], v[198:201], v[26:29]
	v_mfma_f32_16x16x32_bf16 v[22:25], v[232:235], v[198:201], v[22:25]
	v_mfma_f32_16x16x32_bf16 v[14:17], v[224:227], v[208:211], v[14:17]
	v_mfma_f32_16x16x32_bf16 v[10:13], v[232:235], v[208:211], v[10:13]
	v_mfma_f32_16x16x32_bf16 v[6:9], v[224:227], v[216:219], v[6:9]
	v_mfma_f32_16x16x32_bf16 v[2:5], v[232:235], v[216:219], v[2:5]
	s_setprio 0
	s_add_i32 s60, 0, 0x18000
	v_add_u32_e32 v135, s60, v168
	s_barrier
	ds_read_b128 v[140:143], v135
	ds_read_b128 v[156:159], v135 offset:1024
	ds_read_b128 v[178:181], v135 offset:2048
	ds_read_b128 v[182:185], v135 offset:3072
	s_mov_b32 m0, s47
	ds_read_b128 v[186:189], v171 offset:32768
	ds_read_b128 v[190:193], v171 offset:33792
	ds_read_b128 v[194:197], v171 offset:34816
	ds_read_b128 v[198:201], v171 offset:35840
	ds_read_b128 v[202:205], v171 offset:36864
	ds_read_b128 v[208:211], v171 offset:37888
	ds_read_b128 v[212:215], v171 offset:38912
	ds_read_b128 v[216:219], v171 offset:39936
	v_cndmask_b32_e32 v135, v134, v176, vcc
	global_load_lds_dwordx4 v133, s[40:41]
	s_mov_b32 m0, s48
	s_nop 0
	global_load_lds_dwordx4 v135, s[40:41]
	s_waitcnt lgkmcnt(8)
	s_barrier
	s_waitcnt lgkmcnt(0)
	s_setprio 1
	v_mfma_f32_16x16x32_bf16 v[126:129], v[140:143], v[186:189], v[126:129]
	v_mfma_f32_16x16x32_bf16 v[122:125], v[178:181], v[186:189], v[122:125]
	v_mfma_f32_16x16x32_bf16 v[118:121], v[140:143], v[194:197], v[118:121]
	v_mfma_f32_16x16x32_bf16 v[114:117], v[178:181], v[194:197], v[114:117]
	v_mfma_f32_16x16x32_bf16 v[110:113], v[140:143], v[202:205], v[110:113]
	v_mfma_f32_16x16x32_bf16 v[102:105], v[178:181], v[202:205], v[102:105]
	v_mfma_f32_16x16x32_bf16 v[94:97], v[140:143], v[212:215], v[94:97]
	v_mfma_f32_16x16x32_bf16 v[82:85], v[178:181], v[212:215], v[82:85]
	v_mfma_f32_16x16x32_bf16 v[126:129], v[156:159], v[190:193], v[126:129]
	v_mfma_f32_16x16x32_bf16 v[122:125], v[182:185], v[190:193], v[122:125]
	v_mfma_f32_16x16x32_bf16 v[118:121], v[156:159], v[198:201], v[118:121]
	v_mfma_f32_16x16x32_bf16 v[114:117], v[182:185], v[198:201], v[114:117]
	v_mfma_f32_16x16x32_bf16 v[110:113], v[156:159], v[208:211], v[110:113]
	v_mfma_f32_16x16x32_bf16 v[102:105], v[182:185], v[208:211], v[102:105]
	v_mfma_f32_16x16x32_bf16 v[94:97], v[156:159], v[216:219], v[94:97]
	v_mfma_f32_16x16x32_bf16 v[82:85], v[182:185], v[216:219], v[82:85]
	s_setprio 0
	s_barrier
	s_add_i32 s40, 0, 0x1c000
	s_add_i32 s41, s60, s44
	v_add_u32_e32 v133, s40, v168
	v_lshl_add_u64 v[160:161], v[160:161], 0, s[16:17]
	s_mov_b32 m0, s41
	ds_read_b128 v[220:223], v133
	ds_read_b128 v[224:227], v133 offset:1024
	ds_read_b128 v[228:231], v133 offset:2048
	ds_read_b128 v[232:235], v133 offset:3072
	global_load_lds_dwordx4 v[160:161], off
	v_lshl_add_u64 v[160:161], v[206:207], 0, s[16:17]
	s_add_i32 m0, s41, 0x2000
	s_nop 0
	global_load_lds_dwordx4 v[160:161], off
	s_barrier
	s_waitcnt lgkmcnt(0)
	s_setprio 1
	v_mfma_f32_16x16x32_bf16 v[106:109], v[220:223], v[186:189], v[106:109]
	v_mfma_f32_16x16x32_bf16 v[98:101], v[228:231], v[186:189], v[98:101]
	v_mfma_f32_16x16x32_bf16 v[90:93], v[220:223], v[194:197], v[90:93]
	v_mfma_f32_16x16x32_bf16 v[86:89], v[228:231], v[194:197], v[86:89]
	v_mfma_f32_16x16x32_bf16 v[78:81], v[220:223], v[202:205], v[78:81]
	v_mfma_f32_16x16x32_bf16 v[74:77], v[228:231], v[202:205], v[74:77]
	v_mfma_f32_16x16x32_bf16 v[70:73], v[220:223], v[212:215], v[70:73]
	v_mfma_f32_16x16x32_bf16 v[66:69], v[228:231], v[212:215], v[66:69]
	v_mfma_f32_16x16x32_bf16 v[106:109], v[224:227], v[190:193], v[106:109]
	v_mfma_f32_16x16x32_bf16 v[98:101], v[232:235], v[190:193], v[98:101]
	v_mfma_f32_16x16x32_bf16 v[90:93], v[224:227], v[198:201], v[90:93]
	v_mfma_f32_16x16x32_bf16 v[86:89], v[232:235], v[198:201], v[86:89]
	v_mfma_f32_16x16x32_bf16 v[78:81], v[224:227], v[208:211], v[78:81]
	v_mfma_f32_16x16x32_bf16 v[74:77], v[232:235], v[208:211], v[74:77]
	v_mfma_f32_16x16x32_bf16 v[70:73], v[224:227], v[216:219], v[70:73]
	v_mfma_f32_16x16x32_bf16 v[66:69], v[232:235], v[216:219], v[66:69]
	s_setprio 0
	s_mov_b32 m0, s50
	v_lshl_add_u64 v[160:161], v[236:237], 0, s[16:17]
	s_barrier
	ds_read_b128 v[186:189], v171 offset:49152
	ds_read_b128 v[190:193], v171 offset:50176
	ds_read_b128 v[194:197], v171 offset:51200
	ds_read_b128 v[198:201], v171 offset:52224
	ds_read_b128 v[202:205], v171 offset:53248
	ds_read_b128 v[208:211], v171 offset:54272
	ds_read_b128 v[212:215], v171 offset:55296
	ds_read_b128 v[216:219], v171 offset:56320
	global_load_lds_dwordx4 v[160:161], off
	v_lshl_add_u64 v[144:145], v[144:145], 0, s[16:17]
	s_mov_b32 m0, s51
	s_nop 0
	global_load_lds_dwordx4 v[144:145], off
	s_barrier
; #define PG8_STAGE(bufoff, gbase, v0, v1) do { \
;         __builtin_amdgcn_global_load_lds((const unsigned*)((const char*)(gbase) + (v0)), (LAS unsigned*)(lds + (bufoff) + ldsw), 16, 0, 0); \
;         __builtin_amdgcn_global_load_lds((const unsigned*)((const char*)(gbase) + (v1)), (LAS unsigned*)(lds + (bufoff) + ldsw + 8192), 16, 0, 0); } while (0)
; #define PG8_MMA(ai, bj, At, Bt) do { __builtin_amdgcn_s_setprio(1); _Pragma("unroll") for (int m = 0; m < 4; ++m) _Pragma("unroll") for (int n = 0; n < 2; ++n) _Pragma("unroll") for (int k = 0; k < 2; ++k) \
;         acc[ai][bj][m][n] = __builtin_amdgcn_mfma_f32_16x16x32_bf16(Bt[n][k], At[m][k], acc[ai][bj][m][n], 0, 0, 0); __builtin_amdgcn_s_setprio(0); } while (0)
; #define PG8_WAIT_V(n) asm volatile("s_waitcnt vmcnt(" #n ")" ::: "memory")
; #define PG8_WAIT_L(n) asm volatile("s_waitcnt lgkmcnt(" #n ")" ::: "memory")
; #define PG8_BAR __builtin_amdgcn_s_barrier()
; #define PG8_SCHED __builtin_amdgcn_sched_barrier(0)
; template <class Epi, class Sched>
; __device__ __forceinline__ void gemm_phase(LAS unsigned char* lds, const int K, const Sched& S, const Epi& E) {
;     ...
;             PG8_BAR; PG8_WAIT_L(0); PG8_MMA(1, 0, At, B0); PG8_BAR; PG8_SCHED;
;             PG8_STAGE(PG8_SB(1, 1), b3 + hstep, voffB0, voffB1);
;             PG8_WAIT_V(6); PG8_BAR; PG8_MMA(1, 1, At, B1); PG8_BAR;
;     __device__ __forceinline__ void operator()(const f32x4 (&acc)[2][2][4][2], const Unit& u, int wr, int wc, int fr, int fq) const {
;         const int row0 = u.rbase + wr * 64 + fr, col0 = u.pn * BM + wc * 32 + 4 * fq;
;         f32x4 gv[2][2];
; #pragma unroll
;         for (int bj = 0; bj < 2; ++bj)
; #pragma unroll
;             for (int n = 0; n < 2; ++n) gv[bj][n] = *(const f32x4*)(gate + col0 + bj * HALF + n * 16);
; #pragma unroll
;         for (int ai = 0; ai < 2; ++ai) {
;             f32x4 xv[4][2][2];
; #pragma unroll
;             for (int m = 0; m < 4; ++m) { const size_t ro = (size_t)(row0 + ai * HALF + m * 16) * D + col0;
; #pragma unroll
;                 for (int bj = 0; bj < 2; ++bj)
; #pragma unroll
;                     for (int n = 0; n < 2; ++n) xv[m][bj][n] = *(const f32x4*)(xin + ro + bj * HALF + n * 16); }
	s_waitcnt lgkmcnt(0)
	s_setprio 1
	v_mfma_f32_16x16x32_bf16 v[62:65], v[140:143], v[186:189], v[62:65]
	v_mfma_f32_16x16x32_bf16 v[58:61], v[178:181], v[186:189], v[58:61]
	v_mfma_f32_16x16x32_bf16 v[54:57], v[140:143], v[194:197], v[54:57]
	v_mfma_f32_16x16x32_bf16 v[50:53], v[178:181], v[194:197], v[50:53]
	v_mfma_f32_16x16x32_bf16 v[46:49], v[140:143], v[202:205], v[46:49]
	v_mfma_f32_16x16x32_bf16 v[38:41], v[178:181], v[202:205], v[38:41]
	v_mfma_f32_16x16x32_bf16 v[30:33], v[140:143], v[212:215], v[30:33]
	v_mfma_f32_16x16x32_bf16 v[18:21], v[178:181], v[212:215], v[18:21]
	v_mfma_f32_16x16x32_bf16 v[62:65], v[156:159], v[190:193], v[62:65]
	v_mfma_f32_16x16x32_bf16 v[58:61], v[182:185], v[190:193], v[58:61]
	v_mfma_f32_16x16x32_bf16 v[54:57], v[156:159], v[198:201], v[54:57]
	v_mfma_f32_16x16x32_bf16 v[50:53], v[182:185], v[198:201], v[50:53]
	v_mfma_f32_16x16x32_bf16 v[46:49], v[156:159], v[208:211], v[46:49]
	v_mfma_f32_16x16x32_bf16 v[38:41], v[182:185], v[208:211], v[38:41]
	v_mfma_f32_16x16x32_bf16 v[30:33], v[156:159], v[216:219], v[30:33]
	v_mfma_f32_16x16x32_bf16 v[18:21], v[182:185], v[216:219], v[18:21]
	s_setprio 0
	s_barrier
	s_add_u32 s38, s38, 0x80080
	s_addc_u32 s39, s39, 0
	s_add_i32 s40, s40, s44
	v_lshl_add_u64 v[140:141], s[38:39], 0, v[148:149]
	s_mov_b32 m0, s40
	s_nop 0
	global_load_lds_dwordx4 v[140:141], off
	v_lshl_add_u64 v[140:141], s[38:39], 0, v[146:147]
	s_add_i32 m0, s40, 0x2000
	s_nop 0
	global_load_lds_dwordx4 v[140:141], off
	s_waitcnt vmcnt(6)
	s_barrier
	s_setprio 1
	v_mfma_f32_16x16x32_bf16 v[42:45], v[220:223], v[186:189], v[42:45]
	v_mfma_f32_16x16x32_bf16 v[34:37], v[228:231], v[186:189], v[34:37]
	v_mfma_f32_16x16x32_bf16 v[26:29], v[220:223], v[194:197], v[26:29]
	v_mfma_f32_16x16x32_bf16 v[22:25], v[228:231], v[194:197], v[22:25]
	v_mfma_f32_16x16x32_bf16 v[14:17], v[220:223], v[202:205], v[14:17]
	v_mfma_f32_16x16x32_bf16 v[10:13], v[228:231], v[202:205], v[10:13]
	v_mfma_f32_16x16x32_bf16 v[6:9], v[220:223], v[212:215], v[6:9]
	v_mfma_f32_16x16x32_bf16 v[2:5], v[228:231], v[212:215], v[2:5]
	v_mfma_f32_16x16x32_bf16 v[42:45], v[224:227], v[190:193], v[42:45]
	v_mfma_f32_16x16x32_bf16 v[34:37], v[232:235], v[190:193], v[34:37]
	v_mfma_f32_16x16x32_bf16 v[26:29], v[224:227], v[198:201], v[26:29]
	v_mfma_f32_16x16x32_bf16 v[22:25], v[232:235], v[198:201], v[22:25]
	v_mfma_f32_16x16x32_bf16 v[14:17], v[224:227], v[208:211], v[14:17]
	v_mfma_f32_16x16x32_bf16 v[10:13], v[232:235], v[208:211], v[10:13]
	v_mfma_f32_16x16x32_bf16 v[6:9], v[224:227], v[216:219], v[6:9]
	v_mfma_f32_16x16x32_bf16 v[2:5], v[232:235], v[216:219], v[2:5]
	s_setprio 0
	s_add_i32 s59, s59, 2
	s_add_u32 s36, s36, 0x100
	s_addc_u32 s37, s37, 0
	s_cmp_gt_u32 s59, 29
	s_barrier
	s_cbranch_scc0 .LBB0_942
	v_lshl_or_b32 v130, s57, 8, v169
	v_add_u32_e32 v132, s56, v167
	v_ashrrev_i32_e32 v131, 31, v130
	v_ashrrev_i32_e32 v133, 31, v132
	v_lshlrev_b64 v[156:157], 2, v[130:131]
	v_lshlrev_b64 v[160:161], 13, v[132:133]
	v_lshl_add_u64 v[158:159], s[6:7], 0, v[156:157]
	v_lshl_add_u64 v[206:207], v[160:161], 0, s[18:19]
	v_lshl_add_u64 v[244:245], v[160:161], 0, s[20:21]
	v_lshl_add_u64 v[246:247], v[160:161], 0, s[22:23]
	v_lshl_add_u64 v[130:131], s[12:13], 0, v[156:157]
	v_lshl_add_u64 v[190:191], v[158:159], 0, v[160:161]
	v_lshl_add_u64 v[208:209], v[158:159], 0, v[206:207]
	v_lshl_add_u64 v[224:225], v[158:159], 0, v[244:245]
	v_lshl_add_u64 v[240:241], v[158:159], 0, v[246:247]
	global_load_dwordx4 v[142:145], v[130:131], off
	global_load_dwordx4 v[134:137], v[130:131], off offset:64
	global_load_dwordx4 v[178:181], v[190:191], off
	global_load_dwordx4 v[182:185], v[190:191], off offset:64
	global_load_dwordx4 v[138:141], v[130:131], off offset:512
	s_nop 0
	global_load_dwordx4 v[130:133], v[130:131], off offset:576
	s_nop 0
	global_load_dwordx4 v[186:189], v[190:191], off offset:512
	s_nop 0
	global_load_dwordx4 v[190:193], v[190:191], off offset:576
	s_nop 0
	global_load_dwordx4 v[194:197], v[208:209], off
	global_load_dwordx4 v[198:201], v[208:209], off offset:64
	global_load_dwordx4 v[202:205], v[208:209], off offset:512
	s_nop 0
	global_load_dwordx4 v[208:211], v[208:209], off offset:576
	s_nop 0
	global_load_dwordx4 v[212:215], v[224:225], off
	global_load_dwordx4 v[216:219], v[224:225], off offset:64
	global_load_dwordx4 v[220:223], v[224:225], off offset:512
	s_nop 0
	global_load_dwordx4 v[224:227], v[224:225], off offset:576
	s_nop 0
	global_load_dwordx4 v[228:231], v[240:241], off
	global_load_dwordx4 v[232:235], v[240:241], off offset:64
	global_load_dwordx4 v[236:239], v[240:241], off offset:512
	s_nop 0
	global_load_dwordx4 v[240:243], v[240:241], off offset:576
	v_lshl_add_u64 v[248:249], s[10:11], 0, v[160:161]
	v_lshl_add_u64 v[246:247], s[10:11], 0, v[246:247]
	v_lshl_add_u64 v[248:249], v[248:249], 0, v[156:157]
	v_lshl_add_u64 v[206:207], s[10:11], 0, v[206:207]
	v_lshl_add_u64 v[244:245], s[10:11], 0, v[244:245]
	v_lshl_add_u64 v[246:247], v[246:247], 0, v[156:157]
	v_lshl_add_u64 v[206:207], v[206:207], 0, v[156:157]
	v_lshl_add_u64 v[244:245], v[244:245], 0, v[156:157]
	s_and_b64 vcc, exec, s[0:1]
	s_mov_b32 s57, s34
	s_mov_b32 s56, s54
	s_mov_b64 s[36:37], s[2:3]
	s_waitcnt vmcnt(0)
;     __device__ __forceinline__ void operator()(const f32x4 (&acc)[2][2][4][2], const Unit& u, int wr, int wc, int fr, int fq) const {
;     ...
;         for (int ai = 0; ai < 2; ++ai) {
;             f32x4 xv[4][2][2];
; #pragma unroll
;             for (int m = 0; m < 4; ++m) { const size_t ro = (size_t)(row0 + ai * HALF + m * 16) * D + col0;
; #pragma unroll
;                 for (int bj = 0; bj < 2; ++bj)
; #pragma unroll
;                     for (int n = 0; n < 2; ++n) xv[m][bj][n] = *(const f32x4*)(xin + ro + bj * HALF + n * 16); }
; #pragma unroll
;             for (int m = 0; m < 4; ++m) { const size_t ro = (size_t)(row0 + ai * HALF + m * 16) * D + col0;
; #pragma unroll
;                 for (int bj = 0; bj < 2; ++bj)
; #pragma unroll
;                     for (int n = 0; n < 2; ++n) *(f32x4*)(out + ro + bj * HALF + n * 16) = xv[m][bj][n] + gv[bj][n] * acc[ai][bj][m][n]; }
	v_pk_fma_f32 v[128:129], v[128:129], v[144:145], v[180:181]
	v_pk_fma_f32 v[126:127], v[126:127], v[142:143], v[178:179]
	v_pk_fma_f32 v[122:123], v[122:123], v[134:135], v[182:183]
	v_pk_fma_f32 v[110:111], v[110:111], v[142:143], v[212:213]
	v_pk_fma_f32 v[78:79], v[78:79], v[138:139], v[220:221]
	v_pk_fma_f32 v[94:95], v[94:95], v[142:143], v[228:229]
	v_pk_fma_f32 v[68:69], v[68:69], v[132:133], v[242:243]
	v_pk_fma_f32 v[66:67], v[66:67], v[130:131], v[240:241]
	v_lshl_add_u64 v[178:179], v[160:161], 0, s[24:25]
	v_lshl_add_u64 v[180:181], v[160:161], 0, s[26:27]
	v_lshl_add_u64 v[182:183], v[160:161], 0, s[28:29]
	v_lshl_add_u64 v[160:161], v[160:161], 0, s[30:31]
	v_pk_fma_f32 v[124:125], v[124:125], v[136:137], v[184:185]
	v_pk_fma_f32 v[108:109], v[108:109], v[140:141], v[188:189]
	v_pk_fma_f32 v[106:107], v[106:107], v[138:139], v[186:187]
	v_pk_fma_f32 v[100:101], v[100:101], v[132:133], v[192:193]
	v_pk_fma_f32 v[98:99], v[98:99], v[130:131], v[190:191]
	v_pk_fma_f32 v[120:121], v[120:121], v[144:145], v[196:197]
	v_pk_fma_f32 v[118:119], v[118:119], v[142:143], v[194:195]
	v_pk_fma_f32 v[116:117], v[116:117], v[136:137], v[200:201]
	v_pk_fma_f32 v[114:115], v[114:115], v[134:135], v[198:199]
	v_pk_fma_f32 v[92:93], v[92:93], v[140:141], v[204:205]
	v_pk_fma_f32 v[90:91], v[90:91], v[138:139], v[202:203]
	v_pk_fma_f32 v[88:89], v[88:89], v[132:133], v[210:211]
	v_pk_fma_f32 v[86:87], v[86:87], v[130:131], v[208:209]
	v_pk_fma_f32 v[112:113], v[112:113], v[144:145], v[214:215]
	v_pk_fma_f32 v[104:105], v[104:105], v[136:137], v[218:219]
	v_pk_fma_f32 v[102:103], v[102:103], v[134:135], v[216:217]
	v_pk_fma_f32 v[80:81], v[80:81], v[140:141], v[222:223]
	v_pk_fma_f32 v[76:77], v[76:77], v[132:133], v[226:227]
	v_pk_fma_f32 v[74:75], v[74:75], v[130:131], v[224:225]
	v_pk_fma_f32 v[96:97], v[96:97], v[144:145], v[230:231]
	v_pk_fma_f32 v[84:85], v[84:85], v[136:137], v[234:235]
	v_pk_fma_f32 v[82:83], v[82:83], v[134:135], v[232:233]
	v_pk_fma_f32 v[72:73], v[72:73], v[140:141], v[238:239]
	v_pk_fma_f32 v[70:71], v[70:71], v[138:139], v[236:237]
	global_store_dwordx4 v[248:249], v[126:129], off
	global_store_dwordx4 v[248:249], v[122:125], off offset:64
	global_store_dwordx4 v[248:249], v[106:109], off offset:512
	global_store_dwordx4 v[248:249], v[98:101], off offset:576
	global_store_dwordx4 v[206:207], v[118:121], off
	global_store_dwordx4 v[206:207], v[114:117], off offset:64
	global_store_dwordx4 v[206:207], v[90:93], off offset:512
	global_store_dwordx4 v[206:207], v[86:89], off offset:576
	global_store_dwordx4 v[244:245], v[110:113], off
	global_store_dwordx4 v[244:245], v[102:105], off offset:64
	global_store_dwordx4 v[244:245], v[78:81], off offset:512
	global_store_dwordx4 v[244:245], v[74:77], off offset:576
	global_store_dwordx4 v[246:247], v[94:97], off
	global_store_dwordx4 v[246:247], v[82:85], off offset:64
	global_store_dwordx4 v[246:247], v[70:73], off offset:512
	global_store_dwordx4 v[246:247], v[66:69], off offset:576
	v_lshl_add_u64 v[78:79], v[158:159], 0, v[178:179]
	v_lshl_add_u64 v[94:95], v[158:159], 0, v[180:181]
	v_lshl_add_u64 v[110:111], v[158:159], 0, v[182:183]
	v_lshl_add_u64 v[126:127], v[158:159], 0, v[160:161]
	global_load_dwordx4 v[66:69], v[78:79], off
	global_load_dwordx4 v[70:73], v[78:79], off offset:64
	global_load_dwordx4 v[74:77], v[78:79], off offset:512
	s_nop 0
	global_load_dwordx4 v[78:81], v[78:79], off offset:576
	s_nop 0
	global_load_dwordx4 v[82:85], v[94:95], off
	global_load_dwordx4 v[86:89], v[94:95], off offset:64
	global_load_dwordx4 v[90:93], v[94:95], off offset:512
	s_nop 0
	global_load_dwordx4 v[94:97], v[94:95], off offset:576
	s_nop 0
	global_load_dwordx4 v[98:101], v[110:111], off
	global_load_dwordx4 v[102:105], v[110:111], off offset:64
	global_load_dwordx4 v[106:109], v[110:111], off offset:512
	v_lshl_add_u64 v[158:159], s[10:11], 0, v[178:179]
	global_load_dwordx4 v[110:113], v[110:111], off offset:576
	s_nop 0
	global_load_dwordx4 v[114:117], v[126:127], off
	global_load_dwordx4 v[118:121], v[126:127], off offset:64
	global_load_dwordx4 v[122:125], v[126:127], off offset:512
	s_nop 0
	global_load_dwordx4 v[126:129], v[126:127], off offset:576
	v_lshl_add_u64 v[178:179], s[10:11], 0, v[180:181]
	v_lshl_add_u64 v[180:181], s[10:11], 0, v[182:183]
	v_lshl_add_u64 v[160:161], s[10:11], 0, v[160:161]
	v_lshl_add_u64 v[158:159], v[158:159], 0, v[156:157]
	v_lshl_add_u64 v[178:179], v[178:179], 0, v[156:157]
	v_lshl_add_u64 v[180:181], v[180:181], 0, v[156:157]
	v_lshl_add_u64 v[156:157], v[160:161], 0, v[156:157]
	s_waitcnt vmcnt(0)
; #define PG8_WAIT_V(n) asm volatile("s_waitcnt vmcnt(" #n ")" ::: "memory")
; #define PG8_BAR __builtin_amdgcn_s_barrier()
; template <class Epi, class Sched>
; __device__ __forceinline__ void gemm_phase(LAS unsigned char* lds, const int K, const Sched& S, const Epi& E) {
;     ...
;         E(acc, cur, wr, wc, fr, fq);
;         if (!has_next) break;
; #pragma unroll
;         for (int a = 0; a < 2; ++a)
; #pragma unroll
;             for (int b = 0; b < 2; ++b)
; #pragma unroll
;                 for (int m = 0; m < 4; ++m)
; #pragma unroll
;                     for (int n = 0; n < 2; ++n) acc[a][b][m][n] = (f32x4){0.f, 0.f, 0.f, 0.f};
;         cur = nxt; cB = nB; c00 = n00; c01 = n01; c10 = n10; c11 = n11; ++ui;
;     }
;     PG8_WAIT_V(0);
;     if (wr == 0) PG8_BAR;
;     PG8_BAR;
;     __device__ __forceinline__ void operator()(const f32x4 (&acc)[2][2][4][2], const Unit& u, int wr, int wc, int fr, int fq) const {
;     ...
;             for (int m = 0; m < 4; ++m) { const size_t ro = (size_t)(row0 + ai * HALF + m * 16) * D + col0;
; #pragma unroll
;                 for (int bj = 0; bj < 2; ++bj)
; #pragma unroll
;                     for (int n = 0; n < 2; ++n) *(f32x4*)(out + ro + bj * HALF + n * 16) = xv[m][bj][n] + gv[bj][n] * acc[ai][bj][m][n]; }
	v_pk_fma_f32 v[64:65], v[64:65], v[144:145], v[68:69]
	v_pk_fma_f32 v[62:63], v[62:63], v[142:143], v[66:67]
	v_pk_fma_f32 v[58:59], v[58:59], v[134:135], v[70:71]
	v_pk_fma_f32 v[36:37], v[36:37], v[132:133], v[80:81]
	v_pk_fma_f32 v[34:35], v[34:35], v[130:131], v[78:79]
	v_pk_fma_f32 v[50:51], v[50:51], v[134:135], v[86:87]
	v_pk_fma_f32 v[24:25], v[24:25], v[132:133], v[96:97]
	v_pk_fma_f32 v[22:23], v[22:23], v[130:131], v[94:95]
	v_pk_fma_f32 v[38:39], v[38:39], v[134:135], v[102:103]
	v_pk_fma_f32 v[12:13], v[12:13], v[132:133], v[112:113]
	v_pk_fma_f32 v[10:11], v[10:11], v[130:131], v[110:111]
	v_pk_fma_f32 v[18:19], v[18:19], v[134:135], v[118:119]
	v_pk_fma_f32 v[4:5], v[4:5], v[132:133], v[128:129]
	v_pk_fma_f32 v[2:3], v[2:3], v[130:131], v[126:127]
	v_mov_b32_e32 v131, v173
	v_mov_b32_e32 v130, v174
	v_mov_b32_e32 v132, v175
	v_mov_b32_e32 v134, v176
	v_pk_fma_f32 v[60:61], v[60:61], v[136:137], v[72:73]
	v_pk_fma_f32 v[44:45], v[44:45], v[140:141], v[76:77]
	v_pk_fma_f32 v[42:43], v[42:43], v[138:139], v[74:75]
	v_pk_fma_f32 v[56:57], v[56:57], v[144:145], v[84:85]
	v_pk_fma_f32 v[54:55], v[54:55], v[142:143], v[82:83]
	v_pk_fma_f32 v[52:53], v[52:53], v[136:137], v[88:89]
	v_pk_fma_f32 v[28:29], v[28:29], v[140:141], v[92:93]
	v_pk_fma_f32 v[26:27], v[26:27], v[138:139], v[90:91]
	v_pk_fma_f32 v[48:49], v[48:49], v[144:145], v[100:101]
	v_pk_fma_f32 v[46:47], v[46:47], v[142:143], v[98:99]
	v_pk_fma_f32 v[40:41], v[40:41], v[136:137], v[104:105]
	v_pk_fma_f32 v[16:17], v[16:17], v[140:141], v[108:109]
	v_pk_fma_f32 v[14:15], v[14:15], v[138:139], v[106:107]
	v_pk_fma_f32 v[32:33], v[32:33], v[144:145], v[116:117]
	v_pk_fma_f32 v[30:31], v[30:31], v[142:143], v[114:115]
	v_pk_fma_f32 v[20:21], v[20:21], v[136:137], v[120:121]
	v_pk_fma_f32 v[8:9], v[8:9], v[140:141], v[124:125]
	v_pk_fma_f32 v[6:7], v[6:7], v[138:139], v[122:123]
	global_store_dwordx4 v[158:159], v[62:65], off
	global_store_dwordx4 v[158:159], v[58:61], off offset:64
	global_store_dwordx4 v[158:159], v[42:45], off offset:512
	global_store_dwordx4 v[158:159], v[34:37], off offset:576
	global_store_dwordx4 v[178:179], v[54:57], off
	global_store_dwordx4 v[178:179], v[50:53], off offset:64
	global_store_dwordx4 v[178:179], v[26:29], off offset:512
	global_store_dwordx4 v[178:179], v[22:25], off offset:576
	global_store_dwordx4 v[180:181], v[46:49], off
	global_store_dwordx4 v[180:181], v[38:41], off offset:64
	global_store_dwordx4 v[180:181], v[14:17], off offset:512
	global_store_dwordx4 v[180:181], v[10:13], off offset:576
	global_store_dwordx4 v[156:157], v[30:33], off
	global_store_dwordx4 v[156:157], v[18:21], off offset:64
	global_store_dwordx4 v[156:157], v[6:9], off offset:512
	global_store_dwordx4 v[156:157], v[2:5], off offset:576
	s_cbranch_vccz .LBB0_933
	s_waitcnt vmcnt(0)
	s_cmpk_gt_u32 s33, 0xff
	s_cbranch_scc1 .LBB0_946
	s_barrier

; #define PG8_STAGE(bufoff, gbase, v0, v1) do { \
;         __builtin_amdgcn_global_load_lds((const unsigned*)((const char*)(gbase) + (v0)), (LAS unsigned*)(lds + (bufoff) + ldsw), 16, 0, 0); \
;         __builtin_amdgcn_global_load_lds((const unsigned*)((const char*)(gbase) + (v1)), (LAS unsigned*)(lds + (bufoff) + ldsw + 8192), 16, 0, 0); } while (0)
; #define PG8_LDA(dst, b, h) do { _Pragma("unroll") for (int m = 0; m < 4; ++m) _Pragma("unroll") for (int k = 0; k < 2; ++k) dst[m][k] = *(const LAS bf16x8*)(lds + PG8_SA(b, h) + aoff + m * 2048 + k * 1024); } while (0)
; #define PG8_LDB(dst, b, h) do { _Pragma("unroll") for (int n = 0; n < 2; ++n) _Pragma("unroll") for (int k = 0; k < 2; ++k) dst[n][k] = *(const LAS bf16x8*)(lds + PG8_SB(b, h) + boff + n * 2048 + k * 1024); } while (0)
; #define PG8_WAIT_V(n) asm volatile("s_waitcnt vmcnt(" #n ")" ::: "memory")
; #define PG8_WAIT_L(n) asm volatile("s_waitcnt lgkmcnt(" #n ")" ::: "memory")
; #define PG8_BAR __builtin_amdgcn_s_barrier()
; #define PG8_SCHED __builtin_amdgcn_sched_barrier(0)
; template <class Epi, class Sched>
; __device__ __forceinline__ void gemm_phase(LAS unsigned char* lds, const int K, const Sched& S, const Epi& E) {
;     ...
;         for (int t = 0; t < nt; t += 2) {
;             const bool last = (t == nt - 2);
;             const char* a1 = gA + (size_t)(t + 1) * kstep;
;             const char* a2 = last ? gA : gA + (size_t)(t + 2) * kstep; const char* b2 = last ? nB : cB + (size_t)(t + 2) * kstepB;
;             const char* a3 = a2 + kstep; const char* b3 = b2 + kstepB;
;             const unsigned x00 = last ? n00 : c00, x01 = last ? n01 : c01, x10 = last ? n10 : c10, x11 = last ? n11 : c11;
;             PG8_LDB(B0, 0, 0); PG8_SCHED; PG8_LDA(At, 0, 0); PG8_STAGE(PG8_SA(1, 1), a1, c10, c11);
;             PG8_WAIT_L(8); PG8_BAR; PG8_WAIT_L(0); PG8_MMA(0, 0, At, B0); PG8_BAR; PG8_SCHED;
;             PG8_LDB(B1, 0, 1); PG8_STAGE(PG8_SB(0, 0), b2, voffB0, voffB1);
;             PG8_BAR; PG8_WAIT_L(0); PG8_MMA(0, 1, At, B1); PG8_BAR;
;             PG8_LDA(At, 0, 1); PG8_STAGE(PG8_SA(0, 0), a2, x00, x01);
;             PG8_BAR; PG8_WAIT_L(0); PG8_MMA(1, 0, At, B0); PG8_BAR; PG8_SCHED;
;             PG8_STAGE(PG8_SB(0, 1), b2 + hstep, voffB0, voffB1);
;             PG8_WAIT_V(6); PG8_BAR; PG8_MMA(1, 1, At, B1); PG8_BAR;
.LBB0_1094:
	v_add_u32_e32 v139, s46, v149
	s_add_u32 s22, s0, s20
	ds_read_b128 v[160:163], v139
	ds_read_b128 v[164:167], v139 offset:1024
	ds_read_b128 v[168:171], v139 offset:2048
	ds_read_b128 v[172:175], v139 offset:3072
	s_addc_u32 s23, s1, s21
	s_add_u32 s24, s22, 0x34c30100
	s_addc_u32 s25, s23, 0
	s_cmpk_eq_i32 s20, 0xf00
	s_cselect_b64 vcc, -1, 0
	s_and_b64 s[22:23], vcc, exec
	v_cndmask_b32_e32 v134, v158, v156, vcc
	s_cselect_b32 s27, s3, s25
	s_cselect_b32 s26, s2, s24
	v_cndmask_b32_e32 v139, v138, v154, vcc
	s_cselect_b32 s23, s19, s15
	s_cselect_b32 s22, s18, s13
	v_cndmask_b32_e32 v204, v136, v155, vcc
	s_add_u32 s24, s22, 0x20000
	s_addc_u32 s25, s23, 0
	v_lshl_add_u64 v[206:207], v[144:145], 0, s[20:21]
	s_add_i32 m0, s37, 0xc000
	ds_read_b128 v[176:179], v151
	ds_read_b128 v[180:183], v151 offset:1024
	ds_read_b128 v[184:187], v151 offset:2048
	ds_read_b128 v[188:191], v151 offset:3072
	ds_read_b128 v[192:195], v151 offset:4096
	ds_read_b128 v[196:199], v151 offset:5120
	ds_read_b128 v[200:203], v151 offset:6144
	ds_read_b128 v[208:211], v151 offset:7168
	global_load_lds_dwordx4 v[206:207], off
	v_lshl_add_u64 v[206:207], v[142:143], 0, s[20:21]
	s_add_i32 m0, s37, 0xe000
	s_nop 0
	global_load_lds_dwordx4 v[206:207], off
	s_waitcnt lgkmcnt(8)
	s_barrier
	s_waitcnt lgkmcnt(0)
	s_setprio 1
	v_mfma_f32_16x16x32_bf16 v[126:129], v[160:163], v[176:179], v[126:129]
	v_mfma_f32_16x16x32_bf16 v[122:125], v[168:171], v[176:179], v[122:125]
	v_mfma_f32_16x16x32_bf16 v[110:113], v[160:163], v[184:187], v[110:113]
	v_mfma_f32_16x16x32_bf16 v[106:109], v[168:171], v[184:187], v[106:109]
	v_mfma_f32_16x16x32_bf16 v[94:97], v[160:163], v[192:195], v[94:97]
	v_mfma_f32_16x16x32_bf16 v[90:93], v[168:171], v[192:195], v[90:93]
	v_mfma_f32_16x16x32_bf16 v[78:81], v[160:163], v[200:203], v[78:81]
	v_mfma_f32_16x16x32_bf16 v[74:77], v[168:171], v[200:203], v[74:77]
	v_mfma_f32_16x16x32_bf16 v[126:129], v[164:167], v[180:183], v[126:129]
	v_mfma_f32_16x16x32_bf16 v[122:125], v[172:175], v[180:183], v[122:125]
	v_mfma_f32_16x16x32_bf16 v[110:113], v[164:167], v[188:191], v[110:113]
	v_mfma_f32_16x16x32_bf16 v[106:109], v[172:175], v[188:191], v[106:109]
	v_mfma_f32_16x16x32_bf16 v[94:97], v[164:167], v[196:199], v[94:97]
	v_mfma_f32_16x16x32_bf16 v[90:93], v[172:175], v[196:199], v[90:93]
	v_mfma_f32_16x16x32_bf16 v[78:81], v[164:167], v[208:211], v[78:81]
	v_mfma_f32_16x16x32_bf16 v[74:77], v[172:175], v[208:211], v[74:77]
	s_setprio 0
	s_barrier
	s_add_i32 s55, s46, s36
	v_add_u32_e32 v141, s48, v149
	v_lshl_add_u64 v[206:207], s[22:23], 0, v[130:131]
	s_mov_b32 m0, s55
	ds_read_b128 v[212:215], v141
	ds_read_b128 v[216:219], v141 offset:1024
	ds_read_b128 v[220:223], v141 offset:2048
	ds_read_b128 v[224:227], v141 offset:3072
	global_load_lds_dwordx4 v[206:207], off
	v_lshl_add_u64 v[228:229], s[22:23], 0, v[132:133]
	s_add_i32 m0, s55, 0x2000
	s_nop 0
	global_load_lds_dwordx4 v[228:229], off
	s_barrier
	s_waitcnt lgkmcnt(0)
	s_setprio 1
	v_mfma_f32_16x16x32_bf16 v[118:121], v[212:215], v[176:179], v[118:121]
	v_mfma_f32_16x16x32_bf16 v[114:117], v[220:223], v[176:179], v[114:117]
	v_mfma_f32_16x16x32_bf16 v[102:105], v[212:215], v[184:187], v[102:105]
	v_mfma_f32_16x16x32_bf16 v[98:101], v[220:223], v[184:187], v[98:101]
	v_mfma_f32_16x16x32_bf16 v[86:89], v[212:215], v[192:195], v[86:89]
	v_mfma_f32_16x16x32_bf16 v[82:85], v[220:223], v[192:195], v[82:85]
	v_mfma_f32_16x16x32_bf16 v[70:73], v[212:215], v[200:203], v[70:73]
	v_mfma_f32_16x16x32_bf16 v[66:69], v[220:223], v[200:203], v[66:69]
	v_mfma_f32_16x16x32_bf16 v[118:121], v[216:219], v[180:183], v[118:121]
	v_mfma_f32_16x16x32_bf16 v[114:117], v[224:227], v[180:183], v[114:117]
	v_mfma_f32_16x16x32_bf16 v[102:105], v[216:219], v[188:191], v[102:105]
	v_mfma_f32_16x16x32_bf16 v[98:101], v[224:227], v[188:191], v[98:101]
	v_mfma_f32_16x16x32_bf16 v[86:89], v[216:219], v[196:199], v[86:89]
	v_mfma_f32_16x16x32_bf16 v[82:85], v[224:227], v[196:199], v[82:85]
	v_mfma_f32_16x16x32_bf16 v[70:73], v[216:219], v[208:211], v[70:73]
	v_mfma_f32_16x16x32_bf16 v[66:69], v[224:227], v[208:211], v[66:69]
	s_setprio 0
	s_mov_b32 m0, s37
	s_barrier
	ds_read_b128 v[176:179], v151 offset:16384
	ds_read_b128 v[180:183], v151 offset:17408
	ds_read_b128 v[184:187], v151 offset:18432
	ds_read_b128 v[188:191], v151 offset:19456
	ds_read_b128 v[192:195], v151 offset:20480
	ds_read_b128 v[196:199], v151 offset:21504
	ds_read_b128 v[200:203], v151 offset:22528
	ds_read_b128 v[208:211], v151 offset:23552
	global_load_lds_dwordx4 v134, s[26:27]
	s_mov_b32 m0, s38
	v_mov_b32_e32 v205, v135
	global_load_lds_dwordx4 v204, s[26:27]
	s_barrier
	s_waitcnt lgkmcnt(0)
	v_lshl_add_u64 v[230:231], s[26:27], 0, v[134:135]
	v_lshl_add_u64 v[204:205], s[26:27], 0, v[204:205]
	s_setprio 1
	s_waitcnt lgkmcnt(0)
	v_mfma_f32_16x16x32_bf16 v[62:65], v[160:163], v[176:179], v[62:65]
	v_mfma_f32_16x16x32_bf16 v[58:61], v[168:171], v[176:179], v[58:61]
	v_mfma_f32_16x16x32_bf16 v[46:49], v[160:163], v[184:187], v[46:49]
	v_mfma_f32_16x16x32_bf16 v[42:45], v[168:171], v[184:187], v[42:45]
	v_mfma_f32_16x16x32_bf16 v[30:33], v[160:163], v[192:195], v[30:33]
	v_mfma_f32_16x16x32_bf16 v[26:29], v[168:171], v[192:195], v[26:29]
	v_mfma_f32_16x16x32_bf16 v[14:17], v[160:163], v[200:203], v[14:17]
	v_mfma_f32_16x16x32_bf16 v[10:13], v[168:171], v[200:203], v[10:13]
	v_mfma_f32_16x16x32_bf16 v[62:65], v[164:167], v[180:183], v[62:65]
	v_mfma_f32_16x16x32_bf16 v[58:61], v[172:175], v[180:183], v[58:61]
	v_mfma_f32_16x16x32_bf16 v[46:49], v[164:167], v[188:191], v[46:49]
	v_mfma_f32_16x16x32_bf16 v[42:45], v[172:175], v[188:191], v[42:45]
	v_mfma_f32_16x16x32_bf16 v[30:33], v[164:167], v[196:199], v[30:33]
	v_mfma_f32_16x16x32_bf16 v[26:29], v[172:175], v[196:199], v[26:29]
	v_mfma_f32_16x16x32_bf16 v[14:17], v[164:167], v[208:211], v[14:17]
	v_mfma_f32_16x16x32_bf16 v[10:13], v[172:175], v[208:211], v[10:13]
	s_setprio 0
	s_barrier
	s_add_i32 s55, s48, s36
	v_lshl_add_u64 v[160:161], v[206:207], 0, s[4:5]
	s_mov_b32 m0, s55
	s_nop 0
	global_load_lds_dwordx4 v[160:161], off
	v_lshl_add_u64 v[160:161], v[228:229], 0, s[4:5]
	s_add_i32 m0, s55, 0x2000
	s_nop 0
	global_load_lds_dwordx4 v[160:161], off
	s_cmp_eq_u32 s82, 0
	s_cbranch_scc1 .Lpb8_p4n
	s_waitcnt vmcnt(14)
	v_cvt_pk_bf16_f32 v244, v244, v245
	v_cvt_pk_bf16_f32 v245, v246, v247
	v_cvt_pk_bf16_f32 v246, v248, v249
	v_cvt_pk_bf16_f32 v247, v250, v251
	global_store_dwordx4 v253, v[244:247], s[78:79] nt
	s_mov_b32 s82, 0
	s_waitcnt vmcnt(7)
	s_branch .Lpb8_p4j

; #define PG8_STAGE(bufoff, gbase, v0, v1) do { \
;         __builtin_amdgcn_global_load_lds((const unsigned*)((const char*)(gbase) + (v0)), (LAS unsigned*)(lds + (bufoff) + ldsw), 16, 0, 0); \
;         __builtin_amdgcn_global_load_lds((const unsigned*)((const char*)(gbase) + (v1)), (LAS unsigned*)(lds + (bufoff) + ldsw + 8192), 16, 0, 0); } while (0)
; #define PG8_LDA(dst, b, h) do { _Pragma("unroll") for (int m = 0; m < 4; ++m) _Pragma("unroll") for (int k = 0; k < 2; ++k) dst[m][k] = *(const LAS bf16x8*)(lds + PG8_SA(b, h) + aoff + m * 2048 + k * 1024); } while (0)
; #define PG8_LDB(dst, b, h) do { _Pragma("unroll") for (int n = 0; n < 2; ++n) _Pragma("unroll") for (int k = 0; k < 2; ++k) dst[n][k] = *(const LAS bf16x8*)(lds + PG8_SB(b, h) + boff + n * 2048 + k * 1024); } while (0)
; #define PG8_MMA(ai, bj, At, Bt) do { __builtin_amdgcn_s_setprio(1); _Pragma("unroll") for (int m = 0; m < 4; ++m) _Pragma("unroll") for (int n = 0; n < 2; ++n) _Pragma("unroll") for (int k = 0; k < 2; ++k) \
;         acc[ai][bj][m][n] = __builtin_amdgcn_mfma_f32_16x16x32_bf16(Bt[n][k], At[m][k], acc[ai][bj][m][n], 0, 0, 0); __builtin_amdgcn_s_setprio(0); } while (0)
; #define PG8_WAIT_V(n) asm volatile("s_waitcnt vmcnt(" #n ")" ::: "memory")
; #define PG8_WAIT_L(n) asm volatile("s_waitcnt lgkmcnt(" #n ")" ::: "memory")
; #define PG8_BAR __builtin_amdgcn_s_barrier()
; #define PG8_SCHED __builtin_amdgcn_sched_barrier(0)
; template <class Epi, class Sched>
; __device__ __forceinline__ void gemm_phase(LAS unsigned char* lds, const int K, const Sched& S, const Epi& E) {
;     ...
;             PG8_LDB(B0, 1, 0); PG8_SCHED; PG8_LDA(At, 1, 0); PG8_STAGE(PG8_SA(0, 1), a2, x10, x11);
;             PG8_WAIT_L(8); PG8_BAR; PG8_WAIT_L(0); PG8_MMA(0, 0, At, B0); PG8_BAR; PG8_SCHED;
;             PG8_LDB(B1, 1, 1); PG8_STAGE(PG8_SB(1, 0), b3, voffB0, voffB1);
;             PG8_BAR; PG8_WAIT_L(0); PG8_MMA(0, 1, At, B1); PG8_BAR;
;             PG8_LDA(At, 1, 1); PG8_STAGE(PG8_SA(1, 0), a3, x00, x01);
;             PG8_BAR; PG8_WAIT_L(0); PG8_MMA(1, 0, At, B0); PG8_BAR; PG8_SCHED;
;             PG8_STAGE(PG8_SB(1, 1), b3 + hstep, voffB0, voffB1);
;             PG8_WAIT_V(6); PG8_BAR; PG8_MMA(1, 1, At, B1); PG8_BAR;
.Lpb8_p5n:
	s_waitcnt lgkmcnt(8)
	s_barrier
	s_waitcnt lgkmcnt(0)
	s_setprio 1
	v_mfma_f32_16x16x32_bf16 v[126:129], v[160:163], v[176:179], v[126:129]
	v_mfma_f32_16x16x32_bf16 v[122:125], v[168:171], v[176:179], v[122:125]
	v_mfma_f32_16x16x32_bf16 v[110:113], v[160:163], v[184:187], v[110:113]
	v_mfma_f32_16x16x32_bf16 v[106:109], v[168:171], v[184:187], v[106:109]
	v_mfma_f32_16x16x32_bf16 v[94:97], v[160:163], v[192:195], v[94:97]
	v_mfma_f32_16x16x32_bf16 v[90:93], v[168:171], v[192:195], v[90:93]
	v_mfma_f32_16x16x32_bf16 v[78:81], v[160:163], v[200:203], v[78:81]
	v_mfma_f32_16x16x32_bf16 v[74:77], v[168:171], v[200:203], v[74:77]
	v_mfma_f32_16x16x32_bf16 v[126:129], v[164:167], v[180:183], v[126:129]
	v_mfma_f32_16x16x32_bf16 v[122:125], v[172:175], v[180:183], v[122:125]
	v_mfma_f32_16x16x32_bf16 v[110:113], v[164:167], v[188:191], v[110:113]
	v_mfma_f32_16x16x32_bf16 v[106:109], v[172:175], v[188:191], v[106:109]
	v_mfma_f32_16x16x32_bf16 v[94:97], v[164:167], v[196:199], v[94:97]
	v_mfma_f32_16x16x32_bf16 v[90:93], v[172:175], v[196:199], v[90:93]
	v_mfma_f32_16x16x32_bf16 v[78:81], v[164:167], v[208:211], v[78:81]
	v_mfma_f32_16x16x32_bf16 v[74:77], v[172:175], v[208:211], v[74:77]
	s_setprio 0
	s_barrier
	s_add_i32 s26, 0, 0x1c000
	s_add_i32 s27, s55, s36
	v_add_u32_e32 v134, s26, v149
	v_lshl_add_u64 v[206:207], s[24:25], 0, v[130:131]
	s_mov_b32 m0, s27
	ds_read_b128 v[212:215], v134
	ds_read_b128 v[216:219], v134 offset:1024
	ds_read_b128 v[220:223], v134 offset:2048
	ds_read_b128 v[224:227], v134 offset:3072
	global_load_lds_dwordx4 v[206:207], off
	v_lshl_add_u64 v[206:207], s[24:25], 0, v[132:133]
	s_add_i32 m0, s27, 0x2000
	s_nop 0
	global_load_lds_dwordx4 v[206:207], off
	s_barrier
	s_waitcnt lgkmcnt(0)
	s_setprio 1
	v_mfma_f32_16x16x32_bf16 v[118:121], v[212:215], v[176:179], v[118:121]
	v_mfma_f32_16x16x32_bf16 v[114:117], v[220:223], v[176:179], v[114:117]
	v_mfma_f32_16x16x32_bf16 v[102:105], v[212:215], v[184:187], v[102:105]
	v_mfma_f32_16x16x32_bf16 v[98:101], v[220:223], v[184:187], v[98:101]
	v_mfma_f32_16x16x32_bf16 v[86:89], v[212:215], v[192:195], v[86:89]
	v_mfma_f32_16x16x32_bf16 v[82:85], v[220:223], v[192:195], v[82:85]
	v_mfma_f32_16x16x32_bf16 v[70:73], v[212:215], v[200:203], v[70:73]
	v_mfma_f32_16x16x32_bf16 v[66:69], v[220:223], v[200:203], v[66:69]
	v_mfma_f32_16x16x32_bf16 v[118:121], v[216:219], v[180:183], v[118:121]
	v_mfma_f32_16x16x32_bf16 v[114:117], v[224:227], v[180:183], v[114:117]
	v_mfma_f32_16x16x32_bf16 v[102:105], v[216:219], v[188:191], v[102:105]
	v_mfma_f32_16x16x32_bf16 v[98:101], v[224:227], v[188:191], v[98:101]
	v_mfma_f32_16x16x32_bf16 v[86:89], v[216:219], v[196:199], v[86:89]
	v_mfma_f32_16x16x32_bf16 v[82:85], v[224:227], v[196:199], v[82:85]
	v_mfma_f32_16x16x32_bf16 v[70:73], v[216:219], v[208:211], v[70:73]
	v_mfma_f32_16x16x32_bf16 v[66:69], v[224:227], v[208:211], v[66:69]
	s_setprio 0
	s_mov_b32 m0, s43
	v_lshl_add_u64 v[206:207], v[230:231], 0, s[10:11]
	s_barrier
	ds_read_b128 v[176:179], v151 offset:49152
	ds_read_b128 v[180:183], v151 offset:50176
	ds_read_b128 v[184:187], v151 offset:51200
	ds_read_b128 v[188:191], v151 offset:52224
	ds_read_b128 v[192:195], v151 offset:53248
	ds_read_b128 v[196:199], v151 offset:54272
	ds_read_b128 v[200:203], v151 offset:55296
	ds_read_b128 v[208:211], v151 offset:56320
	global_load_lds_dwordx4 v[206:207], off
	v_lshl_add_u64 v[204:205], v[204:205], 0, s[10:11]
	s_mov_b32 m0, s44
	s_nop 0
	global_load_lds_dwordx4 v[204:205], off
	s_barrier
	s_waitcnt lgkmcnt(0)
	s_setprio 1
	v_mfma_f32_16x16x32_bf16 v[62:65], v[160:163], v[176:179], v[62:65]
	v_mfma_f32_16x16x32_bf16 v[58:61], v[168:171], v[176:179], v[58:61]
	v_mfma_f32_16x16x32_bf16 v[46:49], v[160:163], v[184:187], v[46:49]
	v_mfma_f32_16x16x32_bf16 v[42:45], v[168:171], v[184:187], v[42:45]
	v_mfma_f32_16x16x32_bf16 v[30:33], v[160:163], v[192:195], v[30:33]
	v_mfma_f32_16x16x32_bf16 v[26:29], v[168:171], v[192:195], v[26:29]
	v_mfma_f32_16x16x32_bf16 v[14:17], v[160:163], v[200:203], v[14:17]
	v_mfma_f32_16x16x32_bf16 v[10:13], v[168:171], v[200:203], v[10:13]
	v_mfma_f32_16x16x32_bf16 v[62:65], v[164:167], v[180:183], v[62:65]
	v_mfma_f32_16x16x32_bf16 v[58:61], v[172:175], v[180:183], v[58:61]
	v_mfma_f32_16x16x32_bf16 v[46:49], v[164:167], v[188:191], v[46:49]
	v_mfma_f32_16x16x32_bf16 v[42:45], v[172:175], v[188:191], v[42:45]
	v_mfma_f32_16x16x32_bf16 v[30:33], v[164:167], v[196:199], v[30:33]
	v_mfma_f32_16x16x32_bf16 v[26:29], v[172:175], v[196:199], v[26:29]
	v_mfma_f32_16x16x32_bf16 v[14:17], v[164:167], v[208:211], v[14:17]
	v_mfma_f32_16x16x32_bf16 v[10:13], v[172:175], v[208:211], v[10:13]
	s_setprio 0
	s_barrier
	s_add_u32 s22, s22, 0x20800
	s_addc_u32 s23, s23, 0
	s_add_i32 s24, s26, s36
	v_lshl_add_u64 v[160:161], s[22:23], 0, v[130:131]
	s_mov_b32 m0, s24
	s_nop 0
	global_load_lds_dwordx4 v[160:161], off
	v_lshl_add_u64 v[160:161], s[22:23], 0, v[132:133]
	s_add_i32 m0, s24, 0x2000
	s_nop 0
	global_load_lds_dwordx4 v[160:161], off
	s_cmp_eq_u32 s82, 0
	s_cbranch_scc1 .Lpb8_p8n
	s_waitcnt vmcnt(14)
	s_branch .Lpb8_p8j

; #define PG8_STAGE(bufoff, gbase, v0, v1) do { \
;         __builtin_amdgcn_global_load_lds((const unsigned*)((const char*)(gbase) + (v0)), (LAS unsigned*)(lds + (bufoff) + ldsw), 16, 0, 0); \
;         __builtin_amdgcn_global_load_lds((const unsigned*)((const char*)(gbase) + (v1)), (LAS unsigned*)(lds + (bufoff) + ldsw + 8192), 16, 0, 0); } while (0)
; #define PG8_LDA(dst, b, h) do { _Pragma("unroll") for (int m = 0; m < 4; ++m) _Pragma("unroll") for (int k = 0; k < 2; ++k) dst[m][k] = *(const LAS bf16x8*)(lds + PG8_SA(b, h) + aoff + m * 2048 + k * 1024); } while (0)
; #define PG8_LDB(dst, b, h) do { _Pragma("unroll") for (int n = 0; n < 2; ++n) _Pragma("unroll") for (int k = 0; k < 2; ++k) dst[n][k] = *(const LAS bf16x8*)(lds + PG8_SB(b, h) + boff + n * 2048 + k * 1024); } while (0)
; #define PG8_WAIT_V(n) asm volatile("s_waitcnt vmcnt(" #n ")" ::: "memory")
; #define PG8_WAIT_L(n) asm volatile("s_waitcnt lgkmcnt(" #n ")" ::: "memory")
; #define PG8_BAR __builtin_amdgcn_s_barrier()
; #define PG8_SCHED __builtin_amdgcn_sched_barrier(0)
; template <class Epi, class Sched>
; __device__ __forceinline__ void gemm_phase(LAS unsigned char* lds, const int K, const Sched& S, const Epi& E) {
;     ...
;         for (int t = 0; t < nt; t += 2) {
;             const bool last = (t == nt - 2);
;             const char* a1 = gA + (size_t)(t + 1) * kstep;
;             const char* a2 = last ? gA : gA + (size_t)(t + 2) * kstep; const char* b2 = last ? nB : cB + (size_t)(t + 2) * kstepB;
;             const char* a3 = a2 + kstep; const char* b3 = b2 + kstepB;
;             const unsigned x00 = last ? n00 : c00, x01 = last ? n01 : c01, x10 = last ? n10 : c10, x11 = last ? n11 : c11;
;             PG8_LDB(B0, 0, 0); PG8_SCHED; PG8_LDA(At, 0, 0); PG8_STAGE(PG8_SA(1, 1), a1, c10, c11);
;             PG8_WAIT_L(8); PG8_BAR; PG8_WAIT_L(0); PG8_MMA(0, 0, At, B0); PG8_BAR; PG8_SCHED;
;             PG8_LDB(B1, 0, 1); PG8_STAGE(PG8_SB(0, 0), b2, voffB0, voffB1);
;             PG8_BAR; PG8_WAIT_L(0); PG8_MMA(0, 1, At, B1); PG8_BAR;
;             PG8_LDA(At, 0, 1); PG8_STAGE(PG8_SA(0, 0), a2, x00, x01);
;             PG8_BAR; PG8_WAIT_L(0); PG8_MMA(1, 0, At, B0); PG8_BAR; PG8_SCHED;
;             PG8_STAGE(PG8_SB(0, 1), b2 + hstep, voffB0, voffB1);
;             PG8_WAIT_V(6); PG8_BAR; PG8_MMA(1, 1, At, B1); PG8_BAR;
.LBB0_1161:
	s_add_u32 s40, s0, s38
	ds_read_b128 v[164:167], v153
	ds_read_b128 v[168:171], v153 offset:1024
	ds_read_b128 v[172:175], v153 offset:2048
	ds_read_b128 v[176:179], v153 offset:3072
	s_addc_u32 s41, s1, s39
	s_add_u32 s42, s40, 0x3ee90100
	s_addc_u32 s43, s41, 0
	s_cmpk_eq_i32 s38, 0x300
	s_cselect_b64 vcc, -1, 0
	s_and_b64 s[40:41], vcc, exec
	v_cndmask_b32_e32 v134, v162, v157, vcc
	s_cselect_b32 s45, s3, s43
	s_cselect_b32 s44, s2, s42
	v_cndmask_b32_e32 v139, v138, v159, vcc
	s_cselect_b32 s41, s37, s31
	s_cselect_b32 s40, s36, s29
	v_cndmask_b32_e32 v204, v136, v158, vcc
	s_add_u32 s42, s40, 0x40000
	s_addc_u32 s43, s41, 0
	v_lshl_add_u64 v[206:207], v[144:145], 0, s[38:39]
	s_add_i32 m0, s49, 0xc000
	ds_read_b128 v[180:183], v154
	ds_read_b128 v[184:187], v154 offset:1024
	ds_read_b128 v[188:191], v154 offset:2048
	ds_read_b128 v[192:195], v154 offset:3072
	ds_read_b128 v[196:199], v154 offset:4096
	ds_read_b128 v[200:203], v154 offset:5120
	ds_read_b128 v[208:211], v154 offset:6144
	ds_read_b128 v[212:215], v154 offset:7168
	global_load_lds_dwordx4 v[206:207], off
	v_lshl_add_u64 v[206:207], v[142:143], 0, s[38:39]
	s_add_i32 m0, s49, 0xe000
	s_nop 0
	global_load_lds_dwordx4 v[206:207], off
	s_waitcnt lgkmcnt(8)
	s_barrier
	s_waitcnt lgkmcnt(0)
	s_setprio 1
	v_mfma_f32_16x16x32_bf16 v[126:129], v[164:167], v[180:183], v[126:129]
	v_mfma_f32_16x16x32_bf16 v[122:125], v[172:175], v[180:183], v[122:125]
	v_mfma_f32_16x16x32_bf16 v[114:117], v[164:167], v[188:191], v[114:117]
	v_mfma_f32_16x16x32_bf16 v[106:109], v[172:175], v[188:191], v[106:109]
	v_mfma_f32_16x16x32_bf16 v[98:101], v[164:167], v[196:199], v[98:101]
	v_mfma_f32_16x16x32_bf16 v[90:93], v[172:175], v[196:199], v[90:93]
	v_mfma_f32_16x16x32_bf16 v[82:85], v[164:167], v[208:211], v[82:85]
	v_mfma_f32_16x16x32_bf16 v[74:77], v[172:175], v[208:211], v[74:77]
	v_mfma_f32_16x16x32_bf16 v[126:129], v[168:171], v[184:187], v[126:129]
	v_mfma_f32_16x16x32_bf16 v[122:125], v[176:179], v[184:187], v[122:125]
	v_mfma_f32_16x16x32_bf16 v[114:117], v[168:171], v[192:195], v[114:117]
	v_mfma_f32_16x16x32_bf16 v[106:109], v[176:179], v[192:195], v[106:109]
	v_mfma_f32_16x16x32_bf16 v[98:101], v[168:171], v[200:203], v[98:101]
	v_mfma_f32_16x16x32_bf16 v[90:93], v[176:179], v[200:203], v[90:93]
	v_mfma_f32_16x16x32_bf16 v[82:85], v[168:171], v[212:215], v[82:85]
	v_mfma_f32_16x16x32_bf16 v[74:77], v[176:179], v[212:215], v[74:77]
	s_setprio 0
	s_barrier
	s_add_i32 s67, s59, s48
	v_lshl_add_u64 v[206:207], s[40:41], 0, v[132:133]
	s_mov_b32 m0, s67
	ds_read_b128 v[216:219], v155
	ds_read_b128 v[220:223], v155 offset:1024
	ds_read_b128 v[224:227], v155 offset:2048
	ds_read_b128 v[228:231], v155 offset:3072
	global_load_lds_dwordx4 v[206:207], off
	v_lshl_add_u64 v[232:233], s[40:41], 0, v[130:131]
	s_add_i32 m0, s67, 0x2000
	s_nop 0
	global_load_lds_dwordx4 v[232:233], off
	s_barrier
	s_waitcnt lgkmcnt(0)
	s_setprio 1
	v_mfma_f32_16x16x32_bf16 v[118:121], v[216:219], v[180:183], v[118:121]
	v_mfma_f32_16x16x32_bf16 v[110:113], v[224:227], v[180:183], v[110:113]
	v_mfma_f32_16x16x32_bf16 v[102:105], v[216:219], v[188:191], v[102:105]
	v_mfma_f32_16x16x32_bf16 v[94:97], v[224:227], v[188:191], v[94:97]
	v_mfma_f32_16x16x32_bf16 v[86:89], v[216:219], v[196:199], v[86:89]
	v_mfma_f32_16x16x32_bf16 v[78:81], v[224:227], v[196:199], v[78:81]
	v_mfma_f32_16x16x32_bf16 v[70:73], v[216:219], v[208:211], v[70:73]
	v_mfma_f32_16x16x32_bf16 v[66:69], v[224:227], v[208:211], v[66:69]
	v_mfma_f32_16x16x32_bf16 v[118:121], v[220:223], v[184:187], v[118:121]
	v_mfma_f32_16x16x32_bf16 v[110:113], v[228:231], v[184:187], v[110:113]
	v_mfma_f32_16x16x32_bf16 v[102:105], v[220:223], v[192:195], v[102:105]
	v_mfma_f32_16x16x32_bf16 v[94:97], v[228:231], v[192:195], v[94:97]
	v_mfma_f32_16x16x32_bf16 v[86:89], v[220:223], v[200:203], v[86:89]
	v_mfma_f32_16x16x32_bf16 v[78:81], v[228:231], v[200:203], v[78:81]
	v_mfma_f32_16x16x32_bf16 v[70:73], v[220:223], v[212:215], v[70:73]
	v_mfma_f32_16x16x32_bf16 v[66:69], v[228:231], v[212:215], v[66:69]
	s_setprio 0
	s_mov_b32 m0, s49
	s_barrier
	ds_read_b128 v[180:183], v154 offset:16384
	ds_read_b128 v[184:187], v154 offset:17408
	ds_read_b128 v[188:191], v154 offset:18432
	ds_read_b128 v[192:195], v154 offset:19456
	ds_read_b128 v[196:199], v154 offset:20480
	ds_read_b128 v[200:203], v154 offset:21504
	ds_read_b128 v[208:211], v154 offset:22528
	ds_read_b128 v[212:215], v154 offset:23552
	global_load_lds_dwordx4 v134, s[44:45]
	s_mov_b32 m0, s50
	v_mov_b32_e32 v205, v135
	global_load_lds_dwordx4 v204, s[44:45]
	s_barrier
	s_waitcnt lgkmcnt(0)
	v_lshl_add_u64 v[234:235], s[44:45], 0, v[134:135]
	v_lshl_add_u64 v[204:205], s[44:45], 0, v[204:205]
	s_setprio 1
	s_waitcnt lgkmcnt(0)
	v_mfma_f32_16x16x32_bf16 v[62:65], v[164:167], v[180:183], v[62:65]
	v_mfma_f32_16x16x32_bf16 v[58:61], v[172:175], v[180:183], v[58:61]
	v_mfma_f32_16x16x32_bf16 v[46:49], v[164:167], v[188:191], v[46:49]
	v_mfma_f32_16x16x32_bf16 v[42:45], v[172:175], v[188:191], v[42:45]
	v_mfma_f32_16x16x32_bf16 v[30:33], v[164:167], v[196:199], v[30:33]
	v_mfma_f32_16x16x32_bf16 v[26:29], v[172:175], v[196:199], v[26:29]
	v_mfma_f32_16x16x32_bf16 v[14:17], v[164:167], v[208:211], v[14:17]
	v_mfma_f32_16x16x32_bf16 v[10:13], v[172:175], v[208:211], v[10:13]
	v_mfma_f32_16x16x32_bf16 v[62:65], v[168:171], v[184:187], v[62:65]
	v_mfma_f32_16x16x32_bf16 v[58:61], v[176:179], v[184:187], v[58:61]
	v_mfma_f32_16x16x32_bf16 v[46:49], v[168:171], v[192:195], v[46:49]
	v_mfma_f32_16x16x32_bf16 v[42:45], v[176:179], v[192:195], v[42:45]
	v_mfma_f32_16x16x32_bf16 v[30:33], v[168:171], v[200:203], v[30:33]
	v_mfma_f32_16x16x32_bf16 v[26:29], v[176:179], v[200:203], v[26:29]
	v_mfma_f32_16x16x32_bf16 v[14:17], v[168:171], v[212:215], v[14:17]
	v_mfma_f32_16x16x32_bf16 v[10:13], v[176:179], v[212:215], v[10:13]
	s_setprio 0
	s_barrier
	s_add_i32 s67, s60, s48
	v_lshl_add_u64 v[164:165], v[206:207], 0, s[4:5]
	s_mov_b32 m0, s67
	s_nop 0
	global_load_lds_dwordx4 v[164:165], off
	v_lshl_add_u64 v[164:165], v[232:233], 0, s[4:5]
	s_add_i32 m0, s67, 0x2000
	s_nop 0
	global_load_lds_dwordx4 v[164:165], off
	s_cmp_eq_u32 s82, 0
	s_cbranch_scc1 .Lpb9_p4n
	s_waitcnt vmcnt(14)
	v_cvt_pk_bf16_f32 v244, v244, v245
	v_cvt_pk_bf16_f32 v245, v246, v247
	v_cvt_pk_bf16_f32 v246, v248, v249
	v_cvt_pk_bf16_f32 v247, v250, v251
	global_store_dwordx4 v253, v[244:247], s[78:79] nt
	s_mov_b32 s82, 0
	s_waitcnt vmcnt(7)
	s_branch .Lpb9_p4j

; #define PG8_STAGE(bufoff, gbase, v0, v1) do { \
;         __builtin_amdgcn_global_load_lds((const unsigned*)((const char*)(gbase) + (v0)), (LAS unsigned*)(lds + (bufoff) + ldsw), 16, 0, 0); \
;         __builtin_amdgcn_global_load_lds((const unsigned*)((const char*)(gbase) + (v1)), (LAS unsigned*)(lds + (bufoff) + ldsw + 8192), 16, 0, 0); } while (0)
; #define PG8_LDA(dst, b, h) do { _Pragma("unroll") for (int m = 0; m < 4; ++m) _Pragma("unroll") for (int k = 0; k < 2; ++k) dst[m][k] = *(const LAS bf16x8*)(lds + PG8_SA(b, h) + aoff + m * 2048 + k * 1024); } while (0)
; #define PG8_LDB(dst, b, h) do { _Pragma("unroll") for (int n = 0; n < 2; ++n) _Pragma("unroll") for (int k = 0; k < 2; ++k) dst[n][k] = *(const LAS bf16x8*)(lds + PG8_SB(b, h) + boff + n * 2048 + k * 1024); } while (0)
; #define PG8_MMA(ai, bj, At, Bt) do { __builtin_amdgcn_s_setprio(1); _Pragma("unroll") for (int m = 0; m < 4; ++m) _Pragma("unroll") for (int n = 0; n < 2; ++n) _Pragma("unroll") for (int k = 0; k < 2; ++k) \
;         acc[ai][bj][m][n] = __builtin_amdgcn_mfma_f32_16x16x32_bf16(Bt[n][k], At[m][k], acc[ai][bj][m][n], 0, 0, 0); __builtin_amdgcn_s_setprio(0); } while (0)
; #define PG8_WAIT_V(n) asm volatile("s_waitcnt vmcnt(" #n ")" ::: "memory")
; #define PG8_WAIT_L(n) asm volatile("s_waitcnt lgkmcnt(" #n ")" ::: "memory")
; #define PG8_BAR __builtin_amdgcn_s_barrier()
; #define PG8_SCHED __builtin_amdgcn_sched_barrier(0)
; template <class Epi, class Sched>
; __device__ __forceinline__ void gemm_phase(LAS unsigned char* lds, const int K, const Sched& S, const Epi& E) {
;     ...
;             PG8_LDB(B0, 1, 0); PG8_SCHED; PG8_LDA(At, 1, 0); PG8_STAGE(PG8_SA(0, 1), a2, x10, x11);
;             PG8_WAIT_L(8); PG8_BAR; PG8_WAIT_L(0); PG8_MMA(0, 0, At, B0); PG8_BAR; PG8_SCHED;
;             PG8_LDB(B1, 1, 1); PG8_STAGE(PG8_SB(1, 0), b3, voffB0, voffB1);
;             PG8_BAR; PG8_WAIT_L(0); PG8_MMA(0, 1, At, B1); PG8_BAR;
;             PG8_LDA(At, 1, 1); PG8_STAGE(PG8_SA(1, 0), a3, x00, x01);
;             PG8_BAR; PG8_WAIT_L(0); PG8_MMA(1, 0, At, B0); PG8_BAR; PG8_SCHED;
;             PG8_STAGE(PG8_SB(1, 1), b3 + hstep, voffB0, voffB1);
;             PG8_WAIT_V(6); PG8_BAR; PG8_MMA(1, 1, At, B1); PG8_BAR;
.Lpb9_p5n:
	s_waitcnt lgkmcnt(8)
	s_barrier
	s_waitcnt lgkmcnt(0)
	s_setprio 1
	v_mfma_f32_16x16x32_bf16 v[126:129], v[164:167], v[180:183], v[126:129]
	v_mfma_f32_16x16x32_bf16 v[122:125], v[172:175], v[180:183], v[122:125]
	v_mfma_f32_16x16x32_bf16 v[114:117], v[164:167], v[188:191], v[114:117]
	v_mfma_f32_16x16x32_bf16 v[106:109], v[172:175], v[188:191], v[106:109]
	v_mfma_f32_16x16x32_bf16 v[98:101], v[164:167], v[196:199], v[98:101]
	v_mfma_f32_16x16x32_bf16 v[90:93], v[172:175], v[196:199], v[90:93]
	v_mfma_f32_16x16x32_bf16 v[82:85], v[164:167], v[208:211], v[82:85]
	v_mfma_f32_16x16x32_bf16 v[74:77], v[172:175], v[208:211], v[74:77]
	v_mfma_f32_16x16x32_bf16 v[126:129], v[168:171], v[184:187], v[126:129]
	v_mfma_f32_16x16x32_bf16 v[122:125], v[176:179], v[184:187], v[122:125]
	v_mfma_f32_16x16x32_bf16 v[114:117], v[168:171], v[192:195], v[114:117]
	v_mfma_f32_16x16x32_bf16 v[106:109], v[176:179], v[192:195], v[106:109]
	v_mfma_f32_16x16x32_bf16 v[98:101], v[168:171], v[200:203], v[98:101]
	v_mfma_f32_16x16x32_bf16 v[90:93], v[176:179], v[200:203], v[90:93]
	v_mfma_f32_16x16x32_bf16 v[82:85], v[168:171], v[212:215], v[82:85]
	v_mfma_f32_16x16x32_bf16 v[74:77], v[176:179], v[212:215], v[74:77]
	s_setprio 0
	s_barrier
	s_add_i32 s44, 0, 0x1c000
	s_add_i32 s45, s67, s48
	v_add_u32_e32 v134, s44, v151
	v_lshl_add_u64 v[206:207], s[42:43], 0, v[132:133]
	s_mov_b32 m0, s45
	ds_read_b128 v[216:219], v134
	ds_read_b128 v[220:223], v134 offset:1024
	ds_read_b128 v[224:227], v134 offset:2048
	ds_read_b128 v[228:231], v134 offset:3072
	global_load_lds_dwordx4 v[206:207], off
	v_lshl_add_u64 v[206:207], s[42:43], 0, v[130:131]
	s_add_i32 m0, s45, 0x2000
	s_nop 0
	global_load_lds_dwordx4 v[206:207], off
	s_barrier
	s_waitcnt lgkmcnt(0)
	s_setprio 1
	v_mfma_f32_16x16x32_bf16 v[118:121], v[216:219], v[180:183], v[118:121]
	v_mfma_f32_16x16x32_bf16 v[110:113], v[224:227], v[180:183], v[110:113]
	v_mfma_f32_16x16x32_bf16 v[102:105], v[216:219], v[188:191], v[102:105]
	v_mfma_f32_16x16x32_bf16 v[94:97], v[224:227], v[188:191], v[94:97]
	v_mfma_f32_16x16x32_bf16 v[86:89], v[216:219], v[196:199], v[86:89]
	v_mfma_f32_16x16x32_bf16 v[78:81], v[224:227], v[196:199], v[78:81]
	v_mfma_f32_16x16x32_bf16 v[70:73], v[216:219], v[208:211], v[70:73]
	v_mfma_f32_16x16x32_bf16 v[66:69], v[224:227], v[208:211], v[66:69]
	v_mfma_f32_16x16x32_bf16 v[118:121], v[220:223], v[184:187], v[118:121]
	v_mfma_f32_16x16x32_bf16 v[110:113], v[228:231], v[184:187], v[110:113]
	v_mfma_f32_16x16x32_bf16 v[102:105], v[220:223], v[192:195], v[102:105]
	v_mfma_f32_16x16x32_bf16 v[94:97], v[228:231], v[192:195], v[94:97]
	v_mfma_f32_16x16x32_bf16 v[86:89], v[220:223], v[200:203], v[86:89]
	v_mfma_f32_16x16x32_bf16 v[78:81], v[228:231], v[200:203], v[78:81]
	v_mfma_f32_16x16x32_bf16 v[70:73], v[220:223], v[212:215], v[70:73]
	v_mfma_f32_16x16x32_bf16 v[66:69], v[228:231], v[212:215], v[66:69]
	s_setprio 0
	s_mov_b32 m0, s55
	v_lshl_add_u64 v[206:207], v[234:235], 0, s[12:13]
	s_barrier
	ds_read_b128 v[180:183], v154 offset:49152
	ds_read_b128 v[184:187], v154 offset:50176
	ds_read_b128 v[188:191], v154 offset:51200
	ds_read_b128 v[192:195], v154 offset:52224
	ds_read_b128 v[196:199], v154 offset:53248
	ds_read_b128 v[200:203], v154 offset:54272
	ds_read_b128 v[208:211], v154 offset:55296
	ds_read_b128 v[212:215], v154 offset:56320
	global_load_lds_dwordx4 v[206:207], off
	v_lshl_add_u64 v[204:205], v[204:205], 0, s[12:13]
	s_mov_b32 m0, s56
	s_nop 0
	global_load_lds_dwordx4 v[204:205], off
	s_barrier
	s_waitcnt lgkmcnt(0)
	s_setprio 1
	v_mfma_f32_16x16x32_bf16 v[62:65], v[164:167], v[180:183], v[62:65]
	v_mfma_f32_16x16x32_bf16 v[58:61], v[172:175], v[180:183], v[58:61]
	v_mfma_f32_16x16x32_bf16 v[46:49], v[164:167], v[188:191], v[46:49]
	v_mfma_f32_16x16x32_bf16 v[42:45], v[172:175], v[188:191], v[42:45]
	v_mfma_f32_16x16x32_bf16 v[30:33], v[164:167], v[196:199], v[30:33]
	v_mfma_f32_16x16x32_bf16 v[26:29], v[172:175], v[196:199], v[26:29]
	v_mfma_f32_16x16x32_bf16 v[14:17], v[164:167], v[208:211], v[14:17]
	v_mfma_f32_16x16x32_bf16 v[10:13], v[172:175], v[208:211], v[10:13]
	v_mfma_f32_16x16x32_bf16 v[62:65], v[168:171], v[184:187], v[62:65]
	v_mfma_f32_16x16x32_bf16 v[58:61], v[176:179], v[184:187], v[58:61]
	v_mfma_f32_16x16x32_bf16 v[46:49], v[168:171], v[192:195], v[46:49]
	v_mfma_f32_16x16x32_bf16 v[42:45], v[176:179], v[192:195], v[42:45]
	v_mfma_f32_16x16x32_bf16 v[30:33], v[168:171], v[200:203], v[30:33]
	v_mfma_f32_16x16x32_bf16 v[26:29], v[176:179], v[200:203], v[26:29]
	v_mfma_f32_16x16x32_bf16 v[14:17], v[168:171], v[212:215], v[14:17]
	v_mfma_f32_16x16x32_bf16 v[10:13], v[176:179], v[212:215], v[10:13]
	s_setprio 0
	s_barrier
	s_add_u32 s40, s40, 0x40800
	s_addc_u32 s41, s41, 0
	s_add_i32 s42, s44, s48
	v_lshl_add_u64 v[164:165], s[40:41], 0, v[132:133]
	s_mov_b32 m0, s42
	s_nop 0
	global_load_lds_dwordx4 v[164:165], off
	v_lshl_add_u64 v[164:165], s[40:41], 0, v[130:131]
	s_add_i32 m0, s42, 0x2000
	s_nop 0
	global_load_lds_dwordx4 v[164:165], off
	s_cmp_eq_u32 s82, 0
	s_cbranch_scc1 .Lpb9_p8n
	s_waitcnt vmcnt(14)
	s_branch .Lpb9_p8j

; #define PG8_STAGE(bufoff, gbase, v0, v1) do { \
;         __builtin_amdgcn_global_load_lds((const unsigned*)((const char*)(gbase) + (v0)), (LAS unsigned*)(lds + (bufoff) + ldsw), 16, 0, 0); \
;         __builtin_amdgcn_global_load_lds((const unsigned*)((const char*)(gbase) + (v1)), (LAS unsigned*)(lds + (bufoff) + ldsw + 8192), 16, 0, 0); } while (0)
; #define PG8_LDA(dst, b, h) do { _Pragma("unroll") for (int m = 0; m < 4; ++m) _Pragma("unroll") for (int k = 0; k < 2; ++k) dst[m][k] = *(const LAS bf16x8*)(lds + PG8_SA(b, h) + aoff + m * 2048 + k * 1024); } while (0)
; #define PG8_LDB(dst, b, h) do { _Pragma("unroll") for (int n = 0; n < 2; ++n) _Pragma("unroll") for (int k = 0; k < 2; ++k) dst[n][k] = *(const LAS bf16x8*)(lds + PG8_SB(b, h) + boff + n * 2048 + k * 1024); } while (0)
; #define PG8_MMA(ai, bj, At, Bt) do { __builtin_amdgcn_s_setprio(1); _Pragma("unroll") for (int m = 0; m < 4; ++m) _Pragma("unroll") for (int n = 0; n < 2; ++n) _Pragma("unroll") for (int k = 0; k < 2; ++k) \
;         acc[ai][bj][m][n] = __builtin_amdgcn_mfma_f32_16x16x32_bf16(Bt[n][k], At[m][k], acc[ai][bj][m][n], 0, 0, 0); __builtin_amdgcn_s_setprio(0); } while (0)
; #define PG8_WAIT_L(n) asm volatile("s_waitcnt lgkmcnt(" #n ")" ::: "memory")
; template <class Epi, class Sched>
; __device__ __forceinline__ void gemm_phase(LAS unsigned char* lds, const int K, const Sched& S, const Epi& E) {
;     ...
;         for (int t = 0; t < nt; t += 2) {
;             const bool last = (t == nt - 2);
;             const char* a1 = gA + (size_t)(t + 1) * kstep;
;             const char* a2 = last ? gA : gA + (size_t)(t + 2) * kstep; const char* b2 = last ? nB : cB + (size_t)(t + 2) * kstepB;
;             const char* a3 = a2 + kstep; const char* b3 = b2 + kstepB;
;             const unsigned x00 = last ? n00 : c00, x01 = last ? n01 : c01, x10 = last ? n10 : c10, x11 = last ? n11 : c11;
;             PG8_LDB(B0, 0, 0); PG8_SCHED; PG8_LDA(At, 0, 0); PG8_STAGE(PG8_SA(1, 1), a1, c10, c11);
;             PG8_WAIT_L(8); PG8_BAR; PG8_WAIT_L(0); PG8_MMA(0, 0, At, B0); PG8_BAR; PG8_SCHED;
;             PG8_LDB(B1, 0, 1); PG8_STAGE(PG8_SB(0, 0), b2, voffB0, voffB1);
;             PG8_BAR; PG8_WAIT_L(0); PG8_MMA(0, 1, At, B1); PG8_BAR;
;             PG8_LDA(At, 0, 1); PG8_STAGE(PG8_SA(0, 0), a2, x00, x01);
;             PG8_BAR; PG8_WAIT_L(0); PG8_MMA(1, 0, At, B0); PG8_BAR; PG8_SCHED;
.LBB0_1290:
	s_add_u32 s20, s4, s18
	s_addc_u32 s21, s5, s19
	s_add_u32 s22, s20, 0x34c30100
	ds_read_b128 v[166:169], v158
	ds_read_b128 v[170:173], v158 offset:1024
	ds_read_b128 v[174:177], v158 offset:2048
	ds_read_b128 v[178:181], v158 offset:3072
	s_addc_u32 s23, s21, 0
	s_add_u32 s47, s17, s18
	s_addc_u32 s48, s45, s19
	s_cmpk_eq_i32 s18, 0xf00
	s_cselect_b64 vcc, -1, 0
	s_and_b64 s[20:21], vcc, exec
	v_cndmask_b32_e32 v134, v141, v161, vcc
	s_cselect_b32 s23, s7, s23
	s_cselect_b32 s22, s6, s22
	v_cndmask_b32_e32 v143, v142, v163, vcc
	s_cselect_b32 s21, s3, s48
	s_cselect_b32 s20, s2, s47
	v_cndmask_b32_e32 v206, v140, v162, vcc
	s_mov_b32 m0, s40
	v_lshl_add_u64 v[216:217], v[148:149], 0, s[18:19]
	ds_read_b128 v[182:185], v159
	ds_read_b128 v[186:189], v159 offset:1024
	ds_read_b128 v[190:193], v159 offset:2048
	ds_read_b128 v[194:197], v159 offset:3072
	ds_read_b128 v[198:201], v159 offset:4096
	ds_read_b128 v[202:205], v159 offset:5120
	ds_read_b128 v[208:211], v159 offset:6144
	ds_read_b128 v[212:215], v159 offset:7168
	global_load_lds_dwordx4 v[216:217], off
	v_lshl_add_u64 v[216:217], v[146:147], 0, s[18:19]
	s_add_i32 m0, s29, 0xe000
	s_nop 0
	global_load_lds_dwordx4 v[216:217], off
	s_waitcnt lgkmcnt(8)
	s_barrier
	s_waitcnt lgkmcnt(0)
	s_setprio 1
	v_mfma_f32_16x16x32_bf16 v[126:129], v[166:169], v[182:185], v[126:129]
	v_mfma_f32_16x16x32_bf16 v[122:125], v[174:177], v[182:185], v[122:125]
	v_mfma_f32_16x16x32_bf16 v[118:121], v[166:169], v[190:193], v[118:121]
	v_mfma_f32_16x16x32_bf16 v[110:113], v[174:177], v[190:193], v[110:113]
	v_mfma_f32_16x16x32_bf16 v[102:105], v[166:169], v[198:201], v[102:105]
	v_mfma_f32_16x16x32_bf16 v[94:97], v[174:177], v[198:201], v[94:97]
	v_mfma_f32_16x16x32_bf16 v[86:89], v[166:169], v[208:211], v[86:89]
	v_mfma_f32_16x16x32_bf16 v[78:81], v[174:177], v[208:211], v[78:81]
	v_mfma_f32_16x16x32_bf16 v[126:129], v[170:173], v[186:189], v[126:129]
	v_mfma_f32_16x16x32_bf16 v[122:125], v[178:181], v[186:189], v[122:125]
	v_mfma_f32_16x16x32_bf16 v[118:121], v[170:173], v[194:197], v[118:121]
	v_mfma_f32_16x16x32_bf16 v[110:113], v[178:181], v[194:197], v[110:113]
	v_mfma_f32_16x16x32_bf16 v[102:105], v[170:173], v[202:205], v[102:105]
	v_mfma_f32_16x16x32_bf16 v[94:97], v[178:181], v[202:205], v[94:97]
	v_mfma_f32_16x16x32_bf16 v[86:89], v[170:173], v[212:215], v[86:89]
	v_mfma_f32_16x16x32_bf16 v[78:81], v[178:181], v[212:215], v[78:81]
	s_setprio 0
	s_barrier
	s_add_i32 s47, s37, s27
	v_lshl_add_u64 v[232:233], s[20:21], 0, v[132:133]
	s_mov_b32 m0, s47
	ds_read_b128 v[216:219], v160
	ds_read_b128 v[220:223], v160 offset:1024
	ds_read_b128 v[224:227], v160 offset:2048
	ds_read_b128 v[228:231], v160 offset:3072
	global_load_lds_dwordx4 v[232:233], off
	v_lshl_add_u64 v[234:235], s[20:21], 0, v[130:131]
	s_add_i32 m0, s47, 0x2000
	s_nop 0
	global_load_lds_dwordx4 v[234:235], off
	s_barrier
	s_waitcnt lgkmcnt(0)
	s_setprio 1
	v_mfma_f32_16x16x32_bf16 v[114:117], v[216:219], v[182:185], v[114:117]
	v_mfma_f32_16x16x32_bf16 v[106:109], v[224:227], v[182:185], v[106:109]
	v_mfma_f32_16x16x32_bf16 v[98:101], v[216:219], v[190:193], v[98:101]
	v_mfma_f32_16x16x32_bf16 v[90:93], v[224:227], v[190:193], v[90:93]
	v_mfma_f32_16x16x32_bf16 v[82:85], v[216:219], v[198:201], v[82:85]
	v_mfma_f32_16x16x32_bf16 v[74:77], v[224:227], v[198:201], v[74:77]
	v_mfma_f32_16x16x32_bf16 v[70:73], v[216:219], v[208:211], v[70:73]
	v_mfma_f32_16x16x32_bf16 v[66:69], v[224:227], v[208:211], v[66:69]
	v_mfma_f32_16x16x32_bf16 v[114:117], v[220:223], v[186:189], v[114:117]
	v_mfma_f32_16x16x32_bf16 v[106:109], v[228:231], v[186:189], v[106:109]
	v_mfma_f32_16x16x32_bf16 v[98:101], v[220:223], v[194:197], v[98:101]
	v_mfma_f32_16x16x32_bf16 v[90:93], v[228:231], v[194:197], v[90:93]
	v_mfma_f32_16x16x32_bf16 v[82:85], v[220:223], v[202:205], v[82:85]
	v_mfma_f32_16x16x32_bf16 v[74:77], v[228:231], v[202:205], v[74:77]
	v_mfma_f32_16x16x32_bf16 v[70:73], v[220:223], v[212:215], v[70:73]
	v_mfma_f32_16x16x32_bf16 v[66:69], v[228:231], v[212:215], v[66:69]
	s_setprio 0
	s_mov_b32 m0, s29
	s_barrier
	ds_read_b128 v[182:185], v159 offset:16384
	ds_read_b128 v[186:189], v159 offset:17408
	ds_read_b128 v[190:193], v159 offset:18432
	ds_read_b128 v[194:197], v159 offset:19456
	ds_read_b128 v[198:201], v159 offset:20480
	ds_read_b128 v[202:205], v159 offset:21504
	ds_read_b128 v[208:211], v159 offset:22528
	ds_read_b128 v[212:215], v159 offset:23552
	global_load_lds_dwordx4 v134, s[22:23]
	s_mov_b32 m0, s30
	v_mov_b32_e32 v207, v135
	global_load_lds_dwordx4 v206, s[22:23]
	s_barrier
	s_waitcnt lgkmcnt(0)
	v_lshl_add_u64 v[236:237], s[22:23], 0, v[134:135]
	v_lshl_add_u64 v[206:207], s[22:23], 0, v[206:207]
	s_setprio 1
	s_waitcnt lgkmcnt(0)
	v_mfma_f32_16x16x32_bf16 v[62:65], v[166:169], v[182:185], v[62:65]
	v_mfma_f32_16x16x32_bf16 v[58:61], v[174:177], v[182:185], v[58:61]
	v_mfma_f32_16x16x32_bf16 v[54:57], v[166:169], v[190:193], v[54:57]
	v_mfma_f32_16x16x32_bf16 v[46:49], v[174:177], v[190:193], v[46:49]
	v_mfma_f32_16x16x32_bf16 v[38:41], v[166:169], v[198:201], v[38:41]
	v_mfma_f32_16x16x32_bf16 v[30:33], v[174:177], v[198:201], v[30:33]
	v_mfma_f32_16x16x32_bf16 v[22:25], v[166:169], v[208:211], v[22:25]
	v_mfma_f32_16x16x32_bf16 v[14:17], v[174:177], v[208:211], v[14:17]
	v_mfma_f32_16x16x32_bf16 v[62:65], v[170:173], v[186:189], v[62:65]
	v_mfma_f32_16x16x32_bf16 v[58:61], v[178:181], v[186:189], v[58:61]
	v_mfma_f32_16x16x32_bf16 v[54:57], v[170:173], v[194:197], v[54:57]
	v_mfma_f32_16x16x32_bf16 v[46:49], v[178:181], v[194:197], v[46:49]
	v_mfma_f32_16x16x32_bf16 v[38:41], v[170:173], v[202:205], v[38:41]
	v_mfma_f32_16x16x32_bf16 v[30:33], v[178:181], v[202:205], v[30:33]
	v_mfma_f32_16x16x32_bf16 v[22:25], v[170:173], v[212:215], v[22:25]
	v_mfma_f32_16x16x32_bf16 v[14:17], v[178:181], v[212:215], v[14:17]
	s_setprio 0
	s_barrier
; #define PG8_STAGE(bufoff, gbase, v0, v1) do { \
;         __builtin_amdgcn_global_load_lds((const unsigned*)((const char*)(gbase) + (v0)), (LAS unsigned*)(lds + (bufoff) + ldsw), 16, 0, 0); \
;         __builtin_amdgcn_global_load_lds((const unsigned*)((const char*)(gbase) + (v1)), (LAS unsigned*)(lds + (bufoff) + ldsw + 8192), 16, 0, 0); } while (0)
; #define PG8_LDA(dst, b, h) do { _Pragma("unroll") for (int m = 0; m < 4; ++m) _Pragma("unroll") for (int k = 0; k < 2; ++k) dst[m][k] = *(const LAS bf16x8*)(lds + PG8_SA(b, h) + aoff + m * 2048 + k * 1024); } while (0)
; #define PG8_LDB(dst, b, h) do { _Pragma("unroll") for (int n = 0; n < 2; ++n) _Pragma("unroll") for (int k = 0; k < 2; ++k) dst[n][k] = *(const LAS bf16x8*)(lds + PG8_SB(b, h) + boff + n * 2048 + k * 1024); } while (0)
; #define PG8_MMA(ai, bj, At, Bt) do { __builtin_amdgcn_s_setprio(1); _Pragma("unroll") for (int m = 0; m < 4; ++m) _Pragma("unroll") for (int n = 0; n < 2; ++n) _Pragma("unroll") for (int k = 0; k < 2; ++k) \
;         acc[ai][bj][m][n] = __builtin_amdgcn_mfma_f32_16x16x32_bf16(Bt[n][k], At[m][k], acc[ai][bj][m][n], 0, 0, 0); __builtin_amdgcn_s_setprio(0); } while (0)
; #define PG8_WAIT_V(n) asm volatile("s_waitcnt vmcnt(" #n ")" ::: "memory")
; #define PG8_WAIT_L(n) asm volatile("s_waitcnt lgkmcnt(" #n ")" ::: "memory")
; #define PG8_BAR __builtin_amdgcn_s_barrier()
; #define PG8_SCHED __builtin_amdgcn_sched_barrier(0)
; template <class Epi, class Sched>
; __device__ __forceinline__ void gemm_phase(LAS unsigned char* lds, const int K, const Sched& S, const Epi& E) {
;     ...
;             PG8_STAGE(PG8_SB(0, 1), b2 + hstep, voffB0, voffB1);
;             PG8_WAIT_V(6); PG8_BAR; PG8_MMA(1, 1, At, B1); PG8_BAR;
;             PG8_LDB(B0, 1, 0); PG8_SCHED; PG8_LDA(At, 1, 0); PG8_STAGE(PG8_SA(0, 1), a2, x10, x11);
;             PG8_WAIT_L(8); PG8_BAR; PG8_WAIT_L(0); PG8_MMA(0, 0, At, B0); PG8_BAR; PG8_SCHED;
;             PG8_LDB(B1, 1, 1); PG8_STAGE(PG8_SB(1, 0), b3, voffB0, voffB1);
;             PG8_BAR; PG8_WAIT_L(0); PG8_MMA(0, 1, At, B1); PG8_BAR;
;             PG8_LDA(At, 1, 1); PG8_STAGE(PG8_SA(1, 0), a3, x00, x01);
	s_add_u32 s48, s20, 0x80000
	s_addc_u32 s49, s21, 0
	s_add_i32 s47, s38, s27
	v_lshl_add_u64 v[166:167], s[48:49], 0, v[132:133]
	s_mov_b32 m0, s47
	s_nop 0
	global_load_lds_dwordx4 v[166:167], off
	v_lshl_add_u64 v[166:167], s[48:49], 0, v[130:131]
	s_add_i32 m0, s47, 0x2000
	s_nop 0
	global_load_lds_dwordx4 v[166:167], off
	s_waitcnt vmcnt(6)
	s_barrier
	s_setprio 1
	v_mfma_f32_16x16x32_bf16 v[50:53], v[216:219], v[182:185], v[50:53]
	v_mfma_f32_16x16x32_bf16 v[42:45], v[224:227], v[182:185], v[42:45]
	v_mfma_f32_16x16x32_bf16 v[34:37], v[216:219], v[190:193], v[34:37]
	v_mfma_f32_16x16x32_bf16 v[26:29], v[224:227], v[190:193], v[26:29]
	v_mfma_f32_16x16x32_bf16 v[18:21], v[216:219], v[198:201], v[18:21]
	v_mfma_f32_16x16x32_bf16 v[10:13], v[224:227], v[198:201], v[10:13]
	v_mfma_f32_16x16x32_bf16 v[6:9], v[216:219], v[208:211], v[6:9]
	v_mfma_f32_16x16x32_bf16 v[2:5], v[224:227], v[208:211], v[2:5]
	v_mfma_f32_16x16x32_bf16 v[50:53], v[220:223], v[186:189], v[50:53]
	v_mfma_f32_16x16x32_bf16 v[42:45], v[228:231], v[186:189], v[42:45]
	v_mfma_f32_16x16x32_bf16 v[34:37], v[220:223], v[194:197], v[34:37]
	v_mfma_f32_16x16x32_bf16 v[26:29], v[228:231], v[194:197], v[26:29]
	v_mfma_f32_16x16x32_bf16 v[18:21], v[220:223], v[202:205], v[18:21]
	v_mfma_f32_16x16x32_bf16 v[10:13], v[228:231], v[202:205], v[10:13]
	v_mfma_f32_16x16x32_bf16 v[6:9], v[220:223], v[212:215], v[6:9]
	v_mfma_f32_16x16x32_bf16 v[2:5], v[228:231], v[212:215], v[2:5]
	s_setprio 0
	s_add_i32 s47, 0, 0x18000
	v_add_u32_e32 v134, s47, v156
	s_barrier
	ds_read_b128 v[166:169], v134
	ds_read_b128 v[170:173], v134 offset:1024
	ds_read_b128 v[174:177], v134 offset:2048
	ds_read_b128 v[178:181], v134 offset:3072
	s_mov_b32 m0, s31
	ds_read_b128 v[182:185], v159 offset:32768
	ds_read_b128 v[186:189], v159 offset:33792
	ds_read_b128 v[190:193], v159 offset:34816
	ds_read_b128 v[194:197], v159 offset:35840
	ds_read_b128 v[198:201], v159 offset:36864
	ds_read_b128 v[202:205], v159 offset:37888
	ds_read_b128 v[208:211], v159 offset:38912
	ds_read_b128 v[212:215], v159 offset:39936
	v_cndmask_b32_e32 v134, v144, v164, vcc
	global_load_lds_dwordx4 v143, s[22:23]
	s_mov_b32 m0, s33
	s_nop 0
	global_load_lds_dwordx4 v134, s[22:23]
	s_waitcnt lgkmcnt(8)
	s_barrier
	s_waitcnt lgkmcnt(0)
	s_setprio 1
	v_mfma_f32_16x16x32_bf16 v[126:129], v[166:169], v[182:185], v[126:129]
	v_mfma_f32_16x16x32_bf16 v[122:125], v[174:177], v[182:185], v[122:125]
	v_mfma_f32_16x16x32_bf16 v[118:121], v[166:169], v[190:193], v[118:121]
	v_mfma_f32_16x16x32_bf16 v[110:113], v[174:177], v[190:193], v[110:113]
	v_mfma_f32_16x16x32_bf16 v[102:105], v[166:169], v[198:201], v[102:105]
	v_mfma_f32_16x16x32_bf16 v[94:97], v[174:177], v[198:201], v[94:97]
	v_mfma_f32_16x16x32_bf16 v[86:89], v[166:169], v[208:211], v[86:89]
	v_mfma_f32_16x16x32_bf16 v[78:81], v[174:177], v[208:211], v[78:81]
	v_mfma_f32_16x16x32_bf16 v[126:129], v[170:173], v[186:189], v[126:129]
	v_mfma_f32_16x16x32_bf16 v[122:125], v[178:181], v[186:189], v[122:125]
	v_mfma_f32_16x16x32_bf16 v[118:121], v[170:173], v[194:197], v[118:121]
	v_mfma_f32_16x16x32_bf16 v[110:113], v[178:181], v[194:197], v[110:113]
	v_mfma_f32_16x16x32_bf16 v[102:105], v[170:173], v[202:205], v[102:105]
	v_mfma_f32_16x16x32_bf16 v[94:97], v[178:181], v[202:205], v[94:97]
	v_mfma_f32_16x16x32_bf16 v[86:89], v[170:173], v[212:215], v[86:89]
	v_mfma_f32_16x16x32_bf16 v[78:81], v[178:181], v[212:215], v[78:81]
	s_setprio 0
	s_barrier
	s_add_i32 s22, 0, 0x1c000
	s_add_i32 s23, s47, s27
	v_add_u32_e32 v134, s22, v156
	v_lshl_add_u64 v[232:233], v[232:233], 0, s[14:15]
	s_mov_b32 m0, s23
	ds_read_b128 v[216:219], v134
	ds_read_b128 v[220:223], v134 offset:1024
	ds_read_b128 v[224:227], v134 offset:2048
	ds_read_b128 v[228:231], v134 offset:3072
	global_load_lds_dwordx4 v[232:233], off
	v_lshl_add_u64 v[232:233], v[234:235], 0, s[14:15]
	s_add_i32 m0, s23, 0x2000
	s_nop 0
	global_load_lds_dwordx4 v[232:233], off
	s_barrier
	s_waitcnt lgkmcnt(0)
	s_setprio 1
	v_mfma_f32_16x16x32_bf16 v[114:117], v[216:219], v[182:185], v[114:117]
	v_mfma_f32_16x16x32_bf16 v[106:109], v[224:227], v[182:185], v[106:109]
	v_mfma_f32_16x16x32_bf16 v[98:101], v[216:219], v[190:193], v[98:101]
	v_mfma_f32_16x16x32_bf16 v[90:93], v[224:227], v[190:193], v[90:93]
	v_mfma_f32_16x16x32_bf16 v[82:85], v[216:219], v[198:201], v[82:85]
	v_mfma_f32_16x16x32_bf16 v[74:77], v[224:227], v[198:201], v[74:77]
	v_mfma_f32_16x16x32_bf16 v[70:73], v[216:219], v[208:211], v[70:73]
	v_mfma_f32_16x16x32_bf16 v[66:69], v[224:227], v[208:211], v[66:69]
	v_mfma_f32_16x16x32_bf16 v[114:117], v[220:223], v[186:189], v[114:117]
	v_mfma_f32_16x16x32_bf16 v[106:109], v[228:231], v[186:189], v[106:109]
	v_mfma_f32_16x16x32_bf16 v[98:101], v[220:223], v[194:197], v[98:101]
	v_mfma_f32_16x16x32_bf16 v[90:93], v[228:231], v[194:197], v[90:93]
	v_mfma_f32_16x16x32_bf16 v[82:85], v[220:223], v[202:205], v[82:85]
	v_mfma_f32_16x16x32_bf16 v[74:77], v[228:231], v[202:205], v[74:77]
	v_mfma_f32_16x16x32_bf16 v[70:73], v[220:223], v[212:215], v[70:73]
	v_mfma_f32_16x16x32_bf16 v[66:69], v[228:231], v[212:215], v[66:69]
	s_setprio 0
	s_mov_b32 m0, s35
	v_lshl_add_u64 v[232:233], v[236:237], 0, s[14:15]
	s_barrier
	ds_read_b128 v[182:185], v159 offset:49152
	ds_read_b128 v[186:189], v159 offset:50176
	ds_read_b128 v[190:193], v159 offset:51200
	ds_read_b128 v[194:197], v159 offset:52224
	ds_read_b128 v[198:201], v159 offset:53248
	ds_read_b128 v[202:205], v159 offset:54272
	ds_read_b128 v[208:211], v159 offset:55296
	ds_read_b128 v[212:215], v159 offset:56320
	global_load_lds_dwordx4 v[232:233], off
	v_lshl_add_u64 v[206:207], v[206:207], 0, s[14:15]
	s_mov_b32 m0, s36
	s_nop 0
	global_load_lds_dwordx4 v[206:207], off
	s_barrier
; #define PG8_STAGE(bufoff, gbase, v0, v1) do { \
;         __builtin_amdgcn_global_load_lds((const unsigned*)((const char*)(gbase) + (v0)), (LAS unsigned*)(lds + (bufoff) + ldsw), 16, 0, 0); \
;         __builtin_amdgcn_global_load_lds((const unsigned*)((const char*)(gbase) + (v1)), (LAS unsigned*)(lds + (bufoff) + ldsw + 8192), 16, 0, 0); } while (0)
; #define PG8_MMA(ai, bj, At, Bt) do { __builtin_amdgcn_s_setprio(1); _Pragma("unroll") for (int m = 0; m < 4; ++m) _Pragma("unroll") for (int n = 0; n < 2; ++n) _Pragma("unroll") for (int k = 0; k < 2; ++k) \
;         acc[ai][bj][m][n] = __builtin_amdgcn_mfma_f32_16x16x32_bf16(Bt[n][k], At[m][k], acc[ai][bj][m][n], 0, 0, 0); __builtin_amdgcn_s_setprio(0); } while (0)
; #define PG8_WAIT_V(n) asm volatile("s_waitcnt vmcnt(" #n ")" ::: "memory")
; #define PG8_WAIT_L(n) asm volatile("s_waitcnt lgkmcnt(" #n ")" ::: "memory")
; #define PG8_BAR __builtin_amdgcn_s_barrier()
; #define PG8_SCHED __builtin_amdgcn_sched_barrier(0)
; template <class Epi, class Sched>
; __device__ __forceinline__ void gemm_phase(LAS unsigned char* lds, const int K, const Sched& S, const Epi& E) {
;     ...
;             PG8_BAR; PG8_WAIT_L(0); PG8_MMA(1, 0, At, B0); PG8_BAR; PG8_SCHED;
;             PG8_STAGE(PG8_SB(1, 1), b3 + hstep, voffB0, voffB1);
;             PG8_WAIT_V(6); PG8_BAR; PG8_MMA(1, 1, At, B1); PG8_BAR;
	s_waitcnt lgkmcnt(0)
	s_setprio 1
	v_mfma_f32_16x16x32_bf16 v[62:65], v[166:169], v[182:185], v[62:65]
	v_mfma_f32_16x16x32_bf16 v[58:61], v[174:177], v[182:185], v[58:61]
	v_mfma_f32_16x16x32_bf16 v[54:57], v[166:169], v[190:193], v[54:57]
	v_mfma_f32_16x16x32_bf16 v[46:49], v[174:177], v[190:193], v[46:49]
	v_mfma_f32_16x16x32_bf16 v[38:41], v[166:169], v[198:201], v[38:41]
	v_mfma_f32_16x16x32_bf16 v[30:33], v[174:177], v[198:201], v[30:33]
	v_mfma_f32_16x16x32_bf16 v[22:25], v[166:169], v[208:211], v[22:25]
	v_mfma_f32_16x16x32_bf16 v[14:17], v[174:177], v[208:211], v[14:17]
	v_mfma_f32_16x16x32_bf16 v[62:65], v[170:173], v[186:189], v[62:65]
	v_mfma_f32_16x16x32_bf16 v[58:61], v[178:181], v[186:189], v[58:61]
	v_mfma_f32_16x16x32_bf16 v[54:57], v[170:173], v[194:197], v[54:57]
	v_mfma_f32_16x16x32_bf16 v[46:49], v[178:181], v[194:197], v[46:49]
	v_mfma_f32_16x16x32_bf16 v[38:41], v[170:173], v[202:205], v[38:41]
	v_mfma_f32_16x16x32_bf16 v[30:33], v[178:181], v[202:205], v[30:33]
	v_mfma_f32_16x16x32_bf16 v[22:25], v[170:173], v[212:215], v[22:25]
	v_mfma_f32_16x16x32_bf16 v[14:17], v[178:181], v[212:215], v[14:17]
	s_setprio 0
	s_barrier
	s_add_u32 s20, s20, 0x80080
	s_addc_u32 s21, s21, 0
	s_add_i32 s22, s22, s27
	v_lshl_add_u64 v[166:167], s[20:21], 0, v[132:133]
	s_mov_b32 m0, s22
	s_nop 0
	global_load_lds_dwordx4 v[166:167], off
	v_lshl_add_u64 v[166:167], s[20:21], 0, v[130:131]
	s_add_i32 m0, s22, 0x2000
	s_nop 0
	global_load_lds_dwordx4 v[166:167], off
	s_waitcnt vmcnt(6)
	s_barrier
	s_setprio 1
	v_mfma_f32_16x16x32_bf16 v[50:53], v[216:219], v[182:185], v[50:53]
	v_mfma_f32_16x16x32_bf16 v[42:45], v[224:227], v[182:185], v[42:45]
	v_mfma_f32_16x16x32_bf16 v[34:37], v[216:219], v[190:193], v[34:37]
	v_mfma_f32_16x16x32_bf16 v[26:29], v[224:227], v[190:193], v[26:29]
	v_mfma_f32_16x16x32_bf16 v[18:21], v[216:219], v[198:201], v[18:21]
	v_mfma_f32_16x16x32_bf16 v[10:13], v[224:227], v[198:201], v[10:13]
	v_mfma_f32_16x16x32_bf16 v[6:9], v[216:219], v[208:211], v[6:9]
	v_mfma_f32_16x16x32_bf16 v[2:5], v[224:227], v[208:211], v[2:5]
	v_mfma_f32_16x16x32_bf16 v[50:53], v[220:223], v[186:189], v[50:53]
	v_mfma_f32_16x16x32_bf16 v[42:45], v[228:231], v[186:189], v[42:45]
	v_mfma_f32_16x16x32_bf16 v[34:37], v[220:223], v[194:197], v[34:37]
	v_mfma_f32_16x16x32_bf16 v[26:29], v[228:231], v[194:197], v[26:29]
	v_mfma_f32_16x16x32_bf16 v[18:21], v[220:223], v[202:205], v[18:21]
	v_mfma_f32_16x16x32_bf16 v[10:13], v[228:231], v[202:205], v[10:13]
	v_mfma_f32_16x16x32_bf16 v[6:9], v[220:223], v[212:215], v[6:9]
	v_mfma_f32_16x16x32_bf16 v[2:5], v[228:231], v[212:215], v[2:5]
	s_setprio 0
	s_add_i32 s46, s46, 2
	s_add_u32 s18, s18, 0x100
	s_addc_u32 s19, s19, 0
	s_cmp_gt_u32 s46, 29
	s_barrier
	s_cbranch_scc0 .LBB0_1290
; __device__ __forceinline__ unsigned cvt_pk_bf16(float lo, float hi) { unsigned r; asm volatile("v_cvt_pk_bf16_f32 %0, %1, %2" : "=v"(r) : "v"(lo), "v"(hi)); return r; }
; #define PG8_WAIT_V(n) asm volatile("s_waitcnt vmcnt(" #n ")" ::: "memory")
; #define PG8_BAR __builtin_amdgcn_s_barrier()
; template <class Epi, class Sched>
; __device__ __forceinline__ void gemm_phase(LAS unsigned char* lds, const int K, const Sched& S, const Epi& E) {
;     ...
;         E(acc, cur, wr, wc, fr, fq);
;         if (!has_next) break;
; #pragma unroll
;         for (int a = 0; a < 2; ++a)
; #pragma unroll
;             for (int b = 0; b < 2; ++b)
; #pragma unroll
;                 for (int m = 0; m < 4; ++m)
; #pragma unroll
;                     for (int n = 0; n < 2; ++n) acc[a][b][m][n] = (f32x4){0.f, 0.f, 0.f, 0.f};
;         cur = nxt; cB = nB; c00 = n00; c01 = n01; c10 = n10; c11 = n11; ++ui;
;     }
;     PG8_WAIT_V(0);
;     if (wr == 0) PG8_BAR;
;     PG8_BAR;
;     __device__ __forceinline__ void operator()(const f32x4 (&acc)[2][2][4][2], const Unit& u, int wr, int wc, int fr, int fq) const {
;         const int row0 = u.rbase + wr * 64 + fr, col0 = u.pn * BM + wc * 32 + 8 * fq;
; #pragma unroll
;         for (int ai = 0; ai < 2; ++ai)
; #pragma unroll
;             for (int m = 0; m < 4; ++m) { bf16_t* rowp = O + (size_t)(row0 + ai * HALF + m * 16) * ldc + col0;
; #pragma unroll
;                 for (int bj = 0; bj < 2; ++bj) { const f32x4 v0 = acc[ai][bj][m][0], v1 = acc[ai][bj][m][1];
;                     u32x4 w; w.x = cvt_pk_bf16(v0[0], v0[1]); w.y = cvt_pk_bf16(v0[2], v0[3]); w.z = cvt_pk_bf16(v1[0], v1[1]); w.w = cvt_pk_bf16(v1[2], v1[3]);
;                     *(u32x4*)(rowp + bj * HALF) = w; } }
;     }
	v_lshl_or_b32 v142, s44, 8, v157
	v_add_u32_e32 v134, s43, v155
	v_ashrrev_i32_e32 v143, 31, v142
	v_mov_b64_e32 v[140:141], s[10:11]
	v_mad_i64_i32 v[144:145], s[18:19], v134, s39, v[140:141]
	v_lshlrev_b64 v[142:143], 1, v[142:143]
	v_lshl_add_u64 v[144:145], v[144:145], 0, v[142:143]
	v_cvt_pk_bf16_f32 v126, v126, v127
	v_cvt_pk_bf16_f32 v127, v128, v129
	v_cvt_pk_bf16_f32 v128, v122, v123
	v_cvt_pk_bf16_f32 v129, v124, v125
	global_store_dwordx4 v[144:145], v[126:129], off
	v_cvt_pk_bf16_f32 v114, v114, v115
	v_cvt_pk_bf16_f32 v115, v116, v117
	v_cvt_pk_bf16_f32 v116, v106, v107
	v_add_u32_e32 v106, 16, v134
	v_mad_i64_i32 v[106:107], s[18:19], v106, s39, v[140:141]
	v_cvt_pk_bf16_f32 v117, v108, v109
	global_store_dwordx4 v[144:145], v[114:117], off offset:256
	s_and_b64 vcc, exec, s[0:1]
	s_mov_b32 s44, s16
	v_lshl_add_u64 v[114:115], v[106:107], 0, v[142:143]
	v_cvt_pk_bf16_f32 v106, v118, v119
	v_cvt_pk_bf16_f32 v107, v120, v121
	v_cvt_pk_bf16_f32 v108, v110, v111
	v_cvt_pk_bf16_f32 v109, v112, v113
	global_store_dwordx4 v[114:115], v[106:109], off
	v_cvt_pk_bf16_f32 v98, v98, v99
	v_cvt_pk_bf16_f32 v99, v100, v101
	v_cvt_pk_bf16_f32 v100, v90, v91
	v_add_u32_e32 v90, 32, v134
	v_mad_i64_i32 v[90:91], s[18:19], v90, s39, v[140:141]
	v_cvt_pk_bf16_f32 v101, v92, v93
	global_store_dwordx4 v[114:115], v[98:101], off offset:256
	s_mov_b32 s43, s41
	v_mov_b32_e32 v144, v164
	v_lshl_add_u64 v[98:99], v[90:91], 0, v[142:143]
	v_cvt_pk_bf16_f32 v90, v102, v103
	v_cvt_pk_bf16_f32 v91, v104, v105
	v_cvt_pk_bf16_f32 v92, v94, v95
	v_cvt_pk_bf16_f32 v93, v96, v97
	global_store_dwordx4 v[98:99], v[90:93], off
	v_cvt_pk_bf16_f32 v82, v82, v83
	v_cvt_pk_bf16_f32 v83, v84, v85
	v_cvt_pk_bf16_f32 v84, v74, v75
	v_add_u32_e32 v74, 48, v134
	v_mad_i64_i32 v[74:75], s[18:19], v74, s39, v[140:141]
	v_cvt_pk_bf16_f32 v85, v76, v77
	global_store_dwordx4 v[98:99], v[82:85], off offset:256
	s_nop 1
	v_lshl_add_u64 v[82:83], v[74:75], 0, v[142:143]
	v_cvt_pk_bf16_f32 v74, v86, v87
	v_cvt_pk_bf16_f32 v75, v88, v89
	v_cvt_pk_bf16_f32 v76, v78, v79
	v_cvt_pk_bf16_f32 v77, v80, v81
	global_store_dwordx4 v[82:83], v[74:77], off
	v_cvt_pk_bf16_f32 v70, v70, v71
	v_cvt_pk_bf16_f32 v71, v72, v73
	v_cvt_pk_bf16_f32 v72, v66, v67
	v_add_u32_e32 v66, 0x80, v134
	v_mad_i64_i32 v[66:67], s[18:19], v66, s39, v[140:141]
	v_lshl_add_u64 v[66:67], v[66:67], 0, v[142:143]
	v_cvt_pk_bf16_f32 v73, v68, v69
	global_store_dwordx4 v[82:83], v[70:73], off offset:256
	v_cvt_pk_bf16_f32 v62, v62, v63
	v_cvt_pk_bf16_f32 v63, v64, v65
	v_cvt_pk_bf16_f32 v64, v58, v59
	v_cvt_pk_bf16_f32 v65, v60, v61
	global_store_dwordx4 v[66:67], v[62:65], off
	v_cvt_pk_bf16_f32 v50, v50, v51
	v_cvt_pk_bf16_f32 v51, v52, v53
	v_cvt_pk_bf16_f32 v52, v42, v43
	v_add_u32_e32 v42, 0x90, v134
	v_mad_i64_i32 v[42:43], s[18:19], v42, s39, v[140:141]
	v_cvt_pk_bf16_f32 v53, v44, v45
	global_store_dwordx4 v[66:67], v[50:53], off offset:256
	s_nop 1
	v_lshl_add_u64 v[50:51], v[42:43], 0, v[142:143]
	v_cvt_pk_bf16_f32 v42, v54, v55
	v_cvt_pk_bf16_f32 v43, v56, v57
	v_cvt_pk_bf16_f32 v44, v46, v47
	v_cvt_pk_bf16_f32 v45, v48, v49
	global_store_dwordx4 v[50:51], v[42:45], off
	v_cvt_pk_bf16_f32 v34, v34, v35
	v_cvt_pk_bf16_f32 v35, v36, v37
	v_cvt_pk_bf16_f32 v36, v26, v27
	v_add_u32_e32 v26, 0xa0, v134
	v_mad_i64_i32 v[26:27], s[18:19], v26, s39, v[140:141]
	v_cvt_pk_bf16_f32 v37, v28, v29
	global_store_dwordx4 v[50:51], v[34:37], off offset:256
	s_nop 1
	v_lshl_add_u64 v[34:35], v[26:27], 0, v[142:143]
	v_cvt_pk_bf16_f32 v26, v38, v39
	v_cvt_pk_bf16_f32 v27, v40, v41
	v_cvt_pk_bf16_f32 v28, v30, v31
	v_cvt_pk_bf16_f32 v29, v32, v33
	global_store_dwordx4 v[34:35], v[26:29], off
	v_cvt_pk_bf16_f32 v18, v18, v19
	v_cvt_pk_bf16_f32 v19, v20, v21
	v_cvt_pk_bf16_f32 v20, v10, v11
	v_add_u32_e32 v10, 0xb0, v134
	v_mad_i64_i32 v[10:11], s[18:19], v10, s39, v[140:141]
	v_cvt_pk_bf16_f32 v21, v12, v13
	global_store_dwordx4 v[34:35], v[18:21], off offset:256
	v_mov_b32_e32 v141, v161
	v_mov_b32_e32 v140, v162
	v_lshl_add_u64 v[18:19], v[10:11], 0, v[142:143]
	v_mov_b32_e32 v142, v163
	s_mov_b64 s[18:19], s[2:3]
	v_cvt_pk_bf16_f32 v10, v22, v23
	v_cvt_pk_bf16_f32 v11, v24, v25
	v_cvt_pk_bf16_f32 v12, v14, v15
	v_cvt_pk_bf16_f32 v13, v16, v17
	global_store_dwordx4 v[18:19], v[10:13], off
	v_cvt_pk_bf16_f32 v6, v6, v7
	v_cvt_pk_bf16_f32 v7, v8, v9
	v_cvt_pk_bf16_f32 v8, v2, v3
	v_cvt_pk_bf16_f32 v9, v4, v5
	global_store_dwordx4 v[18:19], v[6:9], off offset:256
	s_cbranch_vccz .LBB0_1285
	s_waitcnt vmcnt(0)
	s_cmpk_gt_u32 s24, 0xff
	s_cbranch_scc1 .LBB0_1294
	s_barrier

; #define PG8_STAGE(bufoff, gbase, v0, v1) do { \
;         __builtin_amdgcn_global_load_lds((const unsigned*)((const char*)(gbase) + (v0)), (LAS unsigned*)(lds + (bufoff) + ldsw), 16, 0, 0); \
;         __builtin_amdgcn_global_load_lds((const unsigned*)((const char*)(gbase) + (v1)), (LAS unsigned*)(lds + (bufoff) + ldsw + 8192), 16, 0, 0); } while (0)
; #define PG8_LDA(dst, b, h) do { _Pragma("unroll") for (int m = 0; m < 4; ++m) _Pragma("unroll") for (int k = 0; k < 2; ++k) dst[m][k] = *(const LAS bf16x8*)(lds + PG8_SA(b, h) + aoff + m * 2048 + k * 1024); } while (0)
; #define PG8_LDB(dst, b, h) do { _Pragma("unroll") for (int n = 0; n < 2; ++n) _Pragma("unroll") for (int k = 0; k < 2; ++k) dst[n][k] = *(const LAS bf16x8*)(lds + PG8_SB(b, h) + boff + n * 2048 + k * 1024); } while (0)
; #define PG8_MMA(ai, bj, At, Bt) do { __builtin_amdgcn_s_setprio(1); _Pragma("unroll") for (int m = 0; m < 4; ++m) _Pragma("unroll") for (int n = 0; n < 2; ++n) _Pragma("unroll") for (int k = 0; k < 2; ++k) \
;         acc[ai][bj][m][n] = __builtin_amdgcn_mfma_f32_16x16x32_bf16(Bt[n][k], At[m][k], acc[ai][bj][m][n], 0, 0, 0); __builtin_amdgcn_s_setprio(0); } while (0)
; #define PG8_WAIT_L(n) asm volatile("s_waitcnt lgkmcnt(" #n ")" ::: "memory")
; template <class Epi, class Sched>
; __device__ __forceinline__ void gemm_phase(LAS unsigned char* lds, const int K, const Sched& S, const Epi& E) {
;     ...
;         for (int t = 0; t < nt; t += 2) {
;             const bool last = (t == nt - 2);
;             const char* a1 = gA + (size_t)(t + 1) * kstep;
;             const char* a2 = last ? gA : gA + (size_t)(t + 2) * kstep; const char* b2 = last ? nB : cB + (size_t)(t + 2) * kstepB;
;             const char* a3 = a2 + kstep; const char* b3 = b2 + kstepB;
;             const unsigned x00 = last ? n00 : c00, x01 = last ? n01 : c01, x10 = last ? n10 : c10, x11 = last ? n11 : c11;
;             PG8_LDB(B0, 0, 0); PG8_SCHED; PG8_LDA(At, 0, 0); PG8_STAGE(PG8_SA(1, 1), a1, c10, c11);
;             PG8_WAIT_L(8); PG8_BAR; PG8_WAIT_L(0); PG8_MMA(0, 0, At, B0); PG8_BAR; PG8_SCHED;
;             PG8_LDB(B1, 0, 1); PG8_STAGE(PG8_SB(0, 0), b2, voffB0, voffB1);
;             PG8_BAR; PG8_WAIT_L(0); PG8_MMA(0, 1, At, B1); PG8_BAR;
;             PG8_LDA(At, 0, 1); PG8_STAGE(PG8_SA(0, 0), a2, x00, x01);
;             PG8_BAR; PG8_WAIT_L(0); PG8_MMA(1, 0, At, B0); PG8_BAR; PG8_SCHED;
.LBB0_1679:
	s_add_u32 s40, s4, s38
	s_addc_u32 s41, s5, s39
	s_add_u32 s42, s40, 0x34c30100
	ds_read_b128 v[110:113], v174
	ds_read_b128 v[156:159], v174 offset:1024
	ds_read_b128 v[160:163], v174 offset:2048
	ds_read_b128 v[182:185], v174 offset:3072
	s_addc_u32 s43, s41, 0
	s_add_u32 s62, s37, s38
	s_addc_u32 s63, s60, s39
	s_cmpk_eq_i32 s38, 0xf00
	s_cselect_b64 vcc, -1, 0
	s_and_b64 s[40:41], vcc, exec
	v_cndmask_b32_e32 v150, v79, v177, vcc
	s_cselect_b32 s43, s7, s43
	s_cselect_b32 s42, s6, s42
	v_cndmask_b32_e32 v81, v80, v179, vcc
	s_cselect_b32 s41, s1, s63
	s_cselect_b32 s40, s0, s62
	v_cndmask_b32_e32 v164, v78, v178, vcc
	v_lshl_add_u64 v[96:97], v[94:95], 0, s[38:39]
	s_add_i32 m0, s47, 0xc000
	ds_read_b128 v[186:189], v175
	ds_read_b128 v[190:193], v175 offset:1024
	ds_read_b128 v[194:197], v175 offset:2048
	ds_read_b128 v[198:201], v175 offset:3072
	ds_read_b128 v[202:205], v175 offset:4096
	ds_read_b128 v[206:209], v175 offset:5120
	ds_read_b128 v[210:213], v175 offset:6144
	ds_read_b128 v[214:217], v175 offset:7168
	global_load_lds_dwordx4 v[96:97], off
	v_lshl_add_u64 v[96:97], v[88:89], 0, s[38:39]
	s_add_i32 m0, s47, 0xe000
	s_nop 0
	global_load_lds_dwordx4 v[96:97], off
	s_waitcnt lgkmcnt(8)
	s_barrier
	s_waitcnt lgkmcnt(0)
	s_setprio 1
	v_mfma_f32_16x16x32_bf16 v[142:145], v[110:113], v[186:189], v[142:145]
	v_mfma_f32_16x16x32_bf16 v[138:141], v[160:163], v[186:189], v[138:141]
	v_mfma_f32_16x16x32_bf16 v[134:137], v[110:113], v[194:197], v[134:137]
	v_mfma_f32_16x16x32_bf16 v[130:133], v[160:163], v[194:197], v[130:133]
	v_mfma_f32_16x16x32_bf16 v[122:125], v[110:113], v[202:205], v[122:125]
	v_mfma_f32_16x16x32_bf16 v[114:117], v[160:163], v[202:205], v[114:117]
	v_mfma_f32_16x16x32_bf16 v[102:105], v[110:113], v[210:213], v[102:105]
	v_mfma_f32_16x16x32_bf16 v[90:93], v[160:163], v[210:213], v[90:93]
	v_mfma_f32_16x16x32_bf16 v[142:145], v[156:159], v[190:193], v[142:145]
	v_mfma_f32_16x16x32_bf16 v[138:141], v[182:185], v[190:193], v[138:141]
	v_mfma_f32_16x16x32_bf16 v[134:137], v[156:159], v[198:201], v[134:137]
	v_mfma_f32_16x16x32_bf16 v[130:133], v[182:185], v[198:201], v[130:133]
	v_mfma_f32_16x16x32_bf16 v[122:125], v[156:159], v[206:209], v[122:125]
	v_mfma_f32_16x16x32_bf16 v[114:117], v[182:185], v[206:209], v[114:117]
	v_mfma_f32_16x16x32_bf16 v[102:105], v[156:159], v[214:217], v[102:105]
	v_mfma_f32_16x16x32_bf16 v[90:93], v[182:185], v[214:217], v[90:93]
	s_setprio 0
	s_barrier
	s_add_i32 s62, s54, s46
	v_lshl_add_u64 v[234:235], s[40:41], 0, v[148:149]
	s_mov_b32 m0, s62
	ds_read_b128 v[218:221], v176
	ds_read_b128 v[222:225], v176 offset:1024
	ds_read_b128 v[226:229], v176 offset:2048
	ds_read_b128 v[230:233], v176 offset:3072
	global_load_lds_dwordx4 v[234:235], off
	v_lshl_add_u64 v[236:237], s[40:41], 0, v[146:147]
	s_add_i32 m0, s62, 0x2000
	s_nop 0
	global_load_lds_dwordx4 v[236:237], off
	s_barrier
	s_waitcnt lgkmcnt(0)
	s_setprio 1
	v_mfma_f32_16x16x32_bf16 v[126:129], v[218:221], v[186:189], v[126:129]
	v_mfma_f32_16x16x32_bf16 v[118:121], v[226:229], v[186:189], v[118:121]
	v_mfma_f32_16x16x32_bf16 v[106:109], v[218:221], v[194:197], v[106:109]
	v_mfma_f32_16x16x32_bf16 v[96:99], v[226:229], v[194:197], v[98:101]
	v_mfma_f32_16x16x32_bf16 v[82:85], v[218:221], v[202:205], v[82:85]
	v_mfma_f32_16x16x32_bf16 v[74:77], v[226:229], v[202:205], v[74:77]
	v_mfma_f32_16x16x32_bf16 v[70:73], v[218:221], v[210:213], v[70:73]
	v_mfma_f32_16x16x32_bf16 v[66:69], v[226:229], v[210:213], v[66:69]
	v_mfma_f32_16x16x32_bf16 v[126:129], v[222:225], v[190:193], v[126:129]
	v_mfma_f32_16x16x32_bf16 v[118:121], v[230:233], v[190:193], v[118:121]
	v_mfma_f32_16x16x32_bf16 v[106:109], v[222:225], v[198:201], v[106:109]
	v_mfma_f32_16x16x32_bf16 v[96:99], v[230:233], v[198:201], v[96:99]
	v_mfma_f32_16x16x32_bf16 v[82:85], v[222:225], v[206:209], v[82:85]
	v_mfma_f32_16x16x32_bf16 v[74:77], v[230:233], v[206:209], v[74:77]
	v_mfma_f32_16x16x32_bf16 v[70:73], v[222:225], v[214:217], v[70:73]
	v_mfma_f32_16x16x32_bf16 v[66:69], v[230:233], v[214:217], v[66:69]
	s_setprio 0
	s_mov_b32 m0, s47
	s_barrier
	ds_read_b128 v[186:189], v175 offset:16384
	ds_read_b128 v[190:193], v175 offset:17408
	ds_read_b128 v[194:197], v175 offset:18432
	ds_read_b128 v[198:201], v175 offset:19456
	ds_read_b128 v[202:205], v175 offset:20480
	ds_read_b128 v[206:209], v175 offset:21504
	ds_read_b128 v[210:213], v175 offset:22528
	ds_read_b128 v[214:217], v175 offset:23552
	global_load_lds_dwordx4 v150, s[42:43]
	s_mov_b32 m0, s48
	v_mov_b32_e32 v165, v151
	global_load_lds_dwordx4 v164, s[42:43]
	s_barrier
	s_waitcnt lgkmcnt(0)
	v_lshl_add_u64 v[238:239], s[42:43], 0, v[150:151]
	v_lshl_add_u64 v[164:165], s[42:43], 0, v[164:165]
	s_setprio 1
	s_waitcnt lgkmcnt(0)
	v_mfma_f32_16x16x32_bf16 v[62:65], v[110:113], v[186:189], v[62:65]
	v_mfma_f32_16x16x32_bf16 v[58:61], v[160:163], v[186:189], v[58:61]
	v_mfma_f32_16x16x32_bf16 v[54:57], v[110:113], v[194:197], v[54:57]
	v_mfma_f32_16x16x32_bf16 v[46:49], v[160:163], v[194:197], v[46:49]
	v_mfma_f32_16x16x32_bf16 v[38:41], v[110:113], v[202:205], v[38:41]
	v_mfma_f32_16x16x32_bf16 v[30:33], v[160:163], v[202:205], v[30:33]
	v_mfma_f32_16x16x32_bf16 v[22:25], v[110:113], v[210:213], v[22:25]
	v_mfma_f32_16x16x32_bf16 v[14:17], v[160:163], v[210:213], v[14:17]
	v_mfma_f32_16x16x32_bf16 v[62:65], v[156:159], v[190:193], v[62:65]
	v_mfma_f32_16x16x32_bf16 v[58:61], v[182:185], v[190:193], v[58:61]
	v_mfma_f32_16x16x32_bf16 v[54:57], v[156:159], v[198:201], v[54:57]
	v_mfma_f32_16x16x32_bf16 v[46:49], v[182:185], v[198:201], v[46:49]
	v_mfma_f32_16x16x32_bf16 v[38:41], v[156:159], v[206:209], v[38:41]
	v_mfma_f32_16x16x32_bf16 v[30:33], v[182:185], v[206:209], v[30:33]
	v_mfma_f32_16x16x32_bf16 v[22:25], v[156:159], v[214:217], v[22:25]
	v_mfma_f32_16x16x32_bf16 v[14:17], v[182:185], v[214:217], v[14:17]
	s_setprio 0
	s_barrier
; #define PG8_STAGE(bufoff, gbase, v0, v1) do { \
;         __builtin_amdgcn_global_load_lds((const unsigned*)((const char*)(gbase) + (v0)), (LAS unsigned*)(lds + (bufoff) + ldsw), 16, 0, 0); \
;         __builtin_amdgcn_global_load_lds((const unsigned*)((const char*)(gbase) + (v1)), (LAS unsigned*)(lds + (bufoff) + ldsw + 8192), 16, 0, 0); } while (0)
; #define PG8_LDA(dst, b, h) do { _Pragma("unroll") for (int m = 0; m < 4; ++m) _Pragma("unroll") for (int k = 0; k < 2; ++k) dst[m][k] = *(const LAS bf16x8*)(lds + PG8_SA(b, h) + aoff + m * 2048 + k * 1024); } while (0)
; #define PG8_LDB(dst, b, h) do { _Pragma("unroll") for (int n = 0; n < 2; ++n) _Pragma("unroll") for (int k = 0; k < 2; ++k) dst[n][k] = *(const LAS bf16x8*)(lds + PG8_SB(b, h) + boff + n * 2048 + k * 1024); } while (0)
; #define PG8_MMA(ai, bj, At, Bt) do { __builtin_amdgcn_s_setprio(1); _Pragma("unroll") for (int m = 0; m < 4; ++m) _Pragma("unroll") for (int n = 0; n < 2; ++n) _Pragma("unroll") for (int k = 0; k < 2; ++k) \
;         acc[ai][bj][m][n] = __builtin_amdgcn_mfma_f32_16x16x32_bf16(Bt[n][k], At[m][k], acc[ai][bj][m][n], 0, 0, 0); __builtin_amdgcn_s_setprio(0); } while (0)
; #define PG8_WAIT_V(n) asm volatile("s_waitcnt vmcnt(" #n ")" ::: "memory")
; #define PG8_WAIT_L(n) asm volatile("s_waitcnt lgkmcnt(" #n ")" ::: "memory")
; #define PG8_BAR __builtin_amdgcn_s_barrier()
; #define PG8_SCHED __builtin_amdgcn_sched_barrier(0)
; template <class Epi, class Sched>
; __device__ __forceinline__ void gemm_phase(LAS unsigned char* lds, const int K, const Sched& S, const Epi& E) {
;     ...
;             PG8_STAGE(PG8_SB(0, 1), b2 + hstep, voffB0, voffB1);
;             PG8_WAIT_V(6); PG8_BAR; PG8_MMA(1, 1, At, B1); PG8_BAR;
;             PG8_LDB(B0, 1, 0); PG8_SCHED; PG8_LDA(At, 1, 0); PG8_STAGE(PG8_SA(0, 1), a2, x10, x11);
;             PG8_WAIT_L(8); PG8_BAR; PG8_WAIT_L(0); PG8_MMA(0, 0, At, B0); PG8_BAR; PG8_SCHED;
;             PG8_LDB(B1, 1, 1); PG8_STAGE(PG8_SB(1, 0), b3, voffB0, voffB1);
;             PG8_BAR; PG8_WAIT_L(0); PG8_MMA(0, 1, At, B1); PG8_BAR;
;             PG8_LDA(At, 1, 1); PG8_STAGE(PG8_SA(1, 0), a3, x00, x01);
	s_add_u32 s62, s40, 0x80000
	s_addc_u32 s63, s41, 0
	s_add_i32 s64, s55, s46
	v_lshl_add_u64 v[100:101], s[62:63], 0, v[148:149]
	s_mov_b32 m0, s64
	s_nop 0
	global_load_lds_dwordx4 v[100:101], off
	v_lshl_add_u64 v[100:101], s[62:63], 0, v[146:147]
	s_add_i32 m0, s64, 0x2000
	s_nop 0
	global_load_lds_dwordx4 v[100:101], off
	s_waitcnt vmcnt(6)
	s_barrier
	s_setprio 1
	v_mfma_f32_16x16x32_bf16 v[50:53], v[218:221], v[186:189], v[50:53]
	v_mfma_f32_16x16x32_bf16 v[42:45], v[226:229], v[186:189], v[42:45]
	v_mfma_f32_16x16x32_bf16 v[34:37], v[218:221], v[194:197], v[34:37]
	v_mfma_f32_16x16x32_bf16 v[26:29], v[226:229], v[194:197], v[26:29]
	v_mfma_f32_16x16x32_bf16 v[18:21], v[218:221], v[202:205], v[18:21]
	v_mfma_f32_16x16x32_bf16 v[10:13], v[226:229], v[202:205], v[10:13]
	v_mfma_f32_16x16x32_bf16 v[6:9], v[218:221], v[210:213], v[6:9]
	v_mfma_f32_16x16x32_bf16 v[2:5], v[226:229], v[210:213], v[2:5]
	v_mfma_f32_16x16x32_bf16 v[50:53], v[222:225], v[190:193], v[50:53]
	v_mfma_f32_16x16x32_bf16 v[42:45], v[230:233], v[190:193], v[42:45]
	v_mfma_f32_16x16x32_bf16 v[34:37], v[222:225], v[198:201], v[34:37]
	v_mfma_f32_16x16x32_bf16 v[26:29], v[230:233], v[198:201], v[26:29]
	v_mfma_f32_16x16x32_bf16 v[18:21], v[222:225], v[206:209], v[18:21]
	v_mfma_f32_16x16x32_bf16 v[10:13], v[230:233], v[206:209], v[10:13]
	v_mfma_f32_16x16x32_bf16 v[6:9], v[222:225], v[214:217], v[6:9]
	v_mfma_f32_16x16x32_bf16 v[2:5], v[230:233], v[214:217], v[2:5]
	s_setprio 0
	s_add_i32 s62, 0, 0x18000
	v_add_u32_e32 v87, s62, v172
	s_barrier
	ds_read_b128 v[110:113], v87
	ds_read_b128 v[156:159], v87 offset:1024
	ds_read_b128 v[160:163], v87 offset:2048
	ds_read_b128 v[182:185], v87 offset:3072
	s_mov_b32 m0, s49
	ds_read_b128 v[186:189], v175 offset:32768
	ds_read_b128 v[190:193], v175 offset:33792
	ds_read_b128 v[194:197], v175 offset:34816
	ds_read_b128 v[198:201], v175 offset:35840
	ds_read_b128 v[202:205], v175 offset:36864
	ds_read_b128 v[206:209], v175 offset:37888
	ds_read_b128 v[210:213], v175 offset:38912
	ds_read_b128 v[214:217], v175 offset:39936
	v_cndmask_b32_e32 v87, v86, v180, vcc
	global_load_lds_dwordx4 v81, s[42:43]
	s_mov_b32 m0, s50
	s_nop 0
	global_load_lds_dwordx4 v87, s[42:43]
	s_waitcnt lgkmcnt(8)
	s_barrier
	s_waitcnt lgkmcnt(0)
	s_setprio 1
	v_mfma_f32_16x16x32_bf16 v[142:145], v[110:113], v[186:189], v[142:145]
	v_mfma_f32_16x16x32_bf16 v[138:141], v[160:163], v[186:189], v[138:141]
	v_mfma_f32_16x16x32_bf16 v[134:137], v[110:113], v[194:197], v[134:137]
	v_mfma_f32_16x16x32_bf16 v[130:133], v[160:163], v[194:197], v[130:133]
	v_mfma_f32_16x16x32_bf16 v[122:125], v[110:113], v[202:205], v[122:125]
	v_mfma_f32_16x16x32_bf16 v[114:117], v[160:163], v[202:205], v[114:117]
	v_mfma_f32_16x16x32_bf16 v[100:103], v[110:113], v[210:213], v[102:105]
	v_mfma_f32_16x16x32_bf16 v[90:93], v[160:163], v[210:213], v[90:93]
	v_mfma_f32_16x16x32_bf16 v[142:145], v[156:159], v[190:193], v[142:145]
	v_mfma_f32_16x16x32_bf16 v[138:141], v[182:185], v[190:193], v[138:141]
	v_mfma_f32_16x16x32_bf16 v[134:137], v[156:159], v[198:201], v[134:137]
	v_mfma_f32_16x16x32_bf16 v[130:133], v[182:185], v[198:201], v[130:133]
	v_mfma_f32_16x16x32_bf16 v[122:125], v[156:159], v[206:209], v[122:125]
	v_mfma_f32_16x16x32_bf16 v[114:117], v[182:185], v[206:209], v[114:117]
	v_mfma_f32_16x16x32_bf16 v[102:105], v[156:159], v[214:217], v[100:103]
	v_mfma_f32_16x16x32_bf16 v[90:93], v[182:185], v[214:217], v[90:93]
	s_setprio 0
	s_barrier
	s_add_i32 s42, 0, 0x1c000
	s_add_i32 s43, s62, s46
	v_add_u32_e32 v81, s42, v172
	v_lshl_add_u64 v[100:101], v[234:235], 0, s[18:19]
	s_mov_b32 m0, s43
	ds_read_b128 v[218:221], v81
	ds_read_b128 v[222:225], v81 offset:1024
	ds_read_b128 v[226:229], v81 offset:2048
	ds_read_b128 v[230:233], v81 offset:3072
	global_load_lds_dwordx4 v[100:101], off
	v_lshl_add_u64 v[100:101], v[236:237], 0, s[18:19]
	s_add_i32 m0, s43, 0x2000
	s_nop 0
	global_load_lds_dwordx4 v[100:101], off
	s_barrier
	s_waitcnt lgkmcnt(0)
	s_setprio 1
	v_mfma_f32_16x16x32_bf16 v[126:129], v[218:221], v[186:189], v[126:129]
	v_mfma_f32_16x16x32_bf16 v[118:121], v[226:229], v[186:189], v[118:121]
	v_mfma_f32_16x16x32_bf16 v[106:109], v[218:221], v[194:197], v[106:109]
	v_mfma_f32_16x16x32_bf16 v[96:99], v[226:229], v[194:197], v[96:99]
	v_mfma_f32_16x16x32_bf16 v[82:85], v[218:221], v[202:205], v[82:85]
	v_mfma_f32_16x16x32_bf16 v[74:77], v[226:229], v[202:205], v[74:77]
	v_mfma_f32_16x16x32_bf16 v[70:73], v[218:221], v[210:213], v[70:73]
	v_mfma_f32_16x16x32_bf16 v[66:69], v[226:229], v[210:213], v[66:69]
	v_mfma_f32_16x16x32_bf16 v[126:129], v[222:225], v[190:193], v[126:129]
	v_mfma_f32_16x16x32_bf16 v[118:121], v[230:233], v[190:193], v[118:121]
	v_mfma_f32_16x16x32_bf16 v[106:109], v[222:225], v[198:201], v[106:109]
	v_mfma_f32_16x16x32_bf16 v[98:101], v[230:233], v[198:201], v[96:99]
	v_mfma_f32_16x16x32_bf16 v[82:85], v[222:225], v[206:209], v[82:85]
	v_mfma_f32_16x16x32_bf16 v[74:77], v[230:233], v[206:209], v[74:77]
	v_mfma_f32_16x16x32_bf16 v[70:73], v[222:225], v[214:217], v[70:73]
	v_mfma_f32_16x16x32_bf16 v[66:69], v[230:233], v[214:217], v[66:69]
	s_setprio 0
	s_mov_b32 m0, s52
	v_lshl_add_u64 v[96:97], v[238:239], 0, s[18:19]
	s_barrier
	ds_read_b128 v[186:189], v175 offset:49152
	ds_read_b128 v[190:193], v175 offset:50176
	ds_read_b128 v[194:197], v175 offset:51200
	ds_read_b128 v[198:201], v175 offset:52224
	ds_read_b128 v[202:205], v175 offset:53248
	ds_read_b128 v[206:209], v175 offset:54272
	ds_read_b128 v[210:213], v175 offset:55296
	ds_read_b128 v[214:217], v175 offset:56320
	global_load_lds_dwordx4 v[96:97], off
	v_lshl_add_u64 v[96:97], v[164:165], 0, s[18:19]
	s_mov_b32 m0, s53
	s_nop 0
	global_load_lds_dwordx4 v[96:97], off
	s_barrier
; #define PG8_STAGE(bufoff, gbase, v0, v1) do { \
;         __builtin_amdgcn_global_load_lds((const unsigned*)((const char*)(gbase) + (v0)), (LAS unsigned*)(lds + (bufoff) + ldsw), 16, 0, 0); \
;         __builtin_amdgcn_global_load_lds((const unsigned*)((const char*)(gbase) + (v1)), (LAS unsigned*)(lds + (bufoff) + ldsw + 8192), 16, 0, 0); } while (0)
; #define PG8_MMA(ai, bj, At, Bt) do { __builtin_amdgcn_s_setprio(1); _Pragma("unroll") for (int m = 0; m < 4; ++m) _Pragma("unroll") for (int n = 0; n < 2; ++n) _Pragma("unroll") for (int k = 0; k < 2; ++k) \
;         acc[ai][bj][m][n] = __builtin_amdgcn_mfma_f32_16x16x32_bf16(Bt[n][k], At[m][k], acc[ai][bj][m][n], 0, 0, 0); __builtin_amdgcn_s_setprio(0); } while (0)
; #define PG8_WAIT_V(n) asm volatile("s_waitcnt vmcnt(" #n ")" ::: "memory")
; #define PG8_WAIT_L(n) asm volatile("s_waitcnt lgkmcnt(" #n ")" ::: "memory")
; #define PG8_BAR __builtin_amdgcn_s_barrier()
; #define PG8_SCHED __builtin_amdgcn_sched_barrier(0)
; template <class Epi, class Sched>
; __device__ __forceinline__ void gemm_phase(LAS unsigned char* lds, const int K, const Sched& S, const Epi& E) {
;     ...
;             PG8_BAR; PG8_WAIT_L(0); PG8_MMA(1, 0, At, B0); PG8_BAR; PG8_SCHED;
;             PG8_STAGE(PG8_SB(1, 1), b3 + hstep, voffB0, voffB1);
;             PG8_WAIT_V(6); PG8_BAR; PG8_MMA(1, 1, At, B1); PG8_BAR;
;     __device__ __forceinline__ void operator()(const f32x4 (&acc)[2][2][4][2], const Unit& u, int wr, int wc, int fr, int fq) const {
;         const int row0 = u.rbase + wr * 64 + fr, col0 = u.pn * BM + wc * 32 + 4 * fq;
;         f32x4 gv[2][2];
; #pragma unroll
;         for (int bj = 0; bj < 2; ++bj)
; #pragma unroll
;             for (int n = 0; n < 2; ++n) gv[bj][n] = *(const f32x4*)(gate + col0 + bj * HALF + n * 16);
; #pragma unroll
;         for (int ai = 0; ai < 2; ++ai) {
;             f32x4 xv[4][2][2];
; #pragma unroll
;             for (int m = 0; m < 4; ++m) { const size_t ro = (size_t)(row0 + ai * HALF + m * 16) * D + col0;
; #pragma unroll
;                 for (int bj = 0; bj < 2; ++bj)
; #pragma unroll
;                     for (int n = 0; n < 2; ++n) xv[m][bj][n] = *(const f32x4*)(xin + ro + bj * HALF + n * 16); }
	s_waitcnt lgkmcnt(0)
	s_setprio 1
	v_mfma_f32_16x16x32_bf16 v[62:65], v[110:113], v[186:189], v[62:65]
	v_mfma_f32_16x16x32_bf16 v[58:61], v[160:163], v[186:189], v[58:61]
	v_mfma_f32_16x16x32_bf16 v[54:57], v[110:113], v[194:197], v[54:57]
	v_mfma_f32_16x16x32_bf16 v[46:49], v[160:163], v[194:197], v[46:49]
	v_mfma_f32_16x16x32_bf16 v[38:41], v[110:113], v[202:205], v[38:41]
	v_mfma_f32_16x16x32_bf16 v[30:33], v[160:163], v[202:205], v[30:33]
	v_mfma_f32_16x16x32_bf16 v[22:25], v[110:113], v[210:213], v[22:25]
	v_mfma_f32_16x16x32_bf16 v[14:17], v[160:163], v[210:213], v[14:17]
	v_mfma_f32_16x16x32_bf16 v[62:65], v[156:159], v[190:193], v[62:65]
	v_mfma_f32_16x16x32_bf16 v[58:61], v[182:185], v[190:193], v[58:61]
	v_mfma_f32_16x16x32_bf16 v[54:57], v[156:159], v[198:201], v[54:57]
	v_mfma_f32_16x16x32_bf16 v[46:49], v[182:185], v[198:201], v[46:49]
	v_mfma_f32_16x16x32_bf16 v[38:41], v[156:159], v[206:209], v[38:41]
	v_mfma_f32_16x16x32_bf16 v[30:33], v[182:185], v[206:209], v[30:33]
	v_mfma_f32_16x16x32_bf16 v[22:25], v[156:159], v[214:217], v[22:25]
	v_mfma_f32_16x16x32_bf16 v[14:17], v[182:185], v[214:217], v[14:17]
	s_setprio 0
	s_barrier
	s_add_u32 s40, s40, 0x80080
	s_addc_u32 s41, s41, 0
	s_add_i32 s42, s42, s46
	v_lshl_add_u64 v[96:97], s[40:41], 0, v[148:149]
	s_mov_b32 m0, s42
	s_nop 0
	global_load_lds_dwordx4 v[96:97], off
	v_lshl_add_u64 v[96:97], s[40:41], 0, v[146:147]
	s_add_i32 m0, s42, 0x2000
	s_nop 0
	global_load_lds_dwordx4 v[96:97], off
	s_waitcnt vmcnt(6)
	s_barrier
	s_setprio 1
	v_mfma_f32_16x16x32_bf16 v[50:53], v[218:221], v[186:189], v[50:53]
	v_mfma_f32_16x16x32_bf16 v[42:45], v[226:229], v[186:189], v[42:45]
	v_mfma_f32_16x16x32_bf16 v[34:37], v[218:221], v[194:197], v[34:37]
	v_mfma_f32_16x16x32_bf16 v[26:29], v[226:229], v[194:197], v[26:29]
	v_mfma_f32_16x16x32_bf16 v[18:21], v[218:221], v[202:205], v[18:21]
	v_mfma_f32_16x16x32_bf16 v[10:13], v[226:229], v[202:205], v[10:13]
	v_mfma_f32_16x16x32_bf16 v[6:9], v[218:221], v[210:213], v[6:9]
	v_mfma_f32_16x16x32_bf16 v[2:5], v[226:229], v[210:213], v[2:5]
	v_mfma_f32_16x16x32_bf16 v[50:53], v[222:225], v[190:193], v[50:53]
	v_mfma_f32_16x16x32_bf16 v[42:45], v[230:233], v[190:193], v[42:45]
	v_mfma_f32_16x16x32_bf16 v[34:37], v[222:225], v[198:201], v[34:37]
	v_mfma_f32_16x16x32_bf16 v[26:29], v[230:233], v[198:201], v[26:29]
	v_mfma_f32_16x16x32_bf16 v[18:21], v[222:225], v[206:209], v[18:21]
	v_mfma_f32_16x16x32_bf16 v[10:13], v[230:233], v[206:209], v[10:13]
	v_mfma_f32_16x16x32_bf16 v[6:9], v[222:225], v[214:217], v[6:9]
	v_mfma_f32_16x16x32_bf16 v[2:5], v[230:233], v[214:217], v[2:5]
	s_setprio 0
	s_add_i32 s61, s61, 2
	s_add_u32 s38, s38, 0x100
	s_addc_u32 s39, s39, 0
	s_cmp_gt_u32 s61, 29
	s_barrier
	s_cbranch_scc0 .LBB0_1679
	v_lshl_or_b32 v78, s59, 8, v173
	v_ashrrev_i32_e32 v79, 31, v78
	v_add_u32_e32 v160, s58, v171
	v_lshlrev_b64 v[156:157], 2, v[78:79]
	v_ashrrev_i32_e32 v161, 31, v160
	v_lshl_add_u64 v[158:159], s[10:11], 0, v[156:157]
	v_lshlrev_b64 v[160:161], 13, v[160:161]
	v_lshl_add_u64 v[78:79], s[14:15], 0, v[156:157]
	v_lshl_add_u64 v[190:191], v[158:159], 0, v[160:161]
	global_load_dwordx4 v[110:113], v[78:79], off
	global_load_dwordx4 v[94:97], v[78:79], off offset:64
	global_load_dwordx4 v[86:89], v[78:79], off offset:512
	s_nop 0
	global_load_dwordx4 v[78:81], v[78:79], off offset:576
	s_nop 0
	global_load_dwordx4 v[162:165], v[190:191], off
	global_load_dwordx4 v[182:185], v[190:191], off offset:64
	global_load_dwordx4 v[186:189], v[190:191], off offset:512
	s_nop 0
	global_load_dwordx4 v[190:193], v[190:191], off offset:576
	v_lshl_add_u64 v[242:243], v[160:161], 0, s[20:21]
	v_lshl_add_u64 v[206:207], v[158:159], 0, v[242:243]
	global_load_dwordx4 v[194:197], v[206:207], off
	global_load_dwordx4 v[198:201], v[206:207], off offset:64
	global_load_dwordx4 v[202:205], v[206:207], off offset:512
	s_nop 0
	global_load_dwordx4 v[206:209], v[206:207], off offset:576
	v_lshl_add_u64 v[244:245], v[160:161], 0, s[22:23]
	v_lshl_add_u64 v[222:223], v[158:159], 0, v[244:245]
	global_load_dwordx4 v[210:213], v[222:223], off
	global_load_dwordx4 v[214:217], v[222:223], off offset:64
	global_load_dwordx4 v[218:221], v[222:223], off offset:512
	s_nop 0
	global_load_dwordx4 v[222:225], v[222:223], off offset:576
	v_lshl_add_u64 v[246:247], v[160:161], 0, s[24:25]
	v_lshl_add_u64 v[238:239], v[158:159], 0, v[246:247]
	global_load_dwordx4 v[226:229], v[238:239], off
	global_load_dwordx4 v[230:233], v[238:239], off offset:64
	global_load_dwordx4 v[234:237], v[238:239], off offset:512
	s_nop 0
	global_load_dwordx4 v[238:241], v[238:239], off offset:576
	s_and_b64 vcc, exec, s[2:3]
	s_mov_b32 s59, s36
	s_mov_b32 s58, s56
	s_mov_b64 s[38:39], s[0:1]
	s_waitcnt vmcnt(0)
;     __device__ __forceinline__ void operator()(const f32x4 (&acc)[2][2][4][2], const Unit& u, int wr, int wc, int fr, int fq) const {
;     ...
;         for (int ai = 0; ai < 2; ++ai) {
;             f32x4 xv[4][2][2];
; #pragma unroll
;             for (int m = 0; m < 4; ++m) { const size_t ro = (size_t)(row0 + ai * HALF + m * 16) * D + col0;
; #pragma unroll
;                 for (int bj = 0; bj < 2; ++bj)
; #pragma unroll
;                     for (int n = 0; n < 2; ++n) xv[m][bj][n] = *(const f32x4*)(xin + ro + bj * HALF + n * 16); }
; #pragma unroll
;             for (int m = 0; m < 4; ++m) { const size_t ro = (size_t)(row0 + ai * HALF + m * 16) * D + col0;
; #pragma unroll
;                 for (int bj = 0; bj < 2; ++bj)
; #pragma unroll
;                     for (int n = 0; n < 2; ++n) *(f32x4*)(out + ro + bj * HALF + n * 16) = xv[m][bj][n] + gv[bj][n] * acc[ai][bj][m][n]; }
	v_pk_fma_f32 v[142:143], v[142:143], v[110:111], v[162:163]
	v_lshl_add_u64 v[162:163], s[12:13], 0, v[160:161]
	v_lshl_add_u64 v[162:163], v[162:163], 0, v[156:157]
	v_pk_fma_f32 v[128:129], v[128:129], v[88:89], v[188:189]
	v_pk_fma_f32 v[126:127], v[126:127], v[86:87], v[186:187]
	global_store_dwordx4 v[162:163], v[126:129], off offset:512
	v_pk_fma_f32 v[108:109], v[108:109], v[88:89], v[204:205]
	v_pk_fma_f32 v[106:107], v[106:107], v[86:87], v[202:203]
	v_lshl_add_u64 v[126:127], s[12:13], 0, v[242:243]
	v_lshl_add_u64 v[126:127], v[126:127], 0, v[156:157]
	global_store_dwordx4 v[126:127], v[106:109], off offset:512
	v_pk_fma_f32 v[84:85], v[84:85], v[88:89], v[220:221]
	v_pk_fma_f32 v[82:83], v[82:83], v[86:87], v[218:219]
	v_lshl_add_u64 v[106:107], s[12:13], 0, v[244:245]
	v_lshl_add_u64 v[106:107], v[106:107], 0, v[156:157]
	v_pk_fma_f32 v[120:121], v[120:121], v[80:81], v[192:193]
	v_pk_fma_f32 v[118:119], v[118:119], v[78:79], v[190:191]
	v_pk_fma_f32 v[100:101], v[100:101], v[80:81], v[208:209]
	v_pk_fma_f32 v[98:99], v[98:99], v[78:79], v[206:207]
	global_store_dwordx4 v[106:107], v[82:85], off offset:512
	v_pk_fma_f32 v[76:77], v[76:77], v[80:81], v[224:225]
	v_pk_fma_f32 v[74:75], v[74:75], v[78:79], v[222:223]
	v_lshl_add_u64 v[82:83], s[12:13], 0, v[246:247]
	global_store_dwordx4 v[162:163], v[118:121], off offset:576
	global_store_dwordx4 v[126:127], v[98:101], off offset:576
	global_store_dwordx4 v[106:107], v[74:77], off offset:576
	v_pk_fma_f32 v[120:121], v[136:137], v[112:113], v[196:197]
	v_pk_fma_f32 v[118:119], v[134:135], v[110:111], v[194:195]
	v_pk_fma_f32 v[100:101], v[124:125], v[112:113], v[212:213]
	v_pk_fma_f32 v[98:99], v[122:123], v[110:111], v[210:211]
	v_pk_fma_f32 v[76:77], v[104:105], v[112:113], v[228:229]
	v_pk_fma_f32 v[74:75], v[102:103], v[110:111], v[226:227]
	v_lshl_add_u64 v[82:83], v[82:83], 0, v[156:157]
	v_pk_fma_f32 v[144:145], v[144:145], v[112:113], v[164:165]
	v_pk_fma_f32 v[140:141], v[140:141], v[96:97], v[184:185]
	v_pk_fma_f32 v[138:139], v[138:139], v[94:95], v[182:183]
	global_store_dwordx4 v[126:127], v[118:121], off
	global_store_dwordx4 v[106:107], v[98:101], off
	global_store_dwordx4 v[82:83], v[74:77], off
	v_pk_fma_f32 v[120:121], v[132:133], v[96:97], v[200:201]
	v_pk_fma_f32 v[118:119], v[130:131], v[94:95], v[198:199]
	v_pk_fma_f32 v[100:101], v[116:117], v[96:97], v[216:217]
	v_pk_fma_f32 v[98:99], v[114:115], v[94:95], v[214:215]
	v_pk_fma_f32 v[76:77], v[92:93], v[96:97], v[232:233]
	v_pk_fma_f32 v[74:75], v[90:91], v[94:95], v[230:231]
	v_pk_fma_f32 v[72:73], v[72:73], v[88:89], v[236:237]
	v_pk_fma_f32 v[70:71], v[70:71], v[86:87], v[234:235]
	v_pk_fma_f32 v[68:69], v[68:69], v[80:81], v[240:241]
	v_pk_fma_f32 v[66:67], v[66:67], v[78:79], v[238:239]
	v_lshl_add_u64 v[164:165], v[160:161], 0, s[26:27]
	global_store_dwordx4 v[162:163], v[142:145], off
	global_store_dwordx4 v[162:163], v[138:141], off offset:64
	global_store_dwordx4 v[126:127], v[118:121], off offset:64
	global_store_dwordx4 v[106:107], v[98:101], off offset:64
	global_store_dwordx4 v[82:83], v[74:77], off offset:64
	global_store_dwordx4 v[82:83], v[70:73], off offset:512
	global_store_dwordx4 v[82:83], v[66:69], off offset:576
	v_lshl_add_u64 v[162:163], v[160:161], 0, s[28:29]
	v_lshl_add_u64 v[142:143], v[160:161], 0, s[30:31]
	v_lshl_add_u64 v[66:67], v[158:159], 0, v[164:165]
	global_load_dwordx4 v[130:133], v[66:67], off
	global_load_dwordx4 v[122:125], v[66:67], off offset:64
	global_load_dwordx4 v[118:121], v[66:67], off offset:512
	global_load_dwordx4 v[106:109], v[66:67], off offset:576
	v_lshl_add_u64 v[66:67], v[158:159], 0, v[162:163]
	global_load_dwordx4 v[114:117], v[66:67], off
	global_load_dwordx4 v[102:105], v[66:67], off offset:64
	global_load_dwordx4 v[90:93], v[66:67], off offset:512
	global_load_dwordx4 v[74:77], v[66:67], off offset:576
	v_lshl_add_u64 v[66:67], v[158:159], 0, v[142:143]
	global_load_dwordx4 v[98:101], v[66:67], off
	global_load_dwordx4 v[82:85], v[66:67], off offset:64
	global_load_dwordx4 v[70:73], v[66:67], off offset:512
	s_nop 0
	global_load_dwordx4 v[66:69], v[66:67], off offset:576
	v_lshl_add_u64 v[144:145], v[160:161], 0, s[34:35]
	v_lshl_add_u64 v[138:139], v[158:159], 0, v[144:145]
	global_load_dwordx4 v[158:161], v[138:139], off
	global_load_dwordx4 v[134:137], v[138:139], off offset:64
	global_load_dwordx4 v[126:129], v[138:139], off offset:512
	s_nop 0
	global_load_dwordx4 v[138:141], v[138:139], off offset:576
	s_waitcnt vmcnt(0)
; #define PG8_WAIT_V(n) asm volatile("s_waitcnt vmcnt(" #n ")" ::: "memory")
; #define PG8_BAR __builtin_amdgcn_s_barrier()
; template <class Epi, class Sched>
; __device__ __forceinline__ void gemm_phase(LAS unsigned char* lds, const int K, const Sched& S, const Epi& E) {
;     ...
;         E(acc, cur, wr, wc, fr, fq);
;         if (!has_next) break;
; #pragma unroll
;         for (int a = 0; a < 2; ++a)
; #pragma unroll
;             for (int b = 0; b < 2; ++b)
; #pragma unroll
;                 for (int m = 0; m < 4; ++m)
; #pragma unroll
;                     for (int n = 0; n < 2; ++n) acc[a][b][m][n] = (f32x4){0.f, 0.f, 0.f, 0.f};
;         cur = nxt; cB = nB; c00 = n00; c01 = n01; c10 = n10; c11 = n11; ++ui;
;     }
;     PG8_WAIT_V(0);
;     if (wr == 0) PG8_BAR;
;     PG8_BAR;
;     __device__ __forceinline__ void operator()(const f32x4 (&acc)[2][2][4][2], const Unit& u, int wr, int wc, int fr, int fq) const {
;     ...
;             for (int m = 0; m < 4; ++m) { const size_t ro = (size_t)(row0 + ai * HALF + m * 16) * D + col0;
; #pragma unroll
;                 for (int bj = 0; bj < 2; ++bj)
; #pragma unroll
;                     for (int n = 0; n < 2; ++n) *(f32x4*)(out + ro + bj * HALF + n * 16) = xv[m][bj][n] + gv[bj][n] * acc[ai][bj][m][n]; }
	v_pk_fma_f32 v[62:63], v[62:63], v[110:111], v[130:131]
	v_lshl_add_u64 v[130:131], s[12:13], 0, v[164:165]
	v_lshl_add_u64 v[130:131], v[130:131], 0, v[156:157]
	v_pk_fma_f32 v[52:53], v[52:53], v[88:89], v[120:121]
	v_pk_fma_f32 v[50:51], v[50:51], v[86:87], v[118:119]
	global_store_dwordx4 v[130:131], v[50:53], off offset:512
	v_pk_fma_f32 v[36:37], v[36:37], v[88:89], v[92:93]
	v_pk_fma_f32 v[34:35], v[34:35], v[86:87], v[90:91]
	v_lshl_add_u64 v[50:51], s[12:13], 0, v[162:163]
	v_lshl_add_u64 v[50:51], v[50:51], 0, v[156:157]
	global_store_dwordx4 v[50:51], v[34:37], off offset:512
	v_pk_fma_f32 v[20:21], v[20:21], v[88:89], v[72:73]
	v_pk_fma_f32 v[18:19], v[18:19], v[86:87], v[70:71]
	v_lshl_add_u64 v[34:35], s[12:13], 0, v[142:143]
	v_lshl_add_u64 v[34:35], v[34:35], 0, v[156:157]
	v_pk_fma_f32 v[44:45], v[44:45], v[80:81], v[108:109]
	v_pk_fma_f32 v[42:43], v[42:43], v[78:79], v[106:107]
	v_pk_fma_f32 v[28:29], v[28:29], v[80:81], v[76:77]
	v_pk_fma_f32 v[26:27], v[26:27], v[78:79], v[74:75]
	global_store_dwordx4 v[34:35], v[18:21], off offset:512
	v_pk_fma_f32 v[12:13], v[12:13], v[80:81], v[68:69]
	v_pk_fma_f32 v[10:11], v[10:11], v[78:79], v[66:67]
	v_lshl_add_u64 v[18:19], s[12:13], 0, v[144:145]
	global_store_dwordx4 v[130:131], v[42:45], off offset:576
	global_store_dwordx4 v[50:51], v[26:29], off offset:576
	global_store_dwordx4 v[34:35], v[10:13], off offset:576
	v_pk_fma_f32 v[44:45], v[56:57], v[112:113], v[116:117]
	v_pk_fma_f32 v[42:43], v[54:55], v[110:111], v[114:115]
	v_pk_fma_f32 v[28:29], v[40:41], v[112:113], v[100:101]
	v_pk_fma_f32 v[26:27], v[38:39], v[110:111], v[98:99]
	v_pk_fma_f32 v[12:13], v[24:25], v[112:113], v[160:161]
	v_pk_fma_f32 v[10:11], v[22:23], v[110:111], v[158:159]
	v_lshl_add_u64 v[18:19], v[18:19], 0, v[156:157]
	v_pk_fma_f32 v[64:65], v[64:65], v[112:113], v[132:133]
	v_pk_fma_f32 v[60:61], v[60:61], v[96:97], v[124:125]
	v_pk_fma_f32 v[58:59], v[58:59], v[94:95], v[122:123]
	global_store_dwordx4 v[50:51], v[42:45], off
	global_store_dwordx4 v[34:35], v[26:29], off
	global_store_dwordx4 v[18:19], v[10:13], off
	v_pk_fma_f32 v[44:45], v[48:49], v[96:97], v[104:105]
	v_pk_fma_f32 v[42:43], v[46:47], v[94:95], v[102:103]
	v_pk_fma_f32 v[28:29], v[32:33], v[96:97], v[84:85]
	v_pk_fma_f32 v[26:27], v[30:31], v[94:95], v[82:83]
	v_pk_fma_f32 v[12:13], v[16:17], v[96:97], v[136:137]
	v_pk_fma_f32 v[10:11], v[14:15], v[94:95], v[134:135]
	v_pk_fma_f32 v[8:9], v[8:9], v[88:89], v[128:129]
	v_pk_fma_f32 v[6:7], v[6:7], v[86:87], v[126:127]
	v_pk_fma_f32 v[4:5], v[4:5], v[80:81], v[140:141]
	v_pk_fma_f32 v[2:3], v[2:3], v[78:79], v[138:139]
	v_mov_b32_e32 v79, v177
	v_mov_b32_e32 v78, v178
	v_mov_b32_e32 v80, v179
	v_mov_b32_e32 v86, v180
	global_store_dwordx4 v[130:131], v[62:65], off
	global_store_dwordx4 v[130:131], v[58:61], off offset:64
	global_store_dwordx4 v[50:51], v[42:45], off offset:64
	global_store_dwordx4 v[34:35], v[26:29], off offset:64
	global_store_dwordx4 v[18:19], v[10:13], off offset:64
	global_store_dwordx4 v[18:19], v[6:9], off offset:512
	global_store_dwordx4 v[18:19], v[2:5], off offset:576
	s_cbranch_vccz .LBB0_1670
	s_waitcnt vmcnt(0)
	s_cmpk_gt_u32 s33, 0xff
	s_cbranch_scc1 .LBB0_1683
	s_barrier

; #define PG8_STAGE(bufoff, gbase, v0, v1) do { \
;         __builtin_amdgcn_global_load_lds((const unsigned*)((const char*)(gbase) + (v0)), (LAS unsigned*)(lds + (bufoff) + ldsw), 16, 0, 0); \
;         __builtin_amdgcn_global_load_lds((const unsigned*)((const char*)(gbase) + (v1)), (LAS unsigned*)(lds + (bufoff) + ldsw + 8192), 16, 0, 0); } while (0)
; #define PG8_LDA(dst, b, h) do { _Pragma("unroll") for (int m = 0; m < 4; ++m) _Pragma("unroll") for (int k = 0; k < 2; ++k) dst[m][k] = *(const LAS bf16x8*)(lds + PG8_SA(b, h) + aoff + m * 2048 + k * 1024); } while (0)
; #define PG8_LDB(dst, b, h) do { _Pragma("unroll") for (int n = 0; n < 2; ++n) _Pragma("unroll") for (int k = 0; k < 2; ++k) dst[n][k] = *(const LAS bf16x8*)(lds + PG8_SB(b, h) + boff + n * 2048 + k * 1024); } while (0)
; #define PG8_WAIT_V(n) asm volatile("s_waitcnt vmcnt(" #n ")" ::: "memory")
; #define PG8_WAIT_L(n) asm volatile("s_waitcnt lgkmcnt(" #n ")" ::: "memory")
; #define PG8_BAR __builtin_amdgcn_s_barrier()
; #define PG8_SCHED __builtin_amdgcn_sched_barrier(0)
; template <class Epi, class Sched>
; __device__ __forceinline__ void gemm_phase(LAS unsigned char* lds, const int K, const Sched& S, const Epi& E) {
;     ...
;         for (int t = 0; t < nt; t += 2) {
;             const bool last = (t == nt - 2);
;             const char* a1 = gA + (size_t)(t + 1) * kstep;
;             const char* a2 = last ? gA : gA + (size_t)(t + 2) * kstep; const char* b2 = last ? nB : cB + (size_t)(t + 2) * kstepB;
;             const char* a3 = a2 + kstep; const char* b3 = b2 + kstepB;
;             const unsigned x00 = last ? n00 : c00, x01 = last ? n01 : c01, x10 = last ? n10 : c10, x11 = last ? n11 : c11;
;             PG8_LDB(B0, 0, 0); PG8_SCHED; PG8_LDA(At, 0, 0); PG8_STAGE(PG8_SA(1, 1), a1, c10, c11);
;             PG8_WAIT_L(8); PG8_BAR; PG8_WAIT_L(0); PG8_MMA(0, 0, At, B0); PG8_BAR; PG8_SCHED;
;             PG8_LDB(B1, 0, 1); PG8_STAGE(PG8_SB(0, 0), b2, voffB0, voffB1);
;             PG8_BAR; PG8_WAIT_L(0); PG8_MMA(0, 1, At, B1); PG8_BAR;
;             PG8_LDA(At, 0, 1); PG8_STAGE(PG8_SA(0, 0), a2, x00, x01);
;             PG8_BAR; PG8_WAIT_L(0); PG8_MMA(1, 0, At, B0); PG8_BAR; PG8_SCHED;
;             PG8_STAGE(PG8_SB(0, 1), b2 + hstep, voffB0, voffB1);
;             PG8_WAIT_V(6); PG8_BAR; PG8_MMA(1, 1, At, B1); PG8_BAR;
.LBB0_1831:
	v_add_u32_e32 v139, s46, v149
	s_add_u32 s22, s0, s20
	ds_read_b128 v[160:163], v139
	ds_read_b128 v[164:167], v139 offset:1024
	ds_read_b128 v[168:171], v139 offset:2048
	ds_read_b128 v[172:175], v139 offset:3072
	s_addc_u32 s23, s1, s21
	s_add_u32 s24, s22, 0x34c30100
	s_addc_u32 s25, s23, 0
	s_cmpk_eq_i32 s20, 0xf00
	s_cselect_b64 vcc, -1, 0
	s_and_b64 s[22:23], vcc, exec
	v_cndmask_b32_e32 v134, v158, v156, vcc
	s_cselect_b32 s27, s3, s25
	s_cselect_b32 s26, s2, s24
	v_cndmask_b32_e32 v139, v138, v154, vcc
	s_cselect_b32 s23, s19, s15
	s_cselect_b32 s22, s18, s13
	v_cndmask_b32_e32 v224, v136, v155, vcc
	s_add_u32 s24, s22, 0x20000
	s_addc_u32 s25, s23, 0
	v_lshl_add_u64 v[208:209], v[144:145], 0, s[20:21]
	s_add_i32 m0, s37, 0xc000
	ds_read_b128 v[176:179], v151
	ds_read_b128 v[180:183], v151 offset:1024
	ds_read_b128 v[184:187], v151 offset:2048
	ds_read_b128 v[188:191], v151 offset:3072
	ds_read_b128 v[192:195], v151 offset:4096
	ds_read_b128 v[196:199], v151 offset:5120
	ds_read_b128 v[200:203], v151 offset:6144
	ds_read_b128 v[204:207], v151 offset:7168
	global_load_lds_dwordx4 v[208:209], off
	v_lshl_add_u64 v[208:209], v[142:143], 0, s[20:21]
	s_add_i32 m0, s37, 0xe000
	s_nop 0
	global_load_lds_dwordx4 v[208:209], off
	s_waitcnt lgkmcnt(8)
	s_barrier
	s_waitcnt lgkmcnt(0)
	s_setprio 1
	v_mfma_f32_16x16x32_bf16 v[126:129], v[160:163], v[176:179], v[126:129]
	v_mfma_f32_16x16x32_bf16 v[122:125], v[168:171], v[176:179], v[122:125]
	v_mfma_f32_16x16x32_bf16 v[110:113], v[160:163], v[184:187], v[110:113]
	v_mfma_f32_16x16x32_bf16 v[106:109], v[168:171], v[184:187], v[106:109]
	v_mfma_f32_16x16x32_bf16 v[94:97], v[160:163], v[192:195], v[94:97]
	v_mfma_f32_16x16x32_bf16 v[90:93], v[168:171], v[192:195], v[90:93]
	v_mfma_f32_16x16x32_bf16 v[78:81], v[160:163], v[200:203], v[78:81]
	v_mfma_f32_16x16x32_bf16 v[74:77], v[168:171], v[200:203], v[74:77]
	v_mfma_f32_16x16x32_bf16 v[126:129], v[164:167], v[180:183], v[126:129]
	v_mfma_f32_16x16x32_bf16 v[122:125], v[172:175], v[180:183], v[122:125]
	v_mfma_f32_16x16x32_bf16 v[110:113], v[164:167], v[188:191], v[110:113]
	v_mfma_f32_16x16x32_bf16 v[106:109], v[172:175], v[188:191], v[106:109]
	v_mfma_f32_16x16x32_bf16 v[94:97], v[164:167], v[196:199], v[94:97]
	v_mfma_f32_16x16x32_bf16 v[90:93], v[172:175], v[196:199], v[90:93]
	v_mfma_f32_16x16x32_bf16 v[78:81], v[164:167], v[204:207], v[78:81]
	v_mfma_f32_16x16x32_bf16 v[74:77], v[172:175], v[204:207], v[74:77]
	s_setprio 0
	s_barrier
	s_add_i32 s54, s46, s36
	v_add_u32_e32 v141, s48, v149
	v_lshl_add_u64 v[226:227], s[22:23], 0, v[130:131]
	s_mov_b32 m0, s54
	ds_read_b128 v[208:211], v141
	ds_read_b128 v[212:215], v141 offset:1024
	ds_read_b128 v[216:219], v141 offset:2048
	ds_read_b128 v[220:223], v141 offset:3072
	global_load_lds_dwordx4 v[226:227], off
	v_lshl_add_u64 v[228:229], s[22:23], 0, v[132:133]
	s_add_i32 m0, s54, 0x2000
	s_nop 0
	global_load_lds_dwordx4 v[228:229], off
	s_barrier
	s_waitcnt lgkmcnt(0)
	s_setprio 1
	v_mfma_f32_16x16x32_bf16 v[118:121], v[208:211], v[176:179], v[118:121]
	v_mfma_f32_16x16x32_bf16 v[114:117], v[216:219], v[176:179], v[114:117]
	v_mfma_f32_16x16x32_bf16 v[102:105], v[208:211], v[184:187], v[102:105]
	v_mfma_f32_16x16x32_bf16 v[98:101], v[216:219], v[184:187], v[98:101]
	v_mfma_f32_16x16x32_bf16 v[86:89], v[208:211], v[192:195], v[86:89]
	v_mfma_f32_16x16x32_bf16 v[82:85], v[216:219], v[192:195], v[82:85]
	v_mfma_f32_16x16x32_bf16 v[70:73], v[208:211], v[200:203], v[70:73]
	v_mfma_f32_16x16x32_bf16 v[66:69], v[216:219], v[200:203], v[66:69]
	v_mfma_f32_16x16x32_bf16 v[118:121], v[212:215], v[180:183], v[118:121]
	v_mfma_f32_16x16x32_bf16 v[114:117], v[220:223], v[180:183], v[114:117]
	v_mfma_f32_16x16x32_bf16 v[102:105], v[212:215], v[188:191], v[102:105]
	v_mfma_f32_16x16x32_bf16 v[98:101], v[220:223], v[188:191], v[98:101]
	v_mfma_f32_16x16x32_bf16 v[86:89], v[212:215], v[196:199], v[86:89]
	v_mfma_f32_16x16x32_bf16 v[82:85], v[220:223], v[196:199], v[82:85]
	v_mfma_f32_16x16x32_bf16 v[70:73], v[212:215], v[204:207], v[70:73]
	v_mfma_f32_16x16x32_bf16 v[66:69], v[220:223], v[204:207], v[66:69]
	s_setprio 0
	s_mov_b32 m0, s37
	s_barrier
	ds_read_b128 v[176:179], v151 offset:16384
	ds_read_b128 v[180:183], v151 offset:17408
	ds_read_b128 v[184:187], v151 offset:18432
	ds_read_b128 v[188:191], v151 offset:19456
	ds_read_b128 v[192:195], v151 offset:20480
	ds_read_b128 v[196:199], v151 offset:21504
	ds_read_b128 v[200:203], v151 offset:22528
	ds_read_b128 v[204:207], v151 offset:23552
	global_load_lds_dwordx4 v134, s[26:27]
	s_mov_b32 m0, s38
	v_mov_b32_e32 v225, v135
	global_load_lds_dwordx4 v224, s[26:27]
	s_barrier
	s_waitcnt lgkmcnt(0)
	v_lshl_add_u64 v[230:231], s[26:27], 0, v[134:135]
	v_lshl_add_u64 v[224:225], s[26:27], 0, v[224:225]
	s_setprio 1
	s_waitcnt lgkmcnt(0)
	v_mfma_f32_16x16x32_bf16 v[62:65], v[160:163], v[176:179], v[62:65]
	v_mfma_f32_16x16x32_bf16 v[58:61], v[168:171], v[176:179], v[58:61]
	v_mfma_f32_16x16x32_bf16 v[46:49], v[160:163], v[184:187], v[46:49]
	v_mfma_f32_16x16x32_bf16 v[42:45], v[168:171], v[184:187], v[42:45]
	v_mfma_f32_16x16x32_bf16 v[30:33], v[160:163], v[192:195], v[30:33]
	v_mfma_f32_16x16x32_bf16 v[26:29], v[168:171], v[192:195], v[26:29]
	v_mfma_f32_16x16x32_bf16 v[14:17], v[160:163], v[200:203], v[14:17]
	v_mfma_f32_16x16x32_bf16 v[10:13], v[168:171], v[200:203], v[10:13]
	v_mfma_f32_16x16x32_bf16 v[62:65], v[164:167], v[180:183], v[62:65]
	v_mfma_f32_16x16x32_bf16 v[58:61], v[172:175], v[180:183], v[58:61]
	v_mfma_f32_16x16x32_bf16 v[46:49], v[164:167], v[188:191], v[46:49]
	v_mfma_f32_16x16x32_bf16 v[42:45], v[172:175], v[188:191], v[42:45]
	v_mfma_f32_16x16x32_bf16 v[30:33], v[164:167], v[196:199], v[30:33]
	v_mfma_f32_16x16x32_bf16 v[26:29], v[172:175], v[196:199], v[26:29]
	v_mfma_f32_16x16x32_bf16 v[14:17], v[164:167], v[204:207], v[14:17]
	v_mfma_f32_16x16x32_bf16 v[10:13], v[172:175], v[204:207], v[10:13]
	s_setprio 0
	s_barrier
	s_add_i32 s54, s48, s36
	v_lshl_add_u64 v[160:161], v[226:227], 0, s[4:5]
	s_mov_b32 m0, s54
	s_nop 0
	global_load_lds_dwordx4 v[160:161], off
	v_lshl_add_u64 v[160:161], v[228:229], 0, s[4:5]
	s_add_i32 m0, s54, 0x2000
	s_nop 0
	global_load_lds_dwordx4 v[160:161], off
	s_cmp_eq_u32 s82, 0
	s_cbranch_scc1 .Lpb17_p4n
	s_waitcnt vmcnt(14)
	v_cvt_pk_bf16_f32 v244, v244, v245
	v_cvt_pk_bf16_f32 v245, v246, v247
	v_cvt_pk_bf16_f32 v246, v248, v249
	v_cvt_pk_bf16_f32 v247, v250, v251
	global_store_dwordx4 v253, v[244:247], s[78:79] nt
	s_mov_b32 s82, 0
	s_waitcnt vmcnt(7)
	s_branch .Lpb17_p4j

; #define PG8_STAGE(bufoff, gbase, v0, v1) do { \
;         __builtin_amdgcn_global_load_lds((const unsigned*)((const char*)(gbase) + (v0)), (LAS unsigned*)(lds + (bufoff) + ldsw), 16, 0, 0); \
;         __builtin_amdgcn_global_load_lds((const unsigned*)((const char*)(gbase) + (v1)), (LAS unsigned*)(lds + (bufoff) + ldsw + 8192), 16, 0, 0); } while (0)
; #define PG8_LDA(dst, b, h) do { _Pragma("unroll") for (int m = 0; m < 4; ++m) _Pragma("unroll") for (int k = 0; k < 2; ++k) dst[m][k] = *(const LAS bf16x8*)(lds + PG8_SA(b, h) + aoff + m * 2048 + k * 1024); } while (0)
; #define PG8_LDB(dst, b, h) do { _Pragma("unroll") for (int n = 0; n < 2; ++n) _Pragma("unroll") for (int k = 0; k < 2; ++k) dst[n][k] = *(const LAS bf16x8*)(lds + PG8_SB(b, h) + boff + n * 2048 + k * 1024); } while (0)
; #define PG8_MMA(ai, bj, At, Bt) do { __builtin_amdgcn_s_setprio(1); _Pragma("unroll") for (int m = 0; m < 4; ++m) _Pragma("unroll") for (int n = 0; n < 2; ++n) _Pragma("unroll") for (int k = 0; k < 2; ++k) \
;         acc[ai][bj][m][n] = __builtin_amdgcn_mfma_f32_16x16x32_bf16(Bt[n][k], At[m][k], acc[ai][bj][m][n], 0, 0, 0); __builtin_amdgcn_s_setprio(0); } while (0)
; #define PG8_WAIT_V(n) asm volatile("s_waitcnt vmcnt(" #n ")" ::: "memory")
; #define PG8_WAIT_L(n) asm volatile("s_waitcnt lgkmcnt(" #n ")" ::: "memory")
; #define PG8_BAR __builtin_amdgcn_s_barrier()
; #define PG8_SCHED __builtin_amdgcn_sched_barrier(0)
; template <class Epi, class Sched>
; __device__ __forceinline__ void gemm_phase(LAS unsigned char* lds, const int K, const Sched& S, const Epi& E) {
;     ...
;             PG8_LDB(B0, 1, 0); PG8_SCHED; PG8_LDA(At, 1, 0); PG8_STAGE(PG8_SA(0, 1), a2, x10, x11);
;             PG8_WAIT_L(8); PG8_BAR; PG8_WAIT_L(0); PG8_MMA(0, 0, At, B0); PG8_BAR; PG8_SCHED;
;             PG8_LDB(B1, 1, 1); PG8_STAGE(PG8_SB(1, 0), b3, voffB0, voffB1);
;             PG8_BAR; PG8_WAIT_L(0); PG8_MMA(0, 1, At, B1); PG8_BAR;
;             PG8_LDA(At, 1, 1); PG8_STAGE(PG8_SA(1, 0), a3, x00, x01);
;             PG8_BAR; PG8_WAIT_L(0); PG8_MMA(1, 0, At, B0); PG8_BAR; PG8_SCHED;
;             PG8_STAGE(PG8_SB(1, 1), b3 + hstep, voffB0, voffB1);
;             PG8_WAIT_V(6); PG8_BAR; PG8_MMA(1, 1, At, B1); PG8_BAR;
.Lpb17_p5n:
	s_waitcnt lgkmcnt(8)
	s_barrier
	s_waitcnt lgkmcnt(0)
	s_setprio 1
	v_mfma_f32_16x16x32_bf16 v[126:129], v[160:163], v[176:179], v[126:129]
	v_mfma_f32_16x16x32_bf16 v[122:125], v[168:171], v[176:179], v[122:125]
	v_mfma_f32_16x16x32_bf16 v[110:113], v[160:163], v[184:187], v[110:113]
	v_mfma_f32_16x16x32_bf16 v[106:109], v[168:171], v[184:187], v[106:109]
	v_mfma_f32_16x16x32_bf16 v[94:97], v[160:163], v[192:195], v[94:97]
	v_mfma_f32_16x16x32_bf16 v[90:93], v[168:171], v[192:195], v[90:93]
	v_mfma_f32_16x16x32_bf16 v[78:81], v[160:163], v[200:203], v[78:81]
	v_mfma_f32_16x16x32_bf16 v[74:77], v[168:171], v[200:203], v[74:77]
	v_mfma_f32_16x16x32_bf16 v[126:129], v[164:167], v[180:183], v[126:129]
	v_mfma_f32_16x16x32_bf16 v[122:125], v[172:175], v[180:183], v[122:125]
	v_mfma_f32_16x16x32_bf16 v[110:113], v[164:167], v[188:191], v[110:113]
	v_mfma_f32_16x16x32_bf16 v[106:109], v[172:175], v[188:191], v[106:109]
	v_mfma_f32_16x16x32_bf16 v[94:97], v[164:167], v[196:199], v[94:97]
	v_mfma_f32_16x16x32_bf16 v[90:93], v[172:175], v[196:199], v[90:93]
	v_mfma_f32_16x16x32_bf16 v[78:81], v[164:167], v[204:207], v[78:81]
	v_mfma_f32_16x16x32_bf16 v[74:77], v[172:175], v[204:207], v[74:77]
	s_setprio 0
	s_barrier
	s_add_i32 s26, 0, 0x1c000
	s_add_i32 s27, s54, s36
	v_add_u32_e32 v134, s26, v149
	v_lshl_add_u64 v[226:227], s[24:25], 0, v[130:131]
	s_mov_b32 m0, s27
	ds_read_b128 v[208:211], v134
	ds_read_b128 v[212:215], v134 offset:1024
	ds_read_b128 v[216:219], v134 offset:2048
	ds_read_b128 v[220:223], v134 offset:3072
	global_load_lds_dwordx4 v[226:227], off
	v_lshl_add_u64 v[226:227], s[24:25], 0, v[132:133]
	s_add_i32 m0, s27, 0x2000
	s_nop 0
	global_load_lds_dwordx4 v[226:227], off
	s_barrier
	s_waitcnt lgkmcnt(0)
	s_setprio 1
	v_mfma_f32_16x16x32_bf16 v[118:121], v[208:211], v[176:179], v[118:121]
	v_mfma_f32_16x16x32_bf16 v[114:117], v[216:219], v[176:179], v[114:117]
	v_mfma_f32_16x16x32_bf16 v[102:105], v[208:211], v[184:187], v[102:105]
	v_mfma_f32_16x16x32_bf16 v[98:101], v[216:219], v[184:187], v[98:101]
	v_mfma_f32_16x16x32_bf16 v[86:89], v[208:211], v[192:195], v[86:89]
	v_mfma_f32_16x16x32_bf16 v[82:85], v[216:219], v[192:195], v[82:85]
	v_mfma_f32_16x16x32_bf16 v[70:73], v[208:211], v[200:203], v[70:73]
	v_mfma_f32_16x16x32_bf16 v[66:69], v[216:219], v[200:203], v[66:69]
	v_mfma_f32_16x16x32_bf16 v[118:121], v[212:215], v[180:183], v[118:121]
	v_mfma_f32_16x16x32_bf16 v[114:117], v[220:223], v[180:183], v[114:117]
	v_mfma_f32_16x16x32_bf16 v[102:105], v[212:215], v[188:191], v[102:105]
	v_mfma_f32_16x16x32_bf16 v[98:101], v[220:223], v[188:191], v[98:101]
	v_mfma_f32_16x16x32_bf16 v[86:89], v[212:215], v[196:199], v[86:89]
	v_mfma_f32_16x16x32_bf16 v[82:85], v[220:223], v[196:199], v[82:85]
	v_mfma_f32_16x16x32_bf16 v[70:73], v[212:215], v[204:207], v[70:73]
	v_mfma_f32_16x16x32_bf16 v[66:69], v[220:223], v[204:207], v[66:69]
	s_setprio 0
	s_mov_b32 m0, s43
	v_lshl_add_u64 v[226:227], v[230:231], 0, s[10:11]
	s_barrier
	ds_read_b128 v[176:179], v151 offset:49152
	ds_read_b128 v[180:183], v151 offset:50176
	ds_read_b128 v[184:187], v151 offset:51200
	ds_read_b128 v[188:191], v151 offset:52224
	ds_read_b128 v[192:195], v151 offset:53248
	ds_read_b128 v[196:199], v151 offset:54272
	ds_read_b128 v[200:203], v151 offset:55296
	ds_read_b128 v[204:207], v151 offset:56320
	global_load_lds_dwordx4 v[226:227], off
	v_lshl_add_u64 v[224:225], v[224:225], 0, s[10:11]
	s_mov_b32 m0, s44
	s_nop 0
	global_load_lds_dwordx4 v[224:225], off
	s_barrier
	s_waitcnt lgkmcnt(0)
	s_setprio 1
	v_mfma_f32_16x16x32_bf16 v[62:65], v[160:163], v[176:179], v[62:65]
	v_mfma_f32_16x16x32_bf16 v[58:61], v[168:171], v[176:179], v[58:61]
	v_mfma_f32_16x16x32_bf16 v[46:49], v[160:163], v[184:187], v[46:49]
	v_mfma_f32_16x16x32_bf16 v[42:45], v[168:171], v[184:187], v[42:45]
	v_mfma_f32_16x16x32_bf16 v[30:33], v[160:163], v[192:195], v[30:33]
	v_mfma_f32_16x16x32_bf16 v[26:29], v[168:171], v[192:195], v[26:29]
	v_mfma_f32_16x16x32_bf16 v[14:17], v[160:163], v[200:203], v[14:17]
	v_mfma_f32_16x16x32_bf16 v[10:13], v[168:171], v[200:203], v[10:13]
	v_mfma_f32_16x16x32_bf16 v[62:65], v[164:167], v[180:183], v[62:65]
	v_mfma_f32_16x16x32_bf16 v[58:61], v[172:175], v[180:183], v[58:61]
	v_mfma_f32_16x16x32_bf16 v[46:49], v[164:167], v[188:191], v[46:49]
	v_mfma_f32_16x16x32_bf16 v[42:45], v[172:175], v[188:191], v[42:45]
	v_mfma_f32_16x16x32_bf16 v[30:33], v[164:167], v[196:199], v[30:33]
	v_mfma_f32_16x16x32_bf16 v[26:29], v[172:175], v[196:199], v[26:29]
	v_mfma_f32_16x16x32_bf16 v[14:17], v[164:167], v[204:207], v[14:17]
	v_mfma_f32_16x16x32_bf16 v[10:13], v[172:175], v[204:207], v[10:13]
	s_setprio 0
	s_barrier
	s_add_u32 s22, s22, 0x20800
	s_addc_u32 s23, s23, 0
	s_add_i32 s24, s26, s36
	v_lshl_add_u64 v[160:161], s[22:23], 0, v[130:131]
	s_mov_b32 m0, s24
	s_nop 0
	global_load_lds_dwordx4 v[160:161], off
	v_lshl_add_u64 v[160:161], s[22:23], 0, v[132:133]
	s_add_i32 m0, s24, 0x2000
	s_nop 0
	global_load_lds_dwordx4 v[160:161], off
	s_cmp_eq_u32 s82, 0
	s_cbranch_scc1 .Lpb17_p8n
	s_waitcnt vmcnt(14)
	s_branch .Lpb17_p8j

; #define PG8_STAGE(bufoff, gbase, v0, v1) do { \
;         __builtin_amdgcn_global_load_lds((const unsigned*)((const char*)(gbase) + (v0)), (LAS unsigned*)(lds + (bufoff) + ldsw), 16, 0, 0); \
;         __builtin_amdgcn_global_load_lds((const unsigned*)((const char*)(gbase) + (v1)), (LAS unsigned*)(lds + (bufoff) + ldsw + 8192), 16, 0, 0); } while (0)
; #define PG8_LDA(dst, b, h) do { _Pragma("unroll") for (int m = 0; m < 4; ++m) _Pragma("unroll") for (int k = 0; k < 2; ++k) dst[m][k] = *(const LAS bf16x8*)(lds + PG8_SA(b, h) + aoff + m * 2048 + k * 1024); } while (0)
; #define PG8_LDB(dst, b, h) do { _Pragma("unroll") for (int n = 0; n < 2; ++n) _Pragma("unroll") for (int k = 0; k < 2; ++k) dst[n][k] = *(const LAS bf16x8*)(lds + PG8_SB(b, h) + boff + n * 2048 + k * 1024); } while (0)
; #define PG8_MMA(ai, bj, At, Bt) do { __builtin_amdgcn_s_setprio(1); _Pragma("unroll") for (int m = 0; m < 4; ++m) _Pragma("unroll") for (int n = 0; n < 2; ++n) _Pragma("unroll") for (int k = 0; k < 2; ++k) \
;         acc[ai][bj][m][n] = __builtin_amdgcn_mfma_f32_16x16x32_bf16(Bt[n][k], At[m][k], acc[ai][bj][m][n], 0, 0, 0); __builtin_amdgcn_s_setprio(0); } while (0)
; #define PG8_WAIT_L(n) asm volatile("s_waitcnt lgkmcnt(" #n ")" ::: "memory")
; template <class Epi, class Sched>
; __device__ __forceinline__ void gemm_phase(LAS unsigned char* lds, const int K, const Sched& S, const Epi& E) {
;     ...
;         for (int t = 0; t < nt; t += 2) {
;             const bool last = (t == nt - 2);
;             const char* a1 = gA + (size_t)(t + 1) * kstep;
;             const char* a2 = last ? gA : gA + (size_t)(t + 2) * kstep; const char* b2 = last ? nB : cB + (size_t)(t + 2) * kstepB;
;             const char* a3 = a2 + kstep; const char* b3 = b2 + kstepB;
;             const unsigned x00 = last ? n00 : c00, x01 = last ? n01 : c01, x10 = last ? n10 : c10, x11 = last ? n11 : c11;
;             PG8_LDB(B0, 0, 0); PG8_SCHED; PG8_LDA(At, 0, 0); PG8_STAGE(PG8_SA(1, 1), a1, c10, c11);
;             PG8_WAIT_L(8); PG8_BAR; PG8_WAIT_L(0); PG8_MMA(0, 0, At, B0); PG8_BAR; PG8_SCHED;
;             PG8_LDB(B1, 0, 1); PG8_STAGE(PG8_SB(0, 0), b2, voffB0, voffB1);
;             PG8_BAR; PG8_WAIT_L(0); PG8_MMA(0, 1, At, B1); PG8_BAR;
;             PG8_LDA(At, 0, 1); PG8_STAGE(PG8_SA(0, 0), a2, x00, x01);
;             PG8_BAR; PG8_WAIT_L(0); PG8_MMA(1, 0, At, B0); PG8_BAR; PG8_SCHED;
.LBB0_1898:
	s_add_u32 s40, s0, s38
	ds_read_b128 v[164:167], v153
	ds_read_b128 v[168:171], v153 offset:1024
	ds_read_b128 v[172:175], v153 offset:2048
	ds_read_b128 v[176:179], v153 offset:3072
	s_addc_u32 s41, s1, s39
	s_add_u32 s42, s40, 0x3ee90100
	s_addc_u32 s43, s41, 0
	s_cmpk_eq_i32 s38, 0x300
	s_cselect_b64 vcc, -1, 0
	s_and_b64 s[40:41], vcc, exec
	v_cndmask_b32_e32 v134, v162, v157, vcc
	s_cselect_b32 s45, s3, s43
	s_cselect_b32 s44, s2, s42
	v_cndmask_b32_e32 v139, v138, v159, vcc
	s_cselect_b32 s41, s37, s31
	s_cselect_b32 s40, s36, s29
	v_cndmask_b32_e32 v228, v136, v158, vcc
	s_add_u32 s42, s40, 0x40000
	s_addc_u32 s43, s41, 0
	v_lshl_add_u64 v[212:213], v[144:145], 0, s[38:39]
	s_add_i32 m0, s49, 0xc000
	ds_read_b128 v[180:183], v154
	ds_read_b128 v[184:187], v154 offset:1024
	ds_read_b128 v[188:191], v154 offset:2048
	ds_read_b128 v[192:195], v154 offset:3072
	ds_read_b128 v[196:199], v154 offset:4096
	ds_read_b128 v[200:203], v154 offset:5120
	ds_read_b128 v[204:207], v154 offset:6144
	ds_read_b128 v[208:211], v154 offset:7168
	global_load_lds_dwordx4 v[212:213], off
	v_lshl_add_u64 v[212:213], v[142:143], 0, s[38:39]
	s_add_i32 m0, s49, 0xe000
	s_nop 0
	global_load_lds_dwordx4 v[212:213], off
	s_waitcnt lgkmcnt(8)
	s_barrier
	s_waitcnt lgkmcnt(0)
	s_setprio 1
	v_mfma_f32_16x16x32_bf16 v[126:129], v[164:167], v[180:183], v[126:129]
	v_mfma_f32_16x16x32_bf16 v[122:125], v[172:175], v[180:183], v[122:125]
	v_mfma_f32_16x16x32_bf16 v[114:117], v[164:167], v[188:191], v[114:117]
	v_mfma_f32_16x16x32_bf16 v[106:109], v[172:175], v[188:191], v[106:109]
	v_mfma_f32_16x16x32_bf16 v[98:101], v[164:167], v[196:199], v[98:101]
	v_mfma_f32_16x16x32_bf16 v[90:93], v[172:175], v[196:199], v[90:93]
	v_mfma_f32_16x16x32_bf16 v[82:85], v[164:167], v[204:207], v[82:85]
	v_mfma_f32_16x16x32_bf16 v[74:77], v[172:175], v[204:207], v[74:77]
	v_mfma_f32_16x16x32_bf16 v[126:129], v[168:171], v[184:187], v[126:129]
	v_mfma_f32_16x16x32_bf16 v[122:125], v[176:179], v[184:187], v[122:125]
	v_mfma_f32_16x16x32_bf16 v[114:117], v[168:171], v[192:195], v[114:117]
	v_mfma_f32_16x16x32_bf16 v[106:109], v[176:179], v[192:195], v[106:109]
	v_mfma_f32_16x16x32_bf16 v[98:101], v[168:171], v[200:203], v[98:101]
	v_mfma_f32_16x16x32_bf16 v[90:93], v[176:179], v[200:203], v[90:93]
	v_mfma_f32_16x16x32_bf16 v[82:85], v[168:171], v[208:211], v[82:85]
	v_mfma_f32_16x16x32_bf16 v[74:77], v[176:179], v[208:211], v[74:77]
	s_setprio 0
	s_barrier
	s_add_i32 s66, s59, s48
	v_lshl_add_u64 v[230:231], s[40:41], 0, v[132:133]
	s_mov_b32 m0, s66
	ds_read_b128 v[212:215], v155
	ds_read_b128 v[216:219], v155 offset:1024
	ds_read_b128 v[220:223], v155 offset:2048
	ds_read_b128 v[224:227], v155 offset:3072
	global_load_lds_dwordx4 v[230:231], off
	v_lshl_add_u64 v[232:233], s[40:41], 0, v[130:131]
	s_add_i32 m0, s66, 0x2000
	s_nop 0
	global_load_lds_dwordx4 v[232:233], off
	s_barrier
	s_waitcnt lgkmcnt(0)
	s_setprio 1
	v_mfma_f32_16x16x32_bf16 v[118:121], v[212:215], v[180:183], v[118:121]
	v_mfma_f32_16x16x32_bf16 v[110:113], v[220:223], v[180:183], v[110:113]
	v_mfma_f32_16x16x32_bf16 v[102:105], v[212:215], v[188:191], v[102:105]
	v_mfma_f32_16x16x32_bf16 v[94:97], v[220:223], v[188:191], v[94:97]
	v_mfma_f32_16x16x32_bf16 v[86:89], v[212:215], v[196:199], v[86:89]
	v_mfma_f32_16x16x32_bf16 v[78:81], v[220:223], v[196:199], v[78:81]
	v_mfma_f32_16x16x32_bf16 v[70:73], v[212:215], v[204:207], v[70:73]
	v_mfma_f32_16x16x32_bf16 v[66:69], v[220:223], v[204:207], v[66:69]
	v_mfma_f32_16x16x32_bf16 v[118:121], v[216:219], v[184:187], v[118:121]
	v_mfma_f32_16x16x32_bf16 v[110:113], v[224:227], v[184:187], v[110:113]
	v_mfma_f32_16x16x32_bf16 v[102:105], v[216:219], v[192:195], v[102:105]
	v_mfma_f32_16x16x32_bf16 v[94:97], v[224:227], v[192:195], v[94:97]
	v_mfma_f32_16x16x32_bf16 v[86:89], v[216:219], v[200:203], v[86:89]
	v_mfma_f32_16x16x32_bf16 v[78:81], v[224:227], v[200:203], v[78:81]
	v_mfma_f32_16x16x32_bf16 v[70:73], v[216:219], v[208:211], v[70:73]
	v_mfma_f32_16x16x32_bf16 v[66:69], v[224:227], v[208:211], v[66:69]
	s_setprio 0
	s_mov_b32 m0, s49
	s_barrier
	ds_read_b128 v[180:183], v154 offset:16384
	ds_read_b128 v[184:187], v154 offset:17408
	ds_read_b128 v[188:191], v154 offset:18432
	ds_read_b128 v[192:195], v154 offset:19456
	ds_read_b128 v[196:199], v154 offset:20480
	ds_read_b128 v[200:203], v154 offset:21504
	ds_read_b128 v[204:207], v154 offset:22528
	ds_read_b128 v[208:211], v154 offset:23552
	global_load_lds_dwordx4 v134, s[44:45]
	s_mov_b32 m0, s50
	v_mov_b32_e32 v229, v135
	global_load_lds_dwordx4 v228, s[44:45]
	s_barrier
	s_waitcnt lgkmcnt(0)
	v_lshl_add_u64 v[234:235], s[44:45], 0, v[134:135]
	v_lshl_add_u64 v[228:229], s[44:45], 0, v[228:229]
	s_setprio 1
	s_waitcnt lgkmcnt(0)
	v_mfma_f32_16x16x32_bf16 v[62:65], v[164:167], v[180:183], v[62:65]
	v_mfma_f32_16x16x32_bf16 v[58:61], v[172:175], v[180:183], v[58:61]
	v_mfma_f32_16x16x32_bf16 v[46:49], v[164:167], v[188:191], v[46:49]
	v_mfma_f32_16x16x32_bf16 v[42:45], v[172:175], v[188:191], v[42:45]
	v_mfma_f32_16x16x32_bf16 v[30:33], v[164:167], v[196:199], v[30:33]
	v_mfma_f32_16x16x32_bf16 v[26:29], v[172:175], v[196:199], v[26:29]
	v_mfma_f32_16x16x32_bf16 v[14:17], v[164:167], v[204:207], v[14:17]
	v_mfma_f32_16x16x32_bf16 v[10:13], v[172:175], v[204:207], v[10:13]
	v_mfma_f32_16x16x32_bf16 v[62:65], v[168:171], v[184:187], v[62:65]
	v_mfma_f32_16x16x32_bf16 v[58:61], v[176:179], v[184:187], v[58:61]
	v_mfma_f32_16x16x32_bf16 v[46:49], v[168:171], v[192:195], v[46:49]
	v_mfma_f32_16x16x32_bf16 v[42:45], v[176:179], v[192:195], v[42:45]
	v_mfma_f32_16x16x32_bf16 v[30:33], v[168:171], v[200:203], v[30:33]
	v_mfma_f32_16x16x32_bf16 v[26:29], v[176:179], v[200:203], v[26:29]
	v_mfma_f32_16x16x32_bf16 v[14:17], v[168:171], v[208:211], v[14:17]
	v_mfma_f32_16x16x32_bf16 v[10:13], v[176:179], v[208:211], v[10:13]
	s_setprio 0
	s_barrier
; #define PG8_STAGE(bufoff, gbase, v0, v1) do { \
;         __builtin_amdgcn_global_load_lds((const unsigned*)((const char*)(gbase) + (v0)), (LAS unsigned*)(lds + (bufoff) + ldsw), 16, 0, 0); \
;         __builtin_amdgcn_global_load_lds((const unsigned*)((const char*)(gbase) + (v1)), (LAS unsigned*)(lds + (bufoff) + ldsw + 8192), 16, 0, 0); } while (0)
; #define PG8_LDA(dst, b, h) do { _Pragma("unroll") for (int m = 0; m < 4; ++m) _Pragma("unroll") for (int k = 0; k < 2; ++k) dst[m][k] = *(const LAS bf16x8*)(lds + PG8_SA(b, h) + aoff + m * 2048 + k * 1024); } while (0)
; #define PG8_LDB(dst, b, h) do { _Pragma("unroll") for (int n = 0; n < 2; ++n) _Pragma("unroll") for (int k = 0; k < 2; ++k) dst[n][k] = *(const LAS bf16x8*)(lds + PG8_SB(b, h) + boff + n * 2048 + k * 1024); } while (0)
; #define PG8_MMA(ai, bj, At, Bt) do { __builtin_amdgcn_s_setprio(1); _Pragma("unroll") for (int m = 0; m < 4; ++m) _Pragma("unroll") for (int n = 0; n < 2; ++n) _Pragma("unroll") for (int k = 0; k < 2; ++k) \
;         acc[ai][bj][m][n] = __builtin_amdgcn_mfma_f32_16x16x32_bf16(Bt[n][k], At[m][k], acc[ai][bj][m][n], 0, 0, 0); __builtin_amdgcn_s_setprio(0); } while (0)
; #define PG8_WAIT_V(n) asm volatile("s_waitcnt vmcnt(" #n ")" ::: "memory")
; #define PG8_WAIT_L(n) asm volatile("s_waitcnt lgkmcnt(" #n ")" ::: "memory")
; #define PG8_BAR __builtin_amdgcn_s_barrier()
; #define PG8_SCHED __builtin_amdgcn_sched_barrier(0)
; template <class Epi, class Sched>
; __device__ __forceinline__ void gemm_phase(LAS unsigned char* lds, const int K, const Sched& S, const Epi& E) {
;     ...
;             PG8_STAGE(PG8_SB(0, 1), b2 + hstep, voffB0, voffB1);
;             PG8_WAIT_V(6); PG8_BAR; PG8_MMA(1, 1, At, B1); PG8_BAR;
;             PG8_LDB(B0, 1, 0); PG8_SCHED; PG8_LDA(At, 1, 0); PG8_STAGE(PG8_SA(0, 1), a2, x10, x11);
;             PG8_WAIT_L(8); PG8_BAR; PG8_WAIT_L(0); PG8_MMA(0, 0, At, B0); PG8_BAR; PG8_SCHED;
;             PG8_LDB(B1, 1, 1); PG8_STAGE(PG8_SB(1, 0), b3, voffB0, voffB1);
;             PG8_BAR; PG8_WAIT_L(0); PG8_MMA(0, 1, At, B1); PG8_BAR;
;             PG8_LDA(At, 1, 1); PG8_STAGE(PG8_SA(1, 0), a3, x00, x01);
	s_add_i32 s66, s60, s48
	v_lshl_add_u64 v[164:165], v[230:231], 0, s[4:5]
	s_mov_b32 m0, s66
	s_nop 0
	global_load_lds_dwordx4 v[164:165], off
	v_lshl_add_u64 v[164:165], v[232:233], 0, s[4:5]
	s_add_i32 m0, s66, 0x2000
	s_nop 0
	global_load_lds_dwordx4 v[164:165], off
	s_waitcnt vmcnt(6)
	s_barrier
	s_setprio 1
	v_mfma_f32_16x16x32_bf16 v[54:57], v[212:215], v[180:183], v[54:57]
	v_mfma_f32_16x16x32_bf16 v[50:53], v[220:223], v[180:183], v[50:53]
	v_mfma_f32_16x16x32_bf16 v[38:41], v[212:215], v[188:191], v[38:41]
	v_mfma_f32_16x16x32_bf16 v[34:37], v[220:223], v[188:191], v[34:37]
	v_mfma_f32_16x16x32_bf16 v[22:25], v[212:215], v[196:199], v[22:25]
	v_mfma_f32_16x16x32_bf16 v[18:21], v[220:223], v[196:199], v[18:21]
	v_mfma_f32_16x16x32_bf16 v[6:9], v[212:215], v[204:207], v[6:9]
	v_mfma_f32_16x16x32_bf16 v[2:5], v[220:223], v[204:207], v[2:5]
	v_mfma_f32_16x16x32_bf16 v[54:57], v[216:219], v[184:187], v[54:57]
	v_mfma_f32_16x16x32_bf16 v[50:53], v[224:227], v[184:187], v[50:53]
	v_mfma_f32_16x16x32_bf16 v[38:41], v[216:219], v[192:195], v[38:41]
	v_mfma_f32_16x16x32_bf16 v[34:37], v[224:227], v[192:195], v[34:37]
	v_mfma_f32_16x16x32_bf16 v[22:25], v[216:219], v[200:203], v[22:25]
	v_mfma_f32_16x16x32_bf16 v[18:21], v[224:227], v[200:203], v[18:21]
	v_mfma_f32_16x16x32_bf16 v[6:9], v[216:219], v[208:211], v[6:9]
	v_mfma_f32_16x16x32_bf16 v[2:5], v[224:227], v[208:211], v[2:5]
	s_setprio 0
	s_add_i32 s66, 0, 0x18000
	v_add_u32_e32 v134, s66, v151
	s_barrier
	ds_read_b128 v[164:167], v134
	ds_read_b128 v[168:171], v134 offset:1024
	ds_read_b128 v[172:175], v134 offset:2048
	ds_read_b128 v[176:179], v134 offset:3072
	s_mov_b32 m0, s51
	ds_read_b128 v[180:183], v154 offset:32768
	ds_read_b128 v[184:187], v154 offset:33792
	ds_read_b128 v[188:191], v154 offset:34816
	ds_read_b128 v[192:195], v154 offset:35840
	ds_read_b128 v[196:199], v154 offset:36864
	ds_read_b128 v[200:203], v154 offset:37888
	ds_read_b128 v[204:207], v154 offset:38912
	ds_read_b128 v[208:211], v154 offset:39936
	v_cndmask_b32_e32 v134, v140, v160, vcc
	global_load_lds_dwordx4 v139, s[44:45]
	s_mov_b32 m0, s52
	s_nop 0
	global_load_lds_dwordx4 v134, s[44:45]
	s_waitcnt lgkmcnt(8)
	s_barrier
	s_waitcnt lgkmcnt(0)
	s_setprio 1
	v_mfma_f32_16x16x32_bf16 v[126:129], v[164:167], v[180:183], v[126:129]
	v_mfma_f32_16x16x32_bf16 v[122:125], v[172:175], v[180:183], v[122:125]
	v_mfma_f32_16x16x32_bf16 v[114:117], v[164:167], v[188:191], v[114:117]
	v_mfma_f32_16x16x32_bf16 v[106:109], v[172:175], v[188:191], v[106:109]
	v_mfma_f32_16x16x32_bf16 v[98:101], v[164:167], v[196:199], v[98:101]
	v_mfma_f32_16x16x32_bf16 v[90:93], v[172:175], v[196:199], v[90:93]
	v_mfma_f32_16x16x32_bf16 v[82:85], v[164:167], v[204:207], v[82:85]
	v_mfma_f32_16x16x32_bf16 v[74:77], v[172:175], v[204:207], v[74:77]
	v_mfma_f32_16x16x32_bf16 v[126:129], v[168:171], v[184:187], v[126:129]
	v_mfma_f32_16x16x32_bf16 v[122:125], v[176:179], v[184:187], v[122:125]
	v_mfma_f32_16x16x32_bf16 v[114:117], v[168:171], v[192:195], v[114:117]
	v_mfma_f32_16x16x32_bf16 v[106:109], v[176:179], v[192:195], v[106:109]
	v_mfma_f32_16x16x32_bf16 v[98:101], v[168:171], v[200:203], v[98:101]
	v_mfma_f32_16x16x32_bf16 v[90:93], v[176:179], v[200:203], v[90:93]
	v_mfma_f32_16x16x32_bf16 v[82:85], v[168:171], v[208:211], v[82:85]
	v_mfma_f32_16x16x32_bf16 v[74:77], v[176:179], v[208:211], v[74:77]
	s_setprio 0
	s_barrier
	s_add_i32 s44, 0, 0x1c000
	s_add_i32 s45, s66, s48
	v_add_u32_e32 v134, s44, v151
	v_lshl_add_u64 v[230:231], s[42:43], 0, v[132:133]
	s_mov_b32 m0, s45
	ds_read_b128 v[212:215], v134
	ds_read_b128 v[216:219], v134 offset:1024
	ds_read_b128 v[220:223], v134 offset:2048
	ds_read_b128 v[224:227], v134 offset:3072
	global_load_lds_dwordx4 v[230:231], off
	v_lshl_add_u64 v[230:231], s[42:43], 0, v[130:131]
	s_add_i32 m0, s45, 0x2000
	s_nop 0
	global_load_lds_dwordx4 v[230:231], off
	s_barrier
	s_waitcnt lgkmcnt(0)
	s_setprio 1
	v_mfma_f32_16x16x32_bf16 v[118:121], v[212:215], v[180:183], v[118:121]
	v_mfma_f32_16x16x32_bf16 v[110:113], v[220:223], v[180:183], v[110:113]
	v_mfma_f32_16x16x32_bf16 v[102:105], v[212:215], v[188:191], v[102:105]
	v_mfma_f32_16x16x32_bf16 v[94:97], v[220:223], v[188:191], v[94:97]
	v_mfma_f32_16x16x32_bf16 v[86:89], v[212:215], v[196:199], v[86:89]
	v_mfma_f32_16x16x32_bf16 v[78:81], v[220:223], v[196:199], v[78:81]
	v_mfma_f32_16x16x32_bf16 v[70:73], v[212:215], v[204:207], v[70:73]
	v_mfma_f32_16x16x32_bf16 v[66:69], v[220:223], v[204:207], v[66:69]
	v_mfma_f32_16x16x32_bf16 v[118:121], v[216:219], v[184:187], v[118:121]
	v_mfma_f32_16x16x32_bf16 v[110:113], v[224:227], v[184:187], v[110:113]
	v_mfma_f32_16x16x32_bf16 v[102:105], v[216:219], v[192:195], v[102:105]
	v_mfma_f32_16x16x32_bf16 v[94:97], v[224:227], v[192:195], v[94:97]
	v_mfma_f32_16x16x32_bf16 v[86:89], v[216:219], v[200:203], v[86:89]
	v_mfma_f32_16x16x32_bf16 v[78:81], v[224:227], v[200:203], v[78:81]
	v_mfma_f32_16x16x32_bf16 v[70:73], v[216:219], v[208:211], v[70:73]
	v_mfma_f32_16x16x32_bf16 v[66:69], v[224:227], v[208:211], v[66:69]
	s_setprio 0
	s_mov_b32 m0, s55
	v_lshl_add_u64 v[230:231], v[234:235], 0, s[12:13]
	s_barrier
	ds_read_b128 v[180:183], v154 offset:49152
	ds_read_b128 v[184:187], v154 offset:50176
	ds_read_b128 v[188:191], v154 offset:51200
	ds_read_b128 v[192:195], v154 offset:52224
	ds_read_b128 v[196:199], v154 offset:53248
	ds_read_b128 v[200:203], v154 offset:54272
	ds_read_b128 v[204:207], v154 offset:55296
	ds_read_b128 v[208:211], v154 offset:56320
	global_load_lds_dwordx4 v[230:231], off
	v_lshl_add_u64 v[228:229], v[228:229], 0, s[12:13]
	s_mov_b32 m0, s56
	s_nop 0
	global_load_lds_dwordx4 v[228:229], off
	s_barrier
; #define PG8_STAGE(bufoff, gbase, v0, v1) do { \
;         __builtin_amdgcn_global_load_lds((const unsigned*)((const char*)(gbase) + (v0)), (LAS unsigned*)(lds + (bufoff) + ldsw), 16, 0, 0); \
;         __builtin_amdgcn_global_load_lds((const unsigned*)((const char*)(gbase) + (v1)), (LAS unsigned*)(lds + (bufoff) + ldsw + 8192), 16, 0, 0); } while (0)
; #define PG8_MMA(ai, bj, At, Bt) do { __builtin_amdgcn_s_setprio(1); _Pragma("unroll") for (int m = 0; m < 4; ++m) _Pragma("unroll") for (int n = 0; n < 2; ++n) _Pragma("unroll") for (int k = 0; k < 2; ++k) \
;         acc[ai][bj][m][n] = __builtin_amdgcn_mfma_f32_16x16x32_bf16(Bt[n][k], At[m][k], acc[ai][bj][m][n], 0, 0, 0); __builtin_amdgcn_s_setprio(0); } while (0)
; #define PG8_WAIT_V(n) asm volatile("s_waitcnt vmcnt(" #n ")" ::: "memory")
; #define PG8_WAIT_L(n) asm volatile("s_waitcnt lgkmcnt(" #n ")" ::: "memory")
; #define PG8_BAR __builtin_amdgcn_s_barrier()
; #define PG8_SCHED __builtin_amdgcn_sched_barrier(0)
; __device__ __forceinline__ unsigned pk4_fp8(float a, float b, float c, float d) { int w = 0; w = __builtin_amdgcn_cvt_pk_fp8_f32(a, b, w, false); w = __builtin_amdgcn_cvt_pk_fp8_f32(c, d, w, true); return (unsigned)w; }
; template <class Epi, class Sched>
; __device__ __forceinline__ void gemm_phase(LAS unsigned char* lds, const int K, const Sched& S, const Epi& E) {
;     ...
;             PG8_BAR; PG8_WAIT_L(0); PG8_MMA(1, 0, At, B0); PG8_BAR; PG8_SCHED;
;             PG8_STAGE(PG8_SB(1, 1), b3 + hstep, voffB0, voffB1);
;             PG8_WAIT_V(6); PG8_BAR; PG8_MMA(1, 1, At, B1); PG8_BAR;
;     __device__ __forceinline__ void operator()(const f32x4 (&acc)[2][2][4][2], const Unit& u, int wr, int wc, int fr, int fq) const {
;         const int row0 = u.rbase + wr * 64 + fr, col0 = u.pn * BM + wc * 32 + 8 * fq;
; #pragma unroll
;         for (int ai = 0; ai < 2; ++ai)
; #pragma unroll
;             for (int m = 0; m < 4; ++m) { unsigned char* rowp = O + (size_t)(row0 + ai * HALF + m * 16) * ldc + col0;
; #pragma unroll
;                 for (int bj = 0; bj < 2; ++bj) { const f32x4 v0 = acc[ai][bj][m][0] * scale, v1 = acc[ai][bj][m][1] * scale;
;                     u32x2 w; w.x = pk4_fp8(v0[0], v0[1], v0[2], v0[3]); w.y = pk4_fp8(v1[0], v1[1], v1[2], v1[3]);
;                     *(u32x2*)(rowp + bj * HALF) = w; } }
;     }
	s_waitcnt lgkmcnt(0)
	s_setprio 1
	v_mfma_f32_16x16x32_bf16 v[62:65], v[164:167], v[180:183], v[62:65]
	v_mfma_f32_16x16x32_bf16 v[58:61], v[172:175], v[180:183], v[58:61]
	v_mfma_f32_16x16x32_bf16 v[46:49], v[164:167], v[188:191], v[46:49]
	v_mfma_f32_16x16x32_bf16 v[42:45], v[172:175], v[188:191], v[42:45]
	v_mfma_f32_16x16x32_bf16 v[30:33], v[164:167], v[196:199], v[30:33]
	v_mfma_f32_16x16x32_bf16 v[26:29], v[172:175], v[196:199], v[26:29]
	v_mfma_f32_16x16x32_bf16 v[14:17], v[164:167], v[204:207], v[14:17]
	v_mfma_f32_16x16x32_bf16 v[10:13], v[172:175], v[204:207], v[10:13]
	v_mfma_f32_16x16x32_bf16 v[62:65], v[168:171], v[184:187], v[62:65]
	v_mfma_f32_16x16x32_bf16 v[58:61], v[176:179], v[184:187], v[58:61]
	v_mfma_f32_16x16x32_bf16 v[46:49], v[168:171], v[192:195], v[46:49]
	v_mfma_f32_16x16x32_bf16 v[42:45], v[176:179], v[192:195], v[42:45]
	v_mfma_f32_16x16x32_bf16 v[30:33], v[168:171], v[200:203], v[30:33]
	v_mfma_f32_16x16x32_bf16 v[26:29], v[176:179], v[200:203], v[26:29]
	v_mfma_f32_16x16x32_bf16 v[14:17], v[168:171], v[208:211], v[14:17]
	v_mfma_f32_16x16x32_bf16 v[10:13], v[176:179], v[208:211], v[10:13]
	s_setprio 0
	s_barrier
	s_add_u32 s40, s40, 0x40800
	s_addc_u32 s41, s41, 0
	s_add_i32 s42, s44, s48
	v_lshl_add_u64 v[164:165], s[40:41], 0, v[132:133]
	s_mov_b32 m0, s42
	s_nop 0
	global_load_lds_dwordx4 v[164:165], off
	v_lshl_add_u64 v[164:165], s[40:41], 0, v[130:131]
	s_add_i32 m0, s42, 0x2000
	s_nop 0
	global_load_lds_dwordx4 v[164:165], off
	s_waitcnt vmcnt(6)
	s_barrier
	s_setprio 1
	v_mfma_f32_16x16x32_bf16 v[54:57], v[212:215], v[180:183], v[54:57]
	v_mfma_f32_16x16x32_bf16 v[50:53], v[220:223], v[180:183], v[50:53]
	v_mfma_f32_16x16x32_bf16 v[38:41], v[212:215], v[188:191], v[38:41]
	v_mfma_f32_16x16x32_bf16 v[34:37], v[220:223], v[188:191], v[34:37]
	v_mfma_f32_16x16x32_bf16 v[22:25], v[212:215], v[196:199], v[22:25]
	v_mfma_f32_16x16x32_bf16 v[18:21], v[220:223], v[196:199], v[18:21]
	v_mfma_f32_16x16x32_bf16 v[6:9], v[212:215], v[204:207], v[6:9]
	v_mfma_f32_16x16x32_bf16 v[2:5], v[220:223], v[204:207], v[2:5]
	v_mfma_f32_16x16x32_bf16 v[54:57], v[216:219], v[184:187], v[54:57]
	v_mfma_f32_16x16x32_bf16 v[50:53], v[224:227], v[184:187], v[50:53]
	v_mfma_f32_16x16x32_bf16 v[38:41], v[216:219], v[192:195], v[38:41]
	v_mfma_f32_16x16x32_bf16 v[34:37], v[224:227], v[192:195], v[34:37]
	v_mfma_f32_16x16x32_bf16 v[22:25], v[216:219], v[200:203], v[22:25]
	v_mfma_f32_16x16x32_bf16 v[18:21], v[224:227], v[200:203], v[18:21]
	v_mfma_f32_16x16x32_bf16 v[6:9], v[216:219], v[208:211], v[6:9]
	v_mfma_f32_16x16x32_bf16 v[2:5], v[224:227], v[208:211], v[2:5]
	s_setprio 0
	s_add_i32 s65, s65, 2
	s_add_u32 s29, s29, 0x80000
	s_addc_u32 s31, s31, 0
	s_add_u32 s38, s38, 0x100
	s_addc_u32 s39, s39, 0
	s_cmp_gt_u32 s65, 5
	s_barrier
	s_cbranch_scc0 .LBB0_1898
	v_pk_mul_f32 v[126:127], v[126:127], s[14:15] op_sel_hi:[1,0]
	v_mov_b32_e32 v142, v135
	v_cvt_pk_fp8_f32 v142, v126, v127
	v_pk_mul_f32 v[122:123], v[122:123], s[14:15] op_sel_hi:[1,0]
	v_mov_b32_e32 v143, v135
	v_cvt_pk_fp8_f32 v143, v122, v123
	v_pk_mul_f32 v[122:123], v[128:129], s[14:15] op_sel_hi:[1,0]
	v_pk_mul_f32 v[118:119], v[118:119], s[14:15] op_sel_hi:[1,0]
	v_cvt_pk_fp8_f32 v142, v122, v123 op_sel:[0,0,1]
	v_mov_b32_e32 v122, v135
	v_cvt_pk_fp8_f32 v122, v118, v119
	v_pk_mul_f32 v[114:115], v[114:115], s[14:15] op_sel_hi:[1,0]
	v_mov_b32_e32 v118, v135
	v_cvt_pk_fp8_f32 v118, v114, v115
	v_pk_mul_f32 v[106:107], v[106:107], s[14:15] op_sel_hi:[1,0]
	v_mov_b32_e32 v119, v135
	v_cvt_pk_fp8_f32 v119, v106, v107
	v_pk_mul_f32 v[106:107], v[116:117], s[14:15] op_sel_hi:[1,0]
	v_pk_mul_f32 v[94:95], v[94:95], s[14:15] op_sel_hi:[1,0]
	v_cvt_pk_fp8_f32 v118, v106, v107 op_sel:[0,0,1]
	v_mov_b32_e32 v107, v135
	v_cvt_pk_fp8_f32 v107, v94, v95
	v_pk_mul_f32 v[96:97], v[96:97], s[14:15] op_sel_hi:[1,0]
	v_pk_mul_f32 v[90:91], v[90:91], s[14:15] op_sel_hi:[1,0]
	v_pk_mul_f32 v[78:79], v[78:79], s[14:15] op_sel_hi:[1,0]
	v_cvt_pk_fp8_f32 v107, v96, v97 op_sel:[0,0,1]
	v_pk_mul_f32 v[96:97], v[98:99], s[14:15] op_sel_hi:[1,0]
	v_mov_b32_e32 v98, v135
	v_cvt_pk_fp8_f32 v98, v96, v97
	v_mov_b32_e32 v99, v135
	v_cvt_pk_fp8_f32 v99, v90, v91
	v_pk_mul_f32 v[90:91], v[100:101], s[14:15] op_sel_hi:[1,0]
	v_pk_mul_f32 v[80:81], v[80:81], s[14:15] op_sel_hi:[1,0]
	v_cvt_pk_fp8_f32 v98, v90, v91 op_sel:[0,0,1]
	v_mov_b32_e32 v91, v135
	v_cvt_pk_fp8_f32 v91, v78, v79
	v_pk_mul_f32 v[74:75], v[74:75], s[14:15] op_sel_hi:[1,0]
	v_pk_mul_f32 v[66:67], v[66:67], s[14:15] op_sel_hi:[1,0]
	v_pk_mul_f32 v[68:69], v[68:69], s[14:15] op_sel_hi:[1,0]
	v_cvt_pk_fp8_f32 v91, v80, v81 op_sel:[0,0,1]
	v_pk_mul_f32 v[80:81], v[82:83], s[14:15] op_sel_hi:[1,0]
	v_mov_b32_e32 v82, v135
	v_cvt_pk_fp8_f32 v82, v80, v81
	v_mov_b32_e32 v83, v135
	v_cvt_pk_fp8_f32 v83, v74, v75
	v_pk_mul_f32 v[74:75], v[84:85], s[14:15] op_sel_hi:[1,0]
	v_pk_mul_f32 v[62:63], v[62:63], s[14:15] op_sel_hi:[1,0]
	v_cvt_pk_fp8_f32 v82, v74, v75 op_sel:[0,0,1]
	v_mov_b32_e32 v75, v135
	v_cvt_pk_fp8_f32 v75, v66, v67
	v_pk_mul_f32 v[58:59], v[58:59], s[14:15] op_sel_hi:[1,0]
	v_pk_mul_f32 v[50:51], v[50:51], s[14:15] op_sel_hi:[1,0]
	v_pk_mul_f32 v[52:53], v[52:53], s[14:15] op_sel_hi:[1,0]
	v_cvt_pk_fp8_f32 v75, v68, v69 op_sel:[0,0,1]
	v_mov_b32_e32 v68, v135
	v_cvt_pk_fp8_f32 v68, v62, v63
	v_mov_b32_e32 v69, v135
	v_cvt_pk_fp8_f32 v69, v58, v59
	v_pk_mul_f32 v[58:59], v[64:65], s[14:15] op_sel_hi:[1,0]
	v_pk_mul_f32 v[46:47], v[46:47], s[14:15] op_sel_hi:[1,0]
	v_cvt_pk_fp8_f32 v68, v58, v59 op_sel:[0,0,1]
	v_mov_b32_e32 v59, v135
	v_cvt_pk_fp8_f32 v59, v50, v51
	v_pk_mul_f32 v[42:43], v[42:43], s[14:15] op_sel_hi:[1,0]
; #define PG8_WAIT_V(n) asm volatile("s_waitcnt vmcnt(" #n ")" ::: "memory")
; #define PG8_BAR __builtin_amdgcn_s_barrier()
; __device__ __forceinline__ unsigned pk4_fp8(float a, float b, float c, float d) { int w = 0; w = __builtin_amdgcn_cvt_pk_fp8_f32(a, b, w, false); w = __builtin_amdgcn_cvt_pk_fp8_f32(c, d, w, true); return (unsigned)w; }
; template <class Epi, class Sched>
; __device__ __forceinline__ void gemm_phase(LAS unsigned char* lds, const int K, const Sched& S, const Epi& E) {
;     ...
;     PG8_WAIT_V(0);
;     if (wr == 0) PG8_BAR;
;     PG8_BAR;
;     __device__ __forceinline__ void operator()(const f32x4 (&acc)[2][2][4][2], const Unit& u, int wr, int wc, int fr, int fq) const {
;     ...
;             for (int m = 0; m < 4; ++m) { unsigned char* rowp = O + (size_t)(row0 + ai * HALF + m * 16) * ldc + col0;
; #pragma unroll
;                 for (int bj = 0; bj < 2; ++bj) { const f32x4 v0 = acc[ai][bj][m][0] * scale, v1 = acc[ai][bj][m][1] * scale;
;                     u32x2 w; w.x = pk4_fp8(v0[0], v0[1], v0[2], v0[3]); w.y = pk4_fp8(v1[0], v1[1], v1[2], v1[3]);
;                     *(u32x2*)(rowp + bj * HALF) = w; } }
	v_pk_mul_f32 v[34:35], v[34:35], s[14:15] op_sel_hi:[1,0]
	v_pk_mul_f32 v[36:37], v[36:37], s[14:15] op_sel_hi:[1,0]
	v_cvt_pk_fp8_f32 v59, v52, v53 op_sel:[0,0,1]
	v_mov_b32_e32 v52, v135
	v_cvt_pk_fp8_f32 v52, v46, v47
	v_mov_b32_e32 v53, v135
	v_cvt_pk_fp8_f32 v53, v42, v43
	v_pk_mul_f32 v[42:43], v[48:49], s[14:15] op_sel_hi:[1,0]
	v_pk_mul_f32 v[30:31], v[30:31], s[14:15] op_sel_hi:[1,0]
	v_cvt_pk_fp8_f32 v52, v42, v43 op_sel:[0,0,1]
	v_mov_b32_e32 v43, v135
	v_cvt_pk_fp8_f32 v43, v34, v35
	v_add_u32_e32 v138, v161, v137
	v_pk_mul_f32 v[102:103], v[102:103], s[14:15] op_sel_hi:[1,0]
	v_mov_b32_e32 v106, v135
	v_cvt_pk_fp8_f32 v43, v36, v37 op_sel:[0,0,1]
	v_mov_b32_e32 v36, v135
	v_cvt_pk_fp8_f32 v36, v30, v31
	v_pk_mul_f32 v[26:27], v[26:27], s[14:15] op_sel_hi:[1,0]
	v_mov_b32_e32 v37, v135
	v_readlane_b32 s29, v254, 39
	v_ashrrev_i32_e32 v139, 31, v138
	v_pk_mul_f32 v[110:111], v[110:111], s[14:15] op_sel_hi:[1,0]
	v_mov_b32_e32 v123, v135
	v_cvt_pk_fp8_f32 v106, v102, v103
	v_cvt_pk_fp8_f32 v37, v26, v27
	v_pk_mul_f32 v[26:27], v[32:33], s[14:15] op_sel_hi:[1,0]
	v_lshl_or_b32 v140, s29, 8, v152
	v_lshlrev_b64 v[138:139], 11, v[138:139]
	v_cvt_pk_fp8_f32 v123, v110, v111
	v_pk_mul_f32 v[110:111], v[120:121], s[14:15] op_sel_hi:[1,0]
	v_pk_mul_f32 v[86:87], v[86:87], s[14:15] op_sel_hi:[1,0]
	v_mov_b32_e32 v90, v135
	v_cvt_pk_fp8_f32 v36, v26, v27 op_sel:[0,0,1]
	v_pk_mul_f32 v[18:19], v[18:19], s[14:15] op_sel_hi:[1,0]
	v_mov_b32_e32 v27, v135
	v_ashrrev_i32_e32 v141, 31, v140
	v_cvt_pk_fp8_f32 v122, v110, v111 op_sel:[0,0,1]
	v_lshl_add_u64 v[110:111], s[6:7], 0, v[138:139]
	v_cvt_pk_fp8_f32 v90, v86, v87
	v_cvt_pk_fp8_f32 v27, v18, v19
	v_lshl_add_u64 v[110:111], v[110:111], 0, v[140:141]
	v_pk_mul_f32 v[94:95], v[104:105], s[14:15] op_sel_hi:[1,0]
	v_pk_mul_f32 v[70:71], v[70:71], s[14:15] op_sel_hi:[1,0]
	v_mov_b32_e32 v74, v135
	v_cvt_pk_fp8_f32 v106, v94, v95 op_sel:[0,0,1]
	v_add_co_u32_e32 v94, vcc, s58, v110
	v_cvt_pk_fp8_f32 v74, v70, v71
	s_nop 0
	v_addc_co_u32_e32 v95, vcc, 0, v111, vcc
	v_pk_mul_f32 v[78:79], v[88:89], s[14:15] op_sel_hi:[1,0]
	v_pk_mul_f32 v[54:55], v[54:55], s[14:15] op_sel_hi:[1,0]
	v_mov_b32_e32 v58, v135
	v_pk_mul_f32 v[20:21], v[20:21], s[14:15] op_sel_hi:[1,0]
	v_cvt_pk_fp8_f32 v90, v78, v79 op_sel:[0,0,1]
	v_add_co_u32_e32 v78, vcc, s54, v110
	v_cvt_pk_fp8_f32 v58, v54, v55
	v_cvt_pk_fp8_f32 v27, v20, v21 op_sel:[0,0,1]
	v_pk_mul_f32 v[14:15], v[14:15], s[14:15] op_sel_hi:[1,0]
	v_mov_b32_e32 v20, v135
	v_addc_co_u32_e32 v79, vcc, 0, v111, vcc
	v_pk_mul_f32 v[66:67], v[72:73], s[14:15] op_sel_hi:[1,0]
	v_pk_mul_f32 v[38:39], v[38:39], s[14:15] op_sel_hi:[1,0]
	v_mov_b32_e32 v42, v135
	v_cvt_pk_fp8_f32 v20, v14, v15
	v_cvt_pk_fp8_f32 v74, v66, v67 op_sel:[0,0,1]
	v_add_co_u32_e32 v66, vcc, s57, v110
	v_cvt_pk_fp8_f32 v42, v38, v39
	s_nop 0
	v_addc_co_u32_e32 v67, vcc, 0, v111, vcc
	v_pk_mul_f32 v[50:51], v[56:57], s[14:15] op_sel_hi:[1,0]
	v_pk_mul_f32 v[22:23], v[22:23], s[14:15] op_sel_hi:[1,0]
	v_mov_b32_e32 v26, v135
	v_pk_mul_f32 v[10:11], v[10:11], s[14:15] op_sel_hi:[1,0]
	v_mov_b32_e32 v21, v135
	v_cvt_pk_fp8_f32 v58, v50, v51 op_sel:[0,0,1]
	v_add_co_u32_e32 v50, vcc, s61, v110
	v_cvt_pk_fp8_f32 v26, v22, v23
	v_cvt_pk_fp8_f32 v21, v10, v11
	v_pk_mul_f32 v[10:11], v[16:17], s[14:15] op_sel_hi:[1,0]
	v_addc_co_u32_e32 v51, vcc, 0, v111, vcc
	v_pk_mul_f32 v[34:35], v[40:41], s[14:15] op_sel_hi:[1,0]
	v_cvt_pk_fp8_f32 v20, v10, v11 op_sel:[0,0,1]
	v_pk_mul_f32 v[6:7], v[6:7], s[14:15] op_sel_hi:[1,0]
	v_pk_mul_f32 v[2:3], v[2:3], s[14:15] op_sel_hi:[1,0]
	v_mov_b32_e32 v10, v135
	v_mov_b32_e32 v11, v135
	v_cvt_pk_fp8_f32 v42, v34, v35 op_sel:[0,0,1]
	v_add_co_u32_e32 v34, vcc, s62, v110
	v_cvt_pk_fp8_f32 v10, v6, v7
	v_cvt_pk_fp8_f32 v11, v2, v3
	v_addc_co_u32_e32 v35, vcc, 0, v111, vcc
	v_pk_mul_f32 v[18:19], v[24:25], s[14:15] op_sel_hi:[1,0]
	v_pk_mul_f32 v[124:125], v[124:125], s[14:15] op_sel_hi:[1,0]
	v_pk_mul_f32 v[108:109], v[108:109], s[14:15] op_sel_hi:[1,0]
	v_pk_mul_f32 v[92:93], v[92:93], s[14:15] op_sel_hi:[1,0]
	v_pk_mul_f32 v[76:77], v[76:77], s[14:15] op_sel_hi:[1,0]
	v_pk_mul_f32 v[60:61], v[60:61], s[14:15] op_sel_hi:[1,0]
	v_pk_mul_f32 v[44:45], v[44:45], s[14:15] op_sel_hi:[1,0]
	v_pk_mul_f32 v[28:29], v[28:29], s[14:15] op_sel_hi:[1,0]
	v_cvt_pk_fp8_f32 v26, v18, v19 op_sel:[0,0,1]
	v_add_co_u32_e32 v18, vcc, s63, v110
	v_pk_mul_f32 v[12:13], v[12:13], s[14:15] op_sel_hi:[1,0]
	v_cvt_pk_fp8_f32 v143, v124, v125 op_sel:[0,0,1]
	v_pk_mul_f32 v[112:113], v[112:113], s[14:15] op_sel_hi:[1,0]
	v_cvt_pk_fp8_f32 v119, v108, v109 op_sel:[0,0,1]
	v_cvt_pk_fp8_f32 v99, v92, v93 op_sel:[0,0,1]
	v_cvt_pk_fp8_f32 v83, v76, v77 op_sel:[0,0,1]
	v_cvt_pk_fp8_f32 v69, v60, v61 op_sel:[0,0,1]
	v_cvt_pk_fp8_f32 v53, v44, v45 op_sel:[0,0,1]
	v_cvt_pk_fp8_f32 v37, v28, v29 op_sel:[0,0,1]
	v_addc_co_u32_e32 v19, vcc, 0, v111, vcc
	v_cvt_pk_fp8_f32 v21, v12, v13 op_sel:[0,0,1]
	v_pk_mul_f32 v[2:3], v[8:9], s[14:15] op_sel_hi:[1,0]
	v_pk_mul_f32 v[4:5], v[4:5], s[14:15] op_sel_hi:[1,0]
	v_cvt_pk_fp8_f32 v123, v112, v113 op_sel:[0,0,1]
	v_cvt_pk_fp8_f32 v10, v2, v3 op_sel:[0,0,1]
	v_cvt_pk_fp8_f32 v11, v4, v5 op_sel:[0,0,1]
	v_add_co_u32_e32 v2, vcc, s64, v110
	s_mov_b32 s29, s28
	s_nop 0
	v_addc_co_u32_e32 v3, vcc, 0, v111, vcc
	s_and_b64 vcc, exec, s[34:35]
	v_mov_b32_e32 v161, v156
	v_writelane_b32 v254, s29, 39
	v_mov_b32_e32 v162, v157
	v_mov_b32_e32 v136, v158
	v_mov_b32_e32 v138, v159
	v_mov_b32_e32 v140, v160
	s_mov_b64 s[38:39], s[36:37]
	global_store_dwordx2 v[110:111], v[142:143], off
	global_store_dwordx2 v[110:111], v[122:123], off offset:128
	v_lshl_add_u64 v[112:113], v[110:111], 0, s[16:17]
	global_store_dwordx2 v[94:95], v[118:119], off
	global_store_dwordx2 v[112:113], v[106:107], off offset:128
	v_lshl_add_u64 v[94:95], v[110:111], 0, s[18:19]
	global_store_dwordx2 v[78:79], v[98:99], off
	global_store_dwordx2 v[94:95], v[90:91], off offset:128
	v_lshl_add_u64 v[78:79], v[110:111], 0, s[20:21]
	global_store_dwordx2 v[66:67], v[82:83], off
	global_store_dwordx2 v[78:79], v[74:75], off offset:128
	v_lshl_add_u64 v[66:67], v[110:111], 0, s[10:11]
	global_store_dwordx2 v[50:51], v[68:69], off
	global_store_dwordx2 v[66:67], v[58:59], off offset:128
	v_lshl_add_u64 v[50:51], v[110:111], 0, s[22:23]
	global_store_dwordx2 v[34:35], v[52:53], off
	global_store_dwordx2 v[50:51], v[42:43], off offset:128
	v_lshl_add_u64 v[34:35], v[110:111], 0, s[24:25]
	global_store_dwordx2 v[18:19], v[36:37], off
	global_store_dwordx2 v[34:35], v[26:27], off offset:128
	v_lshl_add_u64 v[18:19], v[110:111], 0, s[26:27]
	global_store_dwordx2 v[2:3], v[20:21], off
	global_store_dwordx2 v[18:19], v[10:11], off offset:128
	s_cbranch_vccz .LBB0_1893
	s_waitcnt vmcnt(0)
	s_cmpk_gt_u32 s33, 0xff
	s_cbranch_scc1 .LBB0_1902
	s_barrier
